# v44 + first K-iteration peeled with C=0 (no accumulator zeroing) in 5 more GEMM loops (down, FoX in/out, NSA in p0, NSA out)
# speedup vs baseline: 1.0239x; 1.0239x over previous
; #define PG8_STAGE(bufoff, gbase, voff) do { _Pragma("unroll") for (int _i = 0; _i < 2; ++_i) \
;         __builtin_amdgcn_global_load_lds((const unsigned*)((const char*)(gbase) + (voff)[_i]), (PG8_LAS unsigned*)(lds + (bufoff) + ldsw + _i * 8192), 16, 0, 0); } while (0)
; #define PG8_LDA(dst, b, h) do { _Pragma("unroll") for (int m = 0; m < 4; ++m) _Pragma("unroll") for (int k = 0; k < 2; ++k) dst[m][k] = *(const PG8_LAS bf16x8*)(lds + PG8_SA(b, h) + aoff + m * 2048 + k * 1024); } while (0)
; #define PG8_LDB(dst, b, h) do { _Pragma("unroll") for (int n = 0; n < 2; ++n) _Pragma("unroll") for (int k = 0; k < 2; ++k) dst[n][k] = *(const PG8_LAS bf16x8*)(lds + PG8_SB(b, h) + boff + n * 2048 + k * 1024); } while (0)
; #define PG8_MMA(ai, bj, At, Bt) do { __builtin_amdgcn_s_setprio(1); _Pragma("unroll") for (int m = 0; m < 4; ++m) _Pragma("unroll") for (int n = 0; n < 2; ++n) _Pragma("unroll") for (int k = 0; k < 2; ++k) \
;         acc[ai][bj][m][n] = __builtin_amdgcn_mfma_f32_16x16x32_bf16(Bt[n][k], At[m][k], acc[ai][bj][m][n], 0, 0, 0); __builtin_amdgcn_s_setprio(0); } while (0)
; #define PG8_WAIT_V(n) asm volatile("s_waitcnt vmcnt(" #n ")" ::: "memory")
; #define PG8_WAIT_L(n) asm volatile("s_waitcnt lgkmcnt(" #n ")" ::: "memory")
; #define PG8_BAR __builtin_amdgcn_s_barrier()
; #define PG8_SCHED __builtin_amdgcn_sched_barrier(0)
; template <class Epi, class Sched, bool ALIGN_EPI = false, bool SP2 = false>
; __device__ __forceinline__ void gemm_phase(PG8_LAS unsigned char* lds, const Gemm g, const Sched& S, const Epi& E) {
;     ...
;             if constexpr (SP2) {
;             PG8_LDB(B0, 0, 0); PG8_LDB(B1, 0, 1); PG8_SCHED; PG8_LDA(At, 0, 0); PG8_STAGE(PG8_SA(1, 1), a1 + hstepA, voffA);
;             PG8_WAIT_V(8); PG8_WAIT_L(0); PG8_BAR; PG8_MMA(0, 0, At, B0); PG8_MMA(0, 1, At, B1); PG8_BAR; PG8_SCHED;
;             PG8_LDA(At, 0, 1); PG8_STAGE(PG8_SB(0, 0), b2, voffB); PG8_STAGE(PG8_SB(0, 1), b2 + hstepB, voffB); PG8_STAGE(PG8_SA(0, 0), a2, voffA);
;             PG8_WAIT_V(8); PG8_WAIT_L(0); PG8_BAR; PG8_MMA(1, 0, At, B0); PG8_MMA(1, 1, At, B1); PG8_BAR; PG8_SCHED;
.LBB0_668:
	s_add_u32 s44, s16, 0x100
	s_addc_u32 s45, s17, 0
	s_mov_b32 s46, -2
	s_add_u32 s16, s14, 0x100
	s_addc_u32 s17, s15, 0
	s_add_i32 s47, 0, 0x10000
	s_cmp_eq_u32 s46, 40
	s_cselect_b32 s21, s5, s17
	s_cselect_b32 s20, s4, s16
	v_add_u32_e32 v144, s47, v146
	s_cselect_b32 s19, s13, s45
	s_cselect_b32 s18, s12, s44
	s_add_i32 s48, 0, 0x14000
	ds_read_b128 v[150:153], v144
	ds_read_b128 v[154:157], v144 offset:1024
	ds_read_b128 v[158:161], v144 offset:2048
	ds_read_b128 v[162:165], v144 offset:3072
	v_add_u32_e32 v144, s48, v146
	ds_read_b128 v[166:169], v144
	ds_read_b128 v[170:173], v144 offset:1024
	ds_read_b128 v[174:177], v144 offset:2048
	ds_read_b128 v[178:181], v144 offset:3072
	v_lshl_add_u64 v[144:145], s[14:15], 0, v[142:143]
	s_add_i32 m0, s28, 0xc000
	ds_read_b128 v[182:185], v148
	ds_read_b128 v[186:189], v148 offset:1024
	ds_read_b128 v[190:193], v148 offset:2048
	ds_read_b128 v[194:197], v148 offset:3072
	ds_read_b128 v[210:213], v148 offset:4096
	ds_read_b128 v[226:229], v148 offset:5120
	ds_read_b128 v[230:233], v148 offset:6144
	ds_read_b128 v[234:237], v148 offset:7168
	v_lshl_add_u64 v[244:245], v[240:241], 0, s[64:65]
	s_mov_b32 m0, s33
	s_nop 0
	global_load_lds_dwordx4 v[244:245], off
	v_lshl_add_u64 v[244:245], v[242:243], 0, s[64:65]
	s_mov_b32 m0, s34
	s_nop 0
	global_load_lds_dwordx4 v[244:245], off
	s_add_i32 m0, s28, 0xc000
	s_nop 0
	global_load_lds_dwordx4 v[144:145], off
	v_lshl_add_u64 v[144:145], s[14:15], 0, v[140:141]
	s_add_i32 m0, s28, 0xe000
	s_nop 0
	global_load_lds_dwordx4 v[144:145], off
	s_waitcnt vmcnt(8)
	s_waitcnt lgkmcnt(0)
	s_barrier
	s_setprio 1
	s_waitcnt lgkmcnt(0)
	v_mfma_f32_16x16x32_bf16 v[128:131], v[150:153], v[182:185], 0
	v_mfma_f32_16x16x32_bf16 v[124:127], v[158:161], v[182:185], 0
	v_mfma_f32_16x16x32_bf16 v[120:123], v[150:153], v[190:193], 0
	v_mfma_f32_16x16x32_bf16 v[112:115], v[158:161], v[190:193], 0
	v_mfma_f32_16x16x32_bf16 v[104:107], v[150:153], v[210:213], 0
	v_mfma_f32_16x16x32_bf16 v[96:99], v[158:161], v[210:213], 0
	v_mfma_f32_16x16x32_bf16 v[88:91], v[150:153], v[230:233], 0
	v_mfma_f32_16x16x32_bf16 v[80:83], v[158:161], v[230:233], 0
	v_mfma_f32_16x16x32_bf16 v[128:131], v[154:157], v[186:189], v[128:131]
	v_mfma_f32_16x16x32_bf16 v[124:127], v[162:165], v[186:189], v[124:127]
	v_mfma_f32_16x16x32_bf16 v[120:123], v[154:157], v[194:197], v[120:123]
	v_mfma_f32_16x16x32_bf16 v[112:115], v[162:165], v[194:197], v[112:115]
	v_mfma_f32_16x16x32_bf16 v[104:107], v[154:157], v[226:229], v[104:107]
	v_mfma_f32_16x16x32_bf16 v[96:99], v[162:165], v[226:229], v[96:99]
	v_mfma_f32_16x16x32_bf16 v[88:91], v[154:157], v[234:237], v[88:91]
	v_mfma_f32_16x16x32_bf16 v[80:83], v[162:165], v[234:237], v[80:83]
	s_setprio 0
	s_setprio 1
	v_mfma_f32_16x16x32_bf16 v[116:119], v[166:169], v[182:185], 0
	v_mfma_f32_16x16x32_bf16 v[108:111], v[174:177], v[182:185], 0
	v_mfma_f32_16x16x32_bf16 v[100:103], v[166:169], v[190:193], 0
	v_mfma_f32_16x16x32_bf16 v[92:95], v[174:177], v[190:193], 0
	v_mfma_f32_16x16x32_bf16 v[84:87], v[166:169], v[210:213], 0
	v_mfma_f32_16x16x32_bf16 v[76:79], v[174:177], v[210:213], 0
	v_mfma_f32_16x16x32_bf16 v[72:75], v[166:169], v[230:233], 0
	v_mfma_f32_16x16x32_bf16 v[68:71], v[174:177], v[230:233], 0
	v_mfma_f32_16x16x32_bf16 v[116:119], v[170:173], v[186:189], v[116:119]
	v_mfma_f32_16x16x32_bf16 v[108:111], v[178:181], v[186:189], v[108:111]
	v_mfma_f32_16x16x32_bf16 v[100:103], v[170:173], v[194:197], v[100:103]
	v_mfma_f32_16x16x32_bf16 v[92:95], v[178:181], v[194:197], v[92:95]
	v_mfma_f32_16x16x32_bf16 v[84:87], v[170:173], v[226:229], v[84:87]
	v_mfma_f32_16x16x32_bf16 v[76:79], v[178:181], v[226:229], v[76:79]
	v_mfma_f32_16x16x32_bf16 v[72:75], v[170:173], v[234:237], v[72:75]
	v_mfma_f32_16x16x32_bf16 v[68:71], v[178:181], v[234:237], v[68:71]
	s_setprio 0
	s_barrier
	s_add_i32 s14, s47, s27
	v_lshl_add_u64 v[144:145], s[18:19], 0, v[134:135]
	s_mov_b32 m0, s14
	ds_read_b128 v[182:185], v148 offset:16384
	ds_read_b128 v[186:189], v148 offset:17408
	ds_read_b128 v[190:193], v148 offset:18432
	ds_read_b128 v[194:197], v148 offset:19456
	ds_read_b128 v[210:213], v148 offset:20480
	ds_read_b128 v[226:229], v148 offset:21504
	ds_read_b128 v[230:233], v148 offset:22528
	ds_read_b128 v[234:237], v148 offset:23552
	global_load_lds_dwordx4 v[144:145], off
	s_add_i32 m0, s14, 0x2000
	s_add_u32 s14, s18, 0xb0000
	v_lshl_add_u64 v[238:239], s[18:19], 0, v[138:139]
	s_addc_u32 s15, s19, 0
	s_add_i32 s47, s48, s27
	global_load_lds_dwordx4 v[238:239], off
	v_lshl_add_u64 v[240:241], s[14:15], 0, v[134:135]
	s_mov_b32 m0, s47
	v_lshl_add_u64 v[242:243], s[20:21], 0, v[136:137]
	global_load_lds_dwordx4 v[240:241], off
	v_lshl_add_u64 v[240:241], s[14:15], 0, v[138:139]
	s_add_i32 m0, s47, 0x2000
	s_nop 0
	global_load_lds_dwordx4 v[240:241], off
	v_lshl_add_u64 v[240:241], s[20:21], 0, v[132:133]
	s_waitcnt vmcnt(6)
	s_waitcnt lgkmcnt(0)
	s_barrier
; #define PG8_STAGE(bufoff, gbase, voff) do { _Pragma("unroll") for (int _i = 0; _i < 2; ++_i) \
;         __builtin_amdgcn_global_load_lds((const unsigned*)((const char*)(gbase) + (voff)[_i]), (PG8_LAS unsigned*)(lds + (bufoff) + ldsw + _i * 8192), 16, 0, 0); } while (0)
; #define PG8_LDA(dst, b, h) do { _Pragma("unroll") for (int m = 0; m < 4; ++m) _Pragma("unroll") for (int k = 0; k < 2; ++k) dst[m][k] = *(const PG8_LAS bf16x8*)(lds + PG8_SA(b, h) + aoff + m * 2048 + k * 1024); } while (0)
; #define PG8_LDB(dst, b, h) do { _Pragma("unroll") for (int n = 0; n < 2; ++n) _Pragma("unroll") for (int k = 0; k < 2; ++k) dst[n][k] = *(const PG8_LAS bf16x8*)(lds + PG8_SB(b, h) + boff + n * 2048 + k * 1024); } while (0)
; #define PG8_MMA(ai, bj, At, Bt) do { __builtin_amdgcn_s_setprio(1); _Pragma("unroll") for (int m = 0; m < 4; ++m) _Pragma("unroll") for (int n = 0; n < 2; ++n) _Pragma("unroll") for (int k = 0; k < 2; ++k) \
;         acc[ai][bj][m][n] = __builtin_amdgcn_mfma_f32_16x16x32_bf16(Bt[n][k], At[m][k], acc[ai][bj][m][n], 0, 0, 0); __builtin_amdgcn_s_setprio(0); } while (0)
; #define PG8_WAIT_V(n) asm volatile("s_waitcnt vmcnt(" #n ")" ::: "memory")
; #define PG8_WAIT_L(n) asm volatile("s_waitcnt lgkmcnt(" #n ")" ::: "memory")
; #define PG8_BAR __builtin_amdgcn_s_barrier()
; #define PG8_SCHED __builtin_amdgcn_sched_barrier(0)
; template <class Epi, class Sched, bool ALIGN_EPI = false, bool SP2 = false>
; __device__ __forceinline__ void gemm_phase(PG8_LAS unsigned char* lds, const Gemm g, const Sched& S, const Epi& E) {
;     ...
;             PG8_WAIT_V(8); PG8_WAIT_L(0); PG8_BAR; PG8_MMA(0, 0, At, B0); PG8_MMA(0, 1, At, B1); PG8_BAR; PG8_SCHED;
;             PG8_LDA(At, 0, 1); PG8_STAGE(PG8_SB(0, 0), b2, voffB); PG8_STAGE(PG8_SB(0, 1), b2 + hstepB, voffB); PG8_STAGE(PG8_SA(0, 0), a2, voffA);
;             PG8_WAIT_V(8); PG8_WAIT_L(0); PG8_BAR; PG8_MMA(1, 0, At, B0); PG8_MMA(1, 1, At, B1); PG8_BAR; PG8_SCHED;
;             PG8_LDB(B0, 1, 0); PG8_LDB(B1, 1, 1); PG8_SCHED; PG8_LDA(At, 1, 0); PG8_STAGE(PG8_SA(0, 1), a2 + hstepA, voffA);
;             PG8_WAIT_V(8); PG8_WAIT_L(0); PG8_BAR; PG8_MMA(0, 0, At, B0); PG8_MMA(0, 1, At, B1); PG8_BAR; PG8_SCHED;
	s_setprio 1
	s_waitcnt lgkmcnt(0)
	v_mfma_f32_16x16x32_bf16 v[64:67], v[150:153], v[182:185], 0
	v_mfma_f32_16x16x32_bf16 v[60:63], v[158:161], v[182:185], 0
	v_mfma_f32_16x16x32_bf16 v[56:59], v[150:153], v[190:193], 0
	v_mfma_f32_16x16x32_bf16 v[48:51], v[158:161], v[190:193], 0
	v_mfma_f32_16x16x32_bf16 v[40:43], v[150:153], v[210:213], 0
	v_mfma_f32_16x16x32_bf16 v[32:35], v[158:161], v[210:213], 0
	v_mfma_f32_16x16x32_bf16 v[24:27], v[150:153], v[230:233], 0
	v_mfma_f32_16x16x32_bf16 v[16:19], v[158:161], v[230:233], 0
	v_mfma_f32_16x16x32_bf16 v[64:67], v[154:157], v[186:189], v[64:67]
	v_mfma_f32_16x16x32_bf16 v[60:63], v[162:165], v[186:189], v[60:63]
	v_mfma_f32_16x16x32_bf16 v[56:59], v[154:157], v[194:197], v[56:59]
	v_mfma_f32_16x16x32_bf16 v[48:51], v[162:165], v[194:197], v[48:51]
	v_mfma_f32_16x16x32_bf16 v[40:43], v[154:157], v[226:229], v[40:43]
	v_mfma_f32_16x16x32_bf16 v[32:35], v[162:165], v[226:229], v[32:35]
	v_mfma_f32_16x16x32_bf16 v[24:27], v[154:157], v[234:237], v[24:27]
	v_mfma_f32_16x16x32_bf16 v[16:19], v[162:165], v[234:237], v[16:19]
	s_setprio 0
	s_setprio 1
	v_mfma_f32_16x16x32_bf16 v[52:55], v[166:169], v[182:185], 0
	v_mfma_f32_16x16x32_bf16 v[44:47], v[174:177], v[182:185], 0
	v_mfma_f32_16x16x32_bf16 v[36:39], v[166:169], v[190:193], 0
	v_mfma_f32_16x16x32_bf16 v[28:31], v[174:177], v[190:193], 0
	v_mfma_f32_16x16x32_bf16 v[20:23], v[166:169], v[210:213], 0
	v_mfma_f32_16x16x32_bf16 v[12:15], v[174:177], v[210:213], 0
	v_mfma_f32_16x16x32_bf16 v[8:11], v[166:169], v[230:233], 0
	v_mfma_f32_16x16x32_bf16 v[4:7], v[174:177], v[230:233], 0
	v_mfma_f32_16x16x32_bf16 v[52:55], v[170:173], v[186:189], v[52:55]
	v_mfma_f32_16x16x32_bf16 v[44:47], v[178:181], v[186:189], v[44:47]
	v_mfma_f32_16x16x32_bf16 v[36:39], v[170:173], v[194:197], v[36:39]
	v_mfma_f32_16x16x32_bf16 v[28:31], v[178:181], v[194:197], v[28:31]
	v_mfma_f32_16x16x32_bf16 v[20:23], v[170:173], v[226:229], v[20:23]
	v_mfma_f32_16x16x32_bf16 v[12:15], v[178:181], v[226:229], v[12:15]
	v_mfma_f32_16x16x32_bf16 v[8:11], v[170:173], v[234:237], v[8:11]
	v_mfma_f32_16x16x32_bf16 v[4:7], v[178:181], v[234:237], v[4:7]
	s_setprio 0
	s_barrier
	s_add_i32 s47, 0, 0x18000
	v_add_u32_e32 v149, s47, v146
	s_add_i32 s48, 0, 0x1c000
	ds_read_b128 v[150:153], v149
	ds_read_b128 v[154:157], v149 offset:1024
	ds_read_b128 v[158:161], v149 offset:2048
	ds_read_b128 v[162:165], v149 offset:3072
	v_add_u32_e32 v149, s48, v146
	ds_read_b128 v[166:169], v149
	ds_read_b128 v[170:173], v149 offset:1024
	ds_read_b128 v[174:177], v149 offset:2048
	ds_read_b128 v[178:181], v149 offset:3072
	s_add_u32 s14, s20, 0xb0000
	s_addc_u32 s15, s21, 0
	s_mov_b32 m0, s30
	v_lshl_add_u64 v[244:245], s[14:15], 0, v[132:133]
	ds_read_b128 v[182:185], v148 offset:32768
	ds_read_b128 v[186:189], v148 offset:33792
	ds_read_b128 v[190:193], v148 offset:34816
	ds_read_b128 v[194:197], v148 offset:35840
	ds_read_b128 v[210:213], v148 offset:36864
	ds_read_b128 v[226:229], v148 offset:37888
	ds_read_b128 v[230:233], v148 offset:38912
	ds_read_b128 v[234:237], v148 offset:39936
	s_mov_b32 m0, s28
	s_nop 0
	global_load_lds_dwordx4 v[240:241], off
	s_mov_b32 m0, s29
	s_nop 0
	global_load_lds_dwordx4 v[242:243], off
	s_mov_b32 m0, s30
	s_nop 0
	global_load_lds_dwordx4 v[244:245], off
	v_lshl_add_u64 v[244:245], s[14:15], 0, v[136:137]
	s_mov_b32 m0, s31
	s_nop 0
	global_load_lds_dwordx4 v[244:245], off
	s_waitcnt vmcnt(8)
	s_waitcnt lgkmcnt(0)
	s_barrier
	s_setprio 1
	s_waitcnt lgkmcnt(0)
	v_mfma_f32_16x16x32_bf16 v[128:131], v[150:153], v[182:185], v[128:131]
	v_mfma_f32_16x16x32_bf16 v[124:127], v[158:161], v[182:185], v[124:127]
	v_mfma_f32_16x16x32_bf16 v[120:123], v[150:153], v[190:193], v[120:123]
	v_mfma_f32_16x16x32_bf16 v[112:115], v[158:161], v[190:193], v[112:115]
	v_mfma_f32_16x16x32_bf16 v[104:107], v[150:153], v[210:213], v[104:107]
	v_mfma_f32_16x16x32_bf16 v[96:99], v[158:161], v[210:213], v[96:99]
	v_mfma_f32_16x16x32_bf16 v[88:91], v[150:153], v[230:233], v[88:91]
	v_mfma_f32_16x16x32_bf16 v[80:83], v[158:161], v[230:233], v[80:83]
	v_mfma_f32_16x16x32_bf16 v[128:131], v[154:157], v[186:189], v[128:131]
	v_mfma_f32_16x16x32_bf16 v[124:127], v[162:165], v[186:189], v[124:127]
	v_mfma_f32_16x16x32_bf16 v[120:123], v[154:157], v[194:197], v[120:123]
	v_mfma_f32_16x16x32_bf16 v[112:115], v[162:165], v[194:197], v[112:115]
	v_mfma_f32_16x16x32_bf16 v[104:107], v[154:157], v[226:229], v[104:107]
	v_mfma_f32_16x16x32_bf16 v[96:99], v[162:165], v[226:229], v[96:99]
	v_mfma_f32_16x16x32_bf16 v[88:91], v[154:157], v[234:237], v[88:91]
	v_mfma_f32_16x16x32_bf16 v[80:83], v[162:165], v[234:237], v[80:83]
	s_setprio 0
	s_setprio 1
	v_mfma_f32_16x16x32_bf16 v[116:119], v[166:169], v[182:185], v[116:119]
	v_mfma_f32_16x16x32_bf16 v[108:111], v[174:177], v[182:185], v[108:111]
	v_mfma_f32_16x16x32_bf16 v[100:103], v[166:169], v[190:193], v[100:103]
	v_mfma_f32_16x16x32_bf16 v[92:95], v[174:177], v[190:193], v[92:95]
	v_mfma_f32_16x16x32_bf16 v[84:87], v[166:169], v[210:213], v[84:87]
	v_mfma_f32_16x16x32_bf16 v[76:79], v[174:177], v[210:213], v[76:79]
	v_mfma_f32_16x16x32_bf16 v[72:75], v[166:169], v[230:233], v[72:75]
	v_mfma_f32_16x16x32_bf16 v[68:71], v[174:177], v[230:233], v[68:71]
	v_mfma_f32_16x16x32_bf16 v[116:119], v[170:173], v[186:189], v[116:119]
	v_mfma_f32_16x16x32_bf16 v[108:111], v[178:181], v[186:189], v[108:111]
	v_mfma_f32_16x16x32_bf16 v[100:103], v[170:173], v[194:197], v[100:103]
	v_mfma_f32_16x16x32_bf16 v[92:95], v[178:181], v[194:197], v[92:95]
	v_mfma_f32_16x16x32_bf16 v[84:87], v[170:173], v[226:229], v[84:87]
	v_mfma_f32_16x16x32_bf16 v[76:79], v[178:181], v[226:229], v[76:79]
	v_mfma_f32_16x16x32_bf16 v[72:75], v[170:173], v[234:237], v[72:75]
	v_mfma_f32_16x16x32_bf16 v[68:71], v[178:181], v[234:237], v[68:71]
	s_setprio 0
	s_barrier
; #define PG8_STR(x) PG8_STR2(x)
; #define PG8_STAGE(bufoff, gbase, voff) do { _Pragma("unroll") for (int _i = 0; _i < 2; ++_i) \
;         __builtin_amdgcn_global_load_lds((const unsigned*)((const char*)(gbase) + (voff)[_i]), (PG8_LAS unsigned*)(lds + (bufoff) + ldsw + _i * 8192), 16, 0, 0); } while (0)
; #define PG8_LDA(dst, b, h) do { _Pragma("unroll") for (int m = 0; m < 4; ++m) _Pragma("unroll") for (int k = 0; k < 2; ++k) dst[m][k] = *(const PG8_LAS bf16x8*)(lds + PG8_SA(b, h) + aoff + m * 2048 + k * 1024); } while (0)
; #define PG8_WAIT_V(n) asm volatile("s_waitcnt vmcnt(" #n ")" ::: "memory")
; template <class Epi, class Sched, bool ALIGN_EPI = false, bool SP2 = false>
; __device__ __forceinline__ void gemm_phase(PG8_LAS unsigned char* lds, const Gemm g, const Sched& S, const Epi& E) {
;     ...
;         for (int t = 0; t < nt; t += 2) {
;     ...
;             asm volatile(".p2align 6\n\t.rept " PG8_STR(KLOOP_ALIGN) "\n\ts_nop 0\n\t.endr");
;     ...
;             const bool last = (t == nt - 2);
;             const char* a1 = cA + (size_t)(t + 1) * kstep;
;             const char* a2 = last ? nA : cA + (size_t)(t + 2) * kstep; const char* b2 = last ? nB : cB + (size_t)(t + 2) * kstep;
;             const char* a3 = a2 + kstep; const char* b3 = b2 + kstep;
;             if (last && has_next) S.a_ready(nxt);
;             if constexpr (SP2) {
;             PG8_LDB(B0, 0, 0); PG8_LDB(B1, 0, 1); PG8_SCHED; PG8_LDA(At, 0, 0); PG8_STAGE(PG8_SA(1, 1), a1 + hstepA, voffA);
;             PG8_WAIT_V(8); PG8_WAIT_L(0); PG8_BAR; PG8_MMA(0, 0, At, B0); PG8_MMA(0, 1, At, B1); PG8_BAR; PG8_SCHED;
;             PG8_LDA(At, 0, 1); PG8_STAGE(PG8_SB(0, 0), b2, voffB); PG8_STAGE(PG8_SB(0, 1), b2 + hstepB, voffB); PG8_STAGE(PG8_SA(0, 0), a2, voffA);
;             PG8_WAIT_V(8); PG8_WAIT_L(0); PG8_BAR; PG8_MMA(1, 0, At, B0); PG8_MMA(1, 1, At, B1); PG8_BAR; PG8_SCHED;
;             PG8_LDB(B0, 1, 0); PG8_LDB(B1, 1, 1); PG8_SCHED; PG8_LDA(At, 1, 0); PG8_STAGE(PG8_SA(0, 1), a2 + hstepA, voffA);
;             PG8_WAIT_V(8); PG8_WAIT_L(0); PG8_BAR; PG8_MMA(0, 0, At, B0); PG8_MMA(0, 1, At, B1); PG8_BAR; PG8_SCHED;
;             PG8_LDA(At, 1, 1); PG8_STAGE(PG8_SB(1, 0), b3, voffB); PG8_STAGE(PG8_SB(1, 1), b3 + hstepB, voffB); PG8_STAGE(PG8_SA(1, 0), a3, voffA);
;             PG8_WAIT_V(8); PG8_WAIT_L(0); PG8_BAR; PG8_MMA(1, 0, At, B0); PG8_MMA(1, 1, At, B1); PG8_BAR; PG8_SCHED;
	s_add_i32 s14, s47, s27
	v_lshl_add_u64 v[144:145], v[144:145], 0, s[64:65]
	s_mov_b32 m0, s14
	ds_read_b128 v[182:185], v148 offset:49152
	ds_read_b128 v[186:189], v148 offset:50176
	ds_read_b128 v[190:193], v148 offset:51200
	ds_read_b128 v[194:197], v148 offset:52224
	ds_read_b128 v[210:213], v148 offset:53248
	ds_read_b128 v[226:229], v148 offset:54272
	ds_read_b128 v[230:233], v148 offset:55296
	ds_read_b128 v[234:237], v148 offset:56320
	global_load_lds_dwordx4 v[144:145], off
	s_add_i32 m0, s14, 0x2000
	s_add_u32 s14, s18, 0xb0080
	v_lshl_add_u64 v[144:145], v[238:239], 0, s[64:65]
	s_addc_u32 s15, s19, 0
	s_add_i32 s18, s48, s27
	global_load_lds_dwordx4 v[144:145], off
	v_lshl_add_u64 v[144:145], s[14:15], 0, v[134:135]
	s_mov_b32 m0, s18
	s_nop 0
	global_load_lds_dwordx4 v[144:145], off
	v_lshl_add_u64 v[144:145], s[14:15], 0, v[138:139]
	s_add_i32 m0, s18, 0x2000
	s_nop 0
	global_load_lds_dwordx4 v[144:145], off
	s_waitcnt vmcnt(6)
	s_waitcnt lgkmcnt(0)
	s_barrier
	s_setprio 1
	s_waitcnt lgkmcnt(0)
	v_mfma_f32_16x16x32_bf16 v[64:67], v[150:153], v[182:185], v[64:67]
	v_mfma_f32_16x16x32_bf16 v[60:63], v[158:161], v[182:185], v[60:63]
	v_mfma_f32_16x16x32_bf16 v[56:59], v[150:153], v[190:193], v[56:59]
	v_mfma_f32_16x16x32_bf16 v[48:51], v[158:161], v[190:193], v[48:51]
	v_mfma_f32_16x16x32_bf16 v[40:43], v[150:153], v[210:213], v[40:43]
	v_mfma_f32_16x16x32_bf16 v[32:35], v[158:161], v[210:213], v[32:35]
	v_mfma_f32_16x16x32_bf16 v[24:27], v[150:153], v[230:233], v[24:27]
	v_mfma_f32_16x16x32_bf16 v[16:19], v[158:161], v[230:233], v[16:19]
	v_mfma_f32_16x16x32_bf16 v[64:67], v[154:157], v[186:189], v[64:67]
	v_mfma_f32_16x16x32_bf16 v[60:63], v[162:165], v[186:189], v[60:63]
	v_mfma_f32_16x16x32_bf16 v[56:59], v[154:157], v[194:197], v[56:59]
	v_mfma_f32_16x16x32_bf16 v[48:51], v[162:165], v[194:197], v[48:51]
	v_mfma_f32_16x16x32_bf16 v[40:43], v[154:157], v[226:229], v[40:43]
	v_mfma_f32_16x16x32_bf16 v[32:35], v[162:165], v[226:229], v[32:35]
	v_mfma_f32_16x16x32_bf16 v[24:27], v[154:157], v[234:237], v[24:27]
	v_mfma_f32_16x16x32_bf16 v[16:19], v[162:165], v[234:237], v[16:19]
	s_setprio 0
	s_setprio 1
	v_mfma_f32_16x16x32_bf16 v[52:55], v[166:169], v[182:185], v[52:55]
	v_mfma_f32_16x16x32_bf16 v[44:47], v[174:177], v[182:185], v[44:47]
	v_mfma_f32_16x16x32_bf16 v[36:39], v[166:169], v[190:193], v[36:39]
	v_mfma_f32_16x16x32_bf16 v[28:31], v[174:177], v[190:193], v[28:31]
	v_mfma_f32_16x16x32_bf16 v[20:23], v[166:169], v[210:213], v[20:23]
	v_mfma_f32_16x16x32_bf16 v[12:15], v[174:177], v[210:213], v[12:15]
	v_mfma_f32_16x16x32_bf16 v[8:11], v[166:169], v[230:233], v[8:11]
	v_mfma_f32_16x16x32_bf16 v[4:7], v[174:177], v[230:233], v[4:7]
	v_mfma_f32_16x16x32_bf16 v[52:55], v[170:173], v[186:189], v[52:55]
	v_mfma_f32_16x16x32_bf16 v[44:47], v[178:181], v[186:189], v[44:47]
	v_mfma_f32_16x16x32_bf16 v[36:39], v[170:173], v[194:197], v[36:39]
	v_mfma_f32_16x16x32_bf16 v[28:31], v[178:181], v[194:197], v[28:31]
	v_mfma_f32_16x16x32_bf16 v[20:23], v[170:173], v[226:229], v[20:23]
	v_mfma_f32_16x16x32_bf16 v[12:15], v[178:181], v[226:229], v[12:15]
	v_mfma_f32_16x16x32_bf16 v[8:11], v[170:173], v[234:237], v[8:11]
	v_mfma_f32_16x16x32_bf16 v[4:7], v[178:181], v[234:237], v[4:7]
	s_setprio 0
	s_barrier
	s_add_i32 s46, s46, 2
	s_add_u32 s44, s44, 0x100
	s_addc_u32 s45, s45, 0
	s_cmp_gt_u32 s46, 41
	s_mov_b64 s[14:15], s[16:17]
	s_cbranch_scc1 .Lpeel_exit_1
.LBB0_669:
	s_add_u32 s16, s14, 0x100
	s_addc_u32 s17, s15, 0
	s_add_i32 s47, 0, 0x10000
	s_cmp_eq_u32 s46, 40
	s_cselect_b32 s21, s5, s17
	s_cselect_b32 s20, s4, s16
	v_add_u32_e32 v144, s47, v146
	s_cselect_b32 s19, s13, s45
	s_cselect_b32 s18, s12, s44
	s_add_i32 s48, 0, 0x14000
	ds_read_b128 v[150:153], v144
	ds_read_b128 v[154:157], v144 offset:1024
	ds_read_b128 v[158:161], v144 offset:2048
	ds_read_b128 v[162:165], v144 offset:3072
	v_add_u32_e32 v144, s48, v146
	ds_read_b128 v[166:169], v144
	ds_read_b128 v[170:173], v144 offset:1024
	ds_read_b128 v[174:177], v144 offset:2048
	ds_read_b128 v[178:181], v144 offset:3072
	v_lshl_add_u64 v[144:145], s[14:15], 0, v[142:143]
	s_add_i32 m0, s28, 0xc000
	ds_read_b128 v[182:185], v148
	ds_read_b128 v[186:189], v148 offset:1024
	ds_read_b128 v[190:193], v148 offset:2048
	ds_read_b128 v[194:197], v148 offset:3072
	ds_read_b128 v[210:213], v148 offset:4096
	ds_read_b128 v[226:229], v148 offset:5120
	ds_read_b128 v[230:233], v148 offset:6144
	ds_read_b128 v[234:237], v148 offset:7168
	v_lshl_add_u64 v[244:245], v[240:241], 0, s[64:65]
	s_mov_b32 m0, s33
	s_nop 0
	global_load_lds_dwordx4 v[244:245], off
	v_lshl_add_u64 v[244:245], v[242:243], 0, s[64:65]
	s_mov_b32 m0, s34
	s_nop 0
	global_load_lds_dwordx4 v[244:245], off
	s_add_i32 m0, s28, 0xc000
	s_nop 0
	global_load_lds_dwordx4 v[144:145], off
	v_lshl_add_u64 v[144:145], s[14:15], 0, v[140:141]
	s_add_i32 m0, s28, 0xe000
	s_nop 0
	global_load_lds_dwordx4 v[144:145], off
	s_waitcnt vmcnt(8)
	s_waitcnt lgkmcnt(0)
	s_barrier
; #define PG8_STAGE(bufoff, gbase, voff) do { _Pragma("unroll") for (int _i = 0; _i < 2; ++_i) \
;         __builtin_amdgcn_global_load_lds((const unsigned*)((const char*)(gbase) + (voff)[_i]), (PG8_LAS unsigned*)(lds + (bufoff) + ldsw + _i * 8192), 16, 0, 0); } while (0)
; #define PG8_LDA(dst, b, h) do { _Pragma("unroll") for (int m = 0; m < 4; ++m) _Pragma("unroll") for (int k = 0; k < 2; ++k) dst[m][k] = *(const PG8_LAS bf16x8*)(lds + PG8_SA(b, h) + aoff + m * 2048 + k * 1024); } while (0)
; #define PG8_LDB(dst, b, h) do { _Pragma("unroll") for (int n = 0; n < 2; ++n) _Pragma("unroll") for (int k = 0; k < 2; ++k) dst[n][k] = *(const PG8_LAS bf16x8*)(lds + PG8_SB(b, h) + boff + n * 2048 + k * 1024); } while (0)
; #define PG8_MMA(ai, bj, At, Bt) do { __builtin_amdgcn_s_setprio(1); _Pragma("unroll") for (int m = 0; m < 4; ++m) _Pragma("unroll") for (int n = 0; n < 2; ++n) _Pragma("unroll") for (int k = 0; k < 2; ++k) \
;         acc[ai][bj][m][n] = __builtin_amdgcn_mfma_f32_16x16x32_bf16(Bt[n][k], At[m][k], acc[ai][bj][m][n], 0, 0, 0); __builtin_amdgcn_s_setprio(0); } while (0)
; #define PG8_WAIT_V(n) asm volatile("s_waitcnt vmcnt(" #n ")" ::: "memory")
; #define PG8_WAIT_L(n) asm volatile("s_waitcnt lgkmcnt(" #n ")" ::: "memory")
; #define PG8_BAR __builtin_amdgcn_s_barrier()
; #define PG8_SCHED __builtin_amdgcn_sched_barrier(0)
; template <class Epi, class Sched, bool ALIGN_EPI = false, bool SP2 = false>
; __device__ __forceinline__ void gemm_phase(PG8_LAS unsigned char* lds, const Gemm g, const Sched& S, const Epi& E) {
;     ...
;             PG8_LDB(B0, 0, 0); PG8_LDB(B1, 0, 1); PG8_SCHED; PG8_LDA(At, 0, 0); PG8_STAGE(PG8_SA(1, 1), a1 + hstepA, voffA);
;             PG8_WAIT_V(8); PG8_WAIT_L(0); PG8_BAR; PG8_MMA(0, 0, At, B0); PG8_MMA(0, 1, At, B1); PG8_BAR; PG8_SCHED;
;             PG8_LDA(At, 0, 1); PG8_STAGE(PG8_SB(0, 0), b2, voffB); PG8_STAGE(PG8_SB(0, 1), b2 + hstepB, voffB); PG8_STAGE(PG8_SA(0, 0), a2, voffA);
;             PG8_WAIT_V(8); PG8_WAIT_L(0); PG8_BAR; PG8_MMA(1, 0, At, B0); PG8_MMA(1, 1, At, B1); PG8_BAR; PG8_SCHED;
;             PG8_LDB(B0, 1, 0); PG8_LDB(B1, 1, 1); PG8_SCHED; PG8_LDA(At, 1, 0); PG8_STAGE(PG8_SA(0, 1), a2 + hstepA, voffA);
;             PG8_WAIT_V(8); PG8_WAIT_L(0); PG8_BAR; PG8_MMA(0, 0, At, B0); PG8_MMA(0, 1, At, B1); PG8_BAR; PG8_SCHED;
	s_setprio 1
	s_waitcnt lgkmcnt(0)
	v_mfma_f32_16x16x32_bf16 v[128:131], v[150:153], v[182:185], v[128:131]
	v_mfma_f32_16x16x32_bf16 v[124:127], v[158:161], v[182:185], v[124:127]
	v_mfma_f32_16x16x32_bf16 v[120:123], v[150:153], v[190:193], v[120:123]
	v_mfma_f32_16x16x32_bf16 v[112:115], v[158:161], v[190:193], v[112:115]
	v_mfma_f32_16x16x32_bf16 v[104:107], v[150:153], v[210:213], v[104:107]
	v_mfma_f32_16x16x32_bf16 v[96:99], v[158:161], v[210:213], v[96:99]
	v_mfma_f32_16x16x32_bf16 v[88:91], v[150:153], v[230:233], v[88:91]
	v_mfma_f32_16x16x32_bf16 v[80:83], v[158:161], v[230:233], v[80:83]
	v_mfma_f32_16x16x32_bf16 v[128:131], v[154:157], v[186:189], v[128:131]
	v_mfma_f32_16x16x32_bf16 v[124:127], v[162:165], v[186:189], v[124:127]
	v_mfma_f32_16x16x32_bf16 v[120:123], v[154:157], v[194:197], v[120:123]
	v_mfma_f32_16x16x32_bf16 v[112:115], v[162:165], v[194:197], v[112:115]
	v_mfma_f32_16x16x32_bf16 v[104:107], v[154:157], v[226:229], v[104:107]
	v_mfma_f32_16x16x32_bf16 v[96:99], v[162:165], v[226:229], v[96:99]
	v_mfma_f32_16x16x32_bf16 v[88:91], v[154:157], v[234:237], v[88:91]
	v_mfma_f32_16x16x32_bf16 v[80:83], v[162:165], v[234:237], v[80:83]
	s_setprio 0
	s_setprio 1
	v_mfma_f32_16x16x32_bf16 v[116:119], v[166:169], v[182:185], v[116:119]
	v_mfma_f32_16x16x32_bf16 v[108:111], v[174:177], v[182:185], v[108:111]
	v_mfma_f32_16x16x32_bf16 v[100:103], v[166:169], v[190:193], v[100:103]
	v_mfma_f32_16x16x32_bf16 v[92:95], v[174:177], v[190:193], v[92:95]
	v_mfma_f32_16x16x32_bf16 v[84:87], v[166:169], v[210:213], v[84:87]
	v_mfma_f32_16x16x32_bf16 v[76:79], v[174:177], v[210:213], v[76:79]
	v_mfma_f32_16x16x32_bf16 v[72:75], v[166:169], v[230:233], v[72:75]
	v_mfma_f32_16x16x32_bf16 v[68:71], v[174:177], v[230:233], v[68:71]
	v_mfma_f32_16x16x32_bf16 v[116:119], v[170:173], v[186:189], v[116:119]
	v_mfma_f32_16x16x32_bf16 v[108:111], v[178:181], v[186:189], v[108:111]
	v_mfma_f32_16x16x32_bf16 v[100:103], v[170:173], v[194:197], v[100:103]
	v_mfma_f32_16x16x32_bf16 v[92:95], v[178:181], v[194:197], v[92:95]
	v_mfma_f32_16x16x32_bf16 v[84:87], v[170:173], v[226:229], v[84:87]
	v_mfma_f32_16x16x32_bf16 v[76:79], v[178:181], v[226:229], v[76:79]
	v_mfma_f32_16x16x32_bf16 v[72:75], v[170:173], v[234:237], v[72:75]
	v_mfma_f32_16x16x32_bf16 v[68:71], v[178:181], v[234:237], v[68:71]
	s_setprio 0
	s_barrier
	s_add_i32 s14, s47, s27
	v_lshl_add_u64 v[144:145], s[18:19], 0, v[134:135]
	s_mov_b32 m0, s14
	ds_read_b128 v[182:185], v148 offset:16384
	ds_read_b128 v[186:189], v148 offset:17408
	ds_read_b128 v[190:193], v148 offset:18432
	ds_read_b128 v[194:197], v148 offset:19456
	ds_read_b128 v[210:213], v148 offset:20480
	ds_read_b128 v[226:229], v148 offset:21504
	ds_read_b128 v[230:233], v148 offset:22528
	ds_read_b128 v[234:237], v148 offset:23552
	global_load_lds_dwordx4 v[144:145], off
	s_add_i32 m0, s14, 0x2000
	s_add_u32 s14, s18, 0xb0000
	v_lshl_add_u64 v[238:239], s[18:19], 0, v[138:139]
	s_addc_u32 s15, s19, 0
	s_add_i32 s47, s48, s27
	global_load_lds_dwordx4 v[238:239], off
	v_lshl_add_u64 v[240:241], s[14:15], 0, v[134:135]
	s_mov_b32 m0, s47
	v_lshl_add_u64 v[242:243], s[20:21], 0, v[136:137]
	global_load_lds_dwordx4 v[240:241], off
	v_lshl_add_u64 v[240:241], s[14:15], 0, v[138:139]
	s_add_i32 m0, s47, 0x2000
	s_nop 0
	global_load_lds_dwordx4 v[240:241], off
	v_lshl_add_u64 v[240:241], s[20:21], 0, v[132:133]
	s_waitcnt vmcnt(6)
	s_waitcnt lgkmcnt(0)
	s_barrier
	s_setprio 1
	s_waitcnt lgkmcnt(0)
	v_mfma_f32_16x16x32_bf16 v[64:67], v[150:153], v[182:185], v[64:67]
	v_mfma_f32_16x16x32_bf16 v[60:63], v[158:161], v[182:185], v[60:63]
	v_mfma_f32_16x16x32_bf16 v[56:59], v[150:153], v[190:193], v[56:59]
	v_mfma_f32_16x16x32_bf16 v[48:51], v[158:161], v[190:193], v[48:51]
	v_mfma_f32_16x16x32_bf16 v[40:43], v[150:153], v[210:213], v[40:43]
	v_mfma_f32_16x16x32_bf16 v[32:35], v[158:161], v[210:213], v[32:35]
	v_mfma_f32_16x16x32_bf16 v[24:27], v[150:153], v[230:233], v[24:27]
	v_mfma_f32_16x16x32_bf16 v[16:19], v[158:161], v[230:233], v[16:19]
	v_mfma_f32_16x16x32_bf16 v[64:67], v[154:157], v[186:189], v[64:67]
	v_mfma_f32_16x16x32_bf16 v[60:63], v[162:165], v[186:189], v[60:63]
	v_mfma_f32_16x16x32_bf16 v[56:59], v[154:157], v[194:197], v[56:59]
	v_mfma_f32_16x16x32_bf16 v[48:51], v[162:165], v[194:197], v[48:51]
	v_mfma_f32_16x16x32_bf16 v[40:43], v[154:157], v[226:229], v[40:43]
	v_mfma_f32_16x16x32_bf16 v[32:35], v[162:165], v[226:229], v[32:35]
	v_mfma_f32_16x16x32_bf16 v[24:27], v[154:157], v[234:237], v[24:27]
	v_mfma_f32_16x16x32_bf16 v[16:19], v[162:165], v[234:237], v[16:19]
	s_setprio 0
	s_setprio 1
	v_mfma_f32_16x16x32_bf16 v[52:55], v[166:169], v[182:185], v[52:55]
	v_mfma_f32_16x16x32_bf16 v[44:47], v[174:177], v[182:185], v[44:47]
	v_mfma_f32_16x16x32_bf16 v[36:39], v[166:169], v[190:193], v[36:39]
	v_mfma_f32_16x16x32_bf16 v[28:31], v[174:177], v[190:193], v[28:31]
	v_mfma_f32_16x16x32_bf16 v[20:23], v[166:169], v[210:213], v[20:23]
	v_mfma_f32_16x16x32_bf16 v[12:15], v[174:177], v[210:213], v[12:15]
	v_mfma_f32_16x16x32_bf16 v[8:11], v[166:169], v[230:233], v[8:11]
	v_mfma_f32_16x16x32_bf16 v[4:7], v[174:177], v[230:233], v[4:7]
	v_mfma_f32_16x16x32_bf16 v[52:55], v[170:173], v[186:189], v[52:55]
	v_mfma_f32_16x16x32_bf16 v[44:47], v[178:181], v[186:189], v[44:47]
	v_mfma_f32_16x16x32_bf16 v[36:39], v[170:173], v[194:197], v[36:39]
	v_mfma_f32_16x16x32_bf16 v[28:31], v[178:181], v[194:197], v[28:31]
	v_mfma_f32_16x16x32_bf16 v[20:23], v[170:173], v[226:229], v[20:23]
	v_mfma_f32_16x16x32_bf16 v[12:15], v[178:181], v[226:229], v[12:15]
	v_mfma_f32_16x16x32_bf16 v[8:11], v[170:173], v[234:237], v[8:11]
	v_mfma_f32_16x16x32_bf16 v[4:7], v[178:181], v[234:237], v[4:7]
	s_setprio 0
	s_barrier
; #define PG8_STAGE(bufoff, gbase, voff) do { _Pragma("unroll") for (int _i = 0; _i < 2; ++_i) \
;         __builtin_amdgcn_global_load_lds((const unsigned*)((const char*)(gbase) + (voff)[_i]), (PG8_LAS unsigned*)(lds + (bufoff) + ldsw + _i * 8192), 16, 0, 0); } while (0)
; #define PG8_LDA(dst, b, h) do { _Pragma("unroll") for (int m = 0; m < 4; ++m) _Pragma("unroll") for (int k = 0; k < 2; ++k) dst[m][k] = *(const PG8_LAS bf16x8*)(lds + PG8_SA(b, h) + aoff + m * 2048 + k * 1024); } while (0)
; #define PG8_LDB(dst, b, h) do { _Pragma("unroll") for (int n = 0; n < 2; ++n) _Pragma("unroll") for (int k = 0; k < 2; ++k) dst[n][k] = *(const PG8_LAS bf16x8*)(lds + PG8_SB(b, h) + boff + n * 2048 + k * 1024); } while (0)
; #define PG8_MMA(ai, bj, At, Bt) do { __builtin_amdgcn_s_setprio(1); _Pragma("unroll") for (int m = 0; m < 4; ++m) _Pragma("unroll") for (int n = 0; n < 2; ++n) _Pragma("unroll") for (int k = 0; k < 2; ++k) \
;         acc[ai][bj][m][n] = __builtin_amdgcn_mfma_f32_16x16x32_bf16(Bt[n][k], At[m][k], acc[ai][bj][m][n], 0, 0, 0); __builtin_amdgcn_s_setprio(0); } while (0)
; #define PG8_WAIT_V(n) asm volatile("s_waitcnt vmcnt(" #n ")" ::: "memory")
; #define PG8_WAIT_L(n) asm volatile("s_waitcnt lgkmcnt(" #n ")" ::: "memory")
; #define PG8_BAR __builtin_amdgcn_s_barrier()
; #define PG8_SCHED __builtin_amdgcn_sched_barrier(0)
; template <class Epi, class Sched, bool ALIGN_EPI = false, bool SP2 = false>
; __device__ __forceinline__ void gemm_phase(PG8_LAS unsigned char* lds, const Gemm g, const Sched& S, const Epi& E) {
;     ...
;             PG8_WAIT_V(8); PG8_WAIT_L(0); PG8_BAR; PG8_MMA(1, 0, At, B0); PG8_MMA(1, 1, At, B1); PG8_BAR; PG8_SCHED;
;             PG8_LDB(B0, 1, 0); PG8_LDB(B1, 1, 1); PG8_SCHED; PG8_LDA(At, 1, 0); PG8_STAGE(PG8_SA(0, 1), a2 + hstepA, voffA);
;             PG8_WAIT_V(8); PG8_WAIT_L(0); PG8_BAR; PG8_MMA(0, 0, At, B0); PG8_MMA(0, 1, At, B1); PG8_BAR; PG8_SCHED;
;             PG8_LDA(At, 1, 1); PG8_STAGE(PG8_SB(1, 0), b3, voffB); PG8_STAGE(PG8_SB(1, 1), b3 + hstepB, voffB); PG8_STAGE(PG8_SA(1, 0), a3, voffA);
;             PG8_WAIT_V(8); PG8_WAIT_L(0); PG8_BAR; PG8_MMA(1, 0, At, B0); PG8_MMA(1, 1, At, B1); PG8_BAR; PG8_SCHED;
	s_add_i32 s47, 0, 0x18000
	v_add_u32_e32 v149, s47, v146
	s_add_i32 s48, 0, 0x1c000
	ds_read_b128 v[150:153], v149
	ds_read_b128 v[154:157], v149 offset:1024
	ds_read_b128 v[158:161], v149 offset:2048
	ds_read_b128 v[162:165], v149 offset:3072
	v_add_u32_e32 v149, s48, v146
	ds_read_b128 v[166:169], v149
	ds_read_b128 v[170:173], v149 offset:1024
	ds_read_b128 v[174:177], v149 offset:2048
	ds_read_b128 v[178:181], v149 offset:3072
	s_add_u32 s14, s20, 0xb0000
	s_addc_u32 s15, s21, 0
	s_mov_b32 m0, s30
	v_lshl_add_u64 v[244:245], s[14:15], 0, v[132:133]
	ds_read_b128 v[182:185], v148 offset:32768
	ds_read_b128 v[186:189], v148 offset:33792
	ds_read_b128 v[190:193], v148 offset:34816
	ds_read_b128 v[194:197], v148 offset:35840
	ds_read_b128 v[210:213], v148 offset:36864
	ds_read_b128 v[226:229], v148 offset:37888
	ds_read_b128 v[230:233], v148 offset:38912
	ds_read_b128 v[234:237], v148 offset:39936
	s_mov_b32 m0, s28
	s_nop 0
	global_load_lds_dwordx4 v[240:241], off
	s_mov_b32 m0, s29
	s_nop 0
	global_load_lds_dwordx4 v[242:243], off
	s_mov_b32 m0, s30
	s_nop 0
	global_load_lds_dwordx4 v[244:245], off
	v_lshl_add_u64 v[244:245], s[14:15], 0, v[136:137]
	s_mov_b32 m0, s31
	s_nop 0
	global_load_lds_dwordx4 v[244:245], off
	s_waitcnt vmcnt(8)
	s_waitcnt lgkmcnt(0)
	s_barrier
	s_setprio 1
	s_waitcnt lgkmcnt(0)
	v_mfma_f32_16x16x32_bf16 v[128:131], v[150:153], v[182:185], v[128:131]
	v_mfma_f32_16x16x32_bf16 v[124:127], v[158:161], v[182:185], v[124:127]
	v_mfma_f32_16x16x32_bf16 v[120:123], v[150:153], v[190:193], v[120:123]
	v_mfma_f32_16x16x32_bf16 v[112:115], v[158:161], v[190:193], v[112:115]
	v_mfma_f32_16x16x32_bf16 v[104:107], v[150:153], v[210:213], v[104:107]
	v_mfma_f32_16x16x32_bf16 v[96:99], v[158:161], v[210:213], v[96:99]
	v_mfma_f32_16x16x32_bf16 v[88:91], v[150:153], v[230:233], v[88:91]
	v_mfma_f32_16x16x32_bf16 v[80:83], v[158:161], v[230:233], v[80:83]
	v_mfma_f32_16x16x32_bf16 v[128:131], v[154:157], v[186:189], v[128:131]
	v_mfma_f32_16x16x32_bf16 v[124:127], v[162:165], v[186:189], v[124:127]
	v_mfma_f32_16x16x32_bf16 v[120:123], v[154:157], v[194:197], v[120:123]
	v_mfma_f32_16x16x32_bf16 v[112:115], v[162:165], v[194:197], v[112:115]
	v_mfma_f32_16x16x32_bf16 v[104:107], v[154:157], v[226:229], v[104:107]
	v_mfma_f32_16x16x32_bf16 v[96:99], v[162:165], v[226:229], v[96:99]
	v_mfma_f32_16x16x32_bf16 v[88:91], v[154:157], v[234:237], v[88:91]
	v_mfma_f32_16x16x32_bf16 v[80:83], v[162:165], v[234:237], v[80:83]
	s_setprio 0
	s_setprio 1
	v_mfma_f32_16x16x32_bf16 v[116:119], v[166:169], v[182:185], v[116:119]
	v_mfma_f32_16x16x32_bf16 v[108:111], v[174:177], v[182:185], v[108:111]
	v_mfma_f32_16x16x32_bf16 v[100:103], v[166:169], v[190:193], v[100:103]
	v_mfma_f32_16x16x32_bf16 v[92:95], v[174:177], v[190:193], v[92:95]
	v_mfma_f32_16x16x32_bf16 v[84:87], v[166:169], v[210:213], v[84:87]
	v_mfma_f32_16x16x32_bf16 v[76:79], v[174:177], v[210:213], v[76:79]
	v_mfma_f32_16x16x32_bf16 v[72:75], v[166:169], v[230:233], v[72:75]
	v_mfma_f32_16x16x32_bf16 v[68:71], v[174:177], v[230:233], v[68:71]
	v_mfma_f32_16x16x32_bf16 v[116:119], v[170:173], v[186:189], v[116:119]
	v_mfma_f32_16x16x32_bf16 v[108:111], v[178:181], v[186:189], v[108:111]
	v_mfma_f32_16x16x32_bf16 v[100:103], v[170:173], v[194:197], v[100:103]
	v_mfma_f32_16x16x32_bf16 v[92:95], v[178:181], v[194:197], v[92:95]
	v_mfma_f32_16x16x32_bf16 v[84:87], v[170:173], v[226:229], v[84:87]
	v_mfma_f32_16x16x32_bf16 v[76:79], v[178:181], v[226:229], v[76:79]
	v_mfma_f32_16x16x32_bf16 v[72:75], v[170:173], v[234:237], v[72:75]
	v_mfma_f32_16x16x32_bf16 v[68:71], v[178:181], v[234:237], v[68:71]
	s_setprio 0
	s_barrier
	s_add_i32 s14, s47, s27
	v_lshl_add_u64 v[144:145], v[144:145], 0, s[64:65]
	s_mov_b32 m0, s14
	ds_read_b128 v[182:185], v148 offset:49152
	ds_read_b128 v[186:189], v148 offset:50176
	ds_read_b128 v[190:193], v148 offset:51200
	ds_read_b128 v[194:197], v148 offset:52224
	ds_read_b128 v[210:213], v148 offset:53248
	ds_read_b128 v[226:229], v148 offset:54272
	ds_read_b128 v[230:233], v148 offset:55296
	ds_read_b128 v[234:237], v148 offset:56320
	global_load_lds_dwordx4 v[144:145], off
	s_add_i32 m0, s14, 0x2000
	s_add_u32 s14, s18, 0xb0080
	v_lshl_add_u64 v[144:145], v[238:239], 0, s[64:65]
	s_addc_u32 s15, s19, 0
	s_add_i32 s18, s48, s27
	global_load_lds_dwordx4 v[144:145], off
	v_lshl_add_u64 v[144:145], s[14:15], 0, v[134:135]
	s_mov_b32 m0, s18
	s_nop 0
	global_load_lds_dwordx4 v[144:145], off
	v_lshl_add_u64 v[144:145], s[14:15], 0, v[138:139]
	s_add_i32 m0, s18, 0x2000
	s_nop 0
	global_load_lds_dwordx4 v[144:145], off
	s_waitcnt vmcnt(6)
	s_waitcnt lgkmcnt(0)
	s_barrier
; #define PG8_STAGE(bufoff, gbase, voff) do { _Pragma("unroll") for (int _i = 0; _i < 2; ++_i) \
;         __builtin_amdgcn_global_load_lds((const unsigned*)((const char*)(gbase) + (voff)[_i]), (PG8_LAS unsigned*)(lds + (bufoff) + ldsw + _i * 8192), 16, 0, 0); } while (0)
; #define PG8_LDA(dst, b, h) do { _Pragma("unroll") for (int m = 0; m < 4; ++m) _Pragma("unroll") for (int k = 0; k < 2; ++k) dst[m][k] = *(const PG8_LAS bf16x8*)(lds + PG8_SA(b, h) + aoff + m * 2048 + k * 1024); } while (0)
; #define PG8_MMA(ai, bj, At, Bt) do { __builtin_amdgcn_s_setprio(1); _Pragma("unroll") for (int m = 0; m < 4; ++m) _Pragma("unroll") for (int n = 0; n < 2; ++n) _Pragma("unroll") for (int k = 0; k < 2; ++k) \
;         acc[ai][bj][m][n] = __builtin_amdgcn_mfma_f32_16x16x32_bf16(Bt[n][k], At[m][k], acc[ai][bj][m][n], 0, 0, 0); __builtin_amdgcn_s_setprio(0); } while (0)
; #define PG8_WAIT_V(n) asm volatile("s_waitcnt vmcnt(" #n ")" ::: "memory")
; #define PG8_WAIT_L(n) asm volatile("s_waitcnt lgkmcnt(" #n ")" ::: "memory")
; #define PG8_BAR __builtin_amdgcn_s_barrier()
; #define PG8_SCHED __builtin_amdgcn_sched_barrier(0)
; template <class Epi, class Sched, bool ALIGN_EPI = false, bool SP2 = false>
; __device__ __forceinline__ void gemm_phase(PG8_LAS unsigned char* lds, const Gemm g, const Sched& S, const Epi& E) {
;     ...
;             PG8_WAIT_V(8); PG8_WAIT_L(0); PG8_BAR; PG8_MMA(0, 0, At, B0); PG8_MMA(0, 1, At, B1); PG8_BAR; PG8_SCHED;
;             PG8_LDA(At, 1, 1); PG8_STAGE(PG8_SB(1, 0), b3, voffB); PG8_STAGE(PG8_SB(1, 1), b3 + hstepB, voffB); PG8_STAGE(PG8_SA(1, 0), a3, voffA);
;             PG8_WAIT_V(8); PG8_WAIT_L(0); PG8_BAR; PG8_MMA(1, 0, At, B0); PG8_MMA(1, 1, At, B1); PG8_BAR; PG8_SCHED;
	s_setprio 1
	s_waitcnt lgkmcnt(0)
	v_mfma_f32_16x16x32_bf16 v[64:67], v[150:153], v[182:185], v[64:67]
	v_mfma_f32_16x16x32_bf16 v[60:63], v[158:161], v[182:185], v[60:63]
	v_mfma_f32_16x16x32_bf16 v[56:59], v[150:153], v[190:193], v[56:59]
	v_mfma_f32_16x16x32_bf16 v[48:51], v[158:161], v[190:193], v[48:51]
	v_mfma_f32_16x16x32_bf16 v[40:43], v[150:153], v[210:213], v[40:43]
	v_mfma_f32_16x16x32_bf16 v[32:35], v[158:161], v[210:213], v[32:35]
	v_mfma_f32_16x16x32_bf16 v[24:27], v[150:153], v[230:233], v[24:27]
	v_mfma_f32_16x16x32_bf16 v[16:19], v[158:161], v[230:233], v[16:19]
	v_mfma_f32_16x16x32_bf16 v[64:67], v[154:157], v[186:189], v[64:67]
	v_mfma_f32_16x16x32_bf16 v[60:63], v[162:165], v[186:189], v[60:63]
	v_mfma_f32_16x16x32_bf16 v[56:59], v[154:157], v[194:197], v[56:59]
	v_mfma_f32_16x16x32_bf16 v[48:51], v[162:165], v[194:197], v[48:51]
	v_mfma_f32_16x16x32_bf16 v[40:43], v[154:157], v[226:229], v[40:43]
	v_mfma_f32_16x16x32_bf16 v[32:35], v[162:165], v[226:229], v[32:35]
	v_mfma_f32_16x16x32_bf16 v[24:27], v[154:157], v[234:237], v[24:27]
	v_mfma_f32_16x16x32_bf16 v[16:19], v[162:165], v[234:237], v[16:19]
	s_setprio 0
	s_setprio 1
	v_mfma_f32_16x16x32_bf16 v[52:55], v[166:169], v[182:185], v[52:55]
	v_mfma_f32_16x16x32_bf16 v[44:47], v[174:177], v[182:185], v[44:47]
	v_mfma_f32_16x16x32_bf16 v[36:39], v[166:169], v[190:193], v[36:39]
	v_mfma_f32_16x16x32_bf16 v[28:31], v[174:177], v[190:193], v[28:31]
	v_mfma_f32_16x16x32_bf16 v[20:23], v[166:169], v[210:213], v[20:23]
	v_mfma_f32_16x16x32_bf16 v[12:15], v[174:177], v[210:213], v[12:15]
	v_mfma_f32_16x16x32_bf16 v[8:11], v[166:169], v[230:233], v[8:11]
	v_mfma_f32_16x16x32_bf16 v[4:7], v[174:177], v[230:233], v[4:7]
	v_mfma_f32_16x16x32_bf16 v[52:55], v[170:173], v[186:189], v[52:55]
	v_mfma_f32_16x16x32_bf16 v[44:47], v[178:181], v[186:189], v[44:47]
	v_mfma_f32_16x16x32_bf16 v[36:39], v[170:173], v[194:197], v[36:39]
	v_mfma_f32_16x16x32_bf16 v[28:31], v[178:181], v[194:197], v[28:31]
	v_mfma_f32_16x16x32_bf16 v[20:23], v[170:173], v[226:229], v[20:23]
	v_mfma_f32_16x16x32_bf16 v[12:15], v[178:181], v[226:229], v[12:15]
	v_mfma_f32_16x16x32_bf16 v[8:11], v[170:173], v[234:237], v[8:11]
	v_mfma_f32_16x16x32_bf16 v[4:7], v[178:181], v[234:237], v[4:7]
	s_setprio 0
	s_barrier
	s_add_i32 s46, s46, 2
	s_add_u32 s44, s44, 0x100
	s_addc_u32 s45, s45, 0
	s_cmp_gt_u32 s46, 41
	s_mov_b64 s[14:15], s[16:17]
	s_cbranch_scc0 .LBB0_669
.Lpeel_exit_1:
	s_and_b64 vcc, exec, s[10:11]
	s_cbranch_vccz .LBB0_672
	s_barrier
; __device__ __forceinline__ u32x4 pack8(const f32x4 a, const f32x4 b) { u32x4 w; w.x = cvt_pk_bf16(a[0], a[1]); w.y = cvt_pk_bf16(a[2], a[3]); w.z = cvt_pk_bf16(b[0], b[1]); w.w = cvt_pk_bf16(b[2], b[3]); return w; }
;     __device__ __forceinline__ void operator()(const f32x4 (&acc)[2][2][4][2], const Unit& u, int wr, int wc, int fr, int fq) const {
;         const int row0 = u.pm * BM + wr * 64 + fr, col0 = u.pn * BM + wc * 32 + 8 * fq;
; #pragma unroll
;         for (int ai = 0; ai < 2; ++ai)
; #pragma unroll
;             for (int m = 0; m < 4; ++m) {
;                 bf16_t* rowp = O + (size_t)(row0 + ai * HALF + m * 16) * ldc + col0;
; #pragma unroll
;                 for (int bj = 0; bj < 2; ++bj) *(u32x4*)(rowp + bj * HALF) = pack8(acc[ai][bj][m][0], acc[ai][bj][m][1]);
;             }
;     }
.LBB0_672:
	v_lshl_add_u32 v150, s42, 8, v2
	v_lshl_or_b32 v144, s43, 8, v147
	v_ashrrev_i32_e32 v151, 31, v150
	v_ashrrev_i32_e32 v145, 31, v144
	v_lshlrev_b64 v[152:153], 11, v[150:151]
	v_lshl_add_u64 v[152:153], s[8:9], 0, v[152:153]
	v_lshlrev_b64 v[154:155], 1, v[144:145]
	v_lshl_add_u64 v[144:145], v[152:153], 0, v[154:155]
	v_cvt_pk_bf16_f32 v128, v128, v129
	v_cvt_pk_bf16_f32 v129, v130, v131
	v_cvt_pk_bf16_f32 v130, v124, v125
	v_cvt_pk_bf16_f32 v131, v126, v127
	flat_store_dwordx4 v[144:145], v[128:131] sc1
	v_cvt_pk_bf16_f32 v116, v116, v117
	v_cvt_pk_bf16_f32 v117, v118, v119
	v_cvt_pk_bf16_f32 v118, v108, v109
	v_or_b32_e32 v108, 16, v150
	v_ashrrev_i32_e32 v109, 31, v108
	v_lshlrev_b64 v[108:109], 11, v[108:109]
	v_lshl_add_u64 v[108:109], s[8:9], 0, v[108:109]
	v_cvt_pk_bf16_f32 v119, v110, v111
	flat_store_dwordx4 v[144:145], v[116:119] offset:256 sc1
	s_mov_b64 s[14:15], 0x40000
	s_nop 0
	v_lshl_add_u64 v[116:117], v[108:109], 0, v[154:155]
	v_cvt_pk_bf16_f32 v108, v120, v121
	v_cvt_pk_bf16_f32 v109, v122, v123
	v_cvt_pk_bf16_f32 v110, v112, v113
	v_cvt_pk_bf16_f32 v111, v114, v115
	flat_store_dwordx4 v[116:117], v[108:111] sc1
	v_cvt_pk_bf16_f32 v100, v100, v101
	v_cvt_pk_bf16_f32 v101, v102, v103
	v_cvt_pk_bf16_f32 v102, v92, v93
	v_or_b32_e32 v92, 32, v150
	v_ashrrev_i32_e32 v93, 31, v92
	v_lshlrev_b64 v[92:93], 11, v[92:93]
	v_lshl_add_u64 v[92:93], s[8:9], 0, v[92:93]
	v_cvt_pk_bf16_f32 v103, v94, v95
	flat_store_dwordx4 v[116:117], v[100:103] offset:256 sc1
	s_nop 1
	v_lshl_add_u64 v[100:101], v[92:93], 0, v[154:155]
	v_cvt_pk_bf16_f32 v92, v104, v105
	v_cvt_pk_bf16_f32 v93, v106, v107
	v_cvt_pk_bf16_f32 v94, v96, v97
	v_cvt_pk_bf16_f32 v95, v98, v99
	flat_store_dwordx4 v[100:101], v[92:95] sc1
	v_cvt_pk_bf16_f32 v84, v84, v85
	v_cvt_pk_bf16_f32 v85, v86, v87
	v_cvt_pk_bf16_f32 v86, v76, v77
	v_or_b32_e32 v76, 48, v150
	v_ashrrev_i32_e32 v77, 31, v76
	v_lshlrev_b64 v[76:77], 11, v[76:77]
	v_lshl_add_u64 v[76:77], s[8:9], 0, v[76:77]
	v_cvt_pk_bf16_f32 v87, v78, v79
	flat_store_dwordx4 v[100:101], v[84:87] offset:256 sc1
	s_nop 1
	v_lshl_add_u64 v[84:85], v[76:77], 0, v[154:155]
	v_cvt_pk_bf16_f32 v76, v88, v89
	v_cvt_pk_bf16_f32 v77, v90, v91
	v_cvt_pk_bf16_f32 v78, v80, v81
	v_cvt_pk_bf16_f32 v79, v82, v83
	flat_store_dwordx4 v[84:85], v[76:79] sc1
	v_cvt_pk_bf16_f32 v72, v72, v73
	v_cvt_pk_bf16_f32 v73, v74, v75
	v_cvt_pk_bf16_f32 v74, v68, v69
	v_lshl_add_u64 v[68:69], v[144:145], 0, s[14:15]
	s_mov_b32 s14, 0x40000
	v_cvt_pk_bf16_f32 v75, v70, v71
	flat_store_dwordx4 v[84:85], v[72:75] offset:256 sc1
	v_cvt_pk_bf16_f32 v64, v64, v65
	v_cvt_pk_bf16_f32 v65, v66, v67
	v_cvt_pk_bf16_f32 v66, v60, v61
	v_add_co_u32_e32 v60, vcc, s14, v144
	v_cvt_pk_bf16_f32 v67, v62, v63
	s_mov_b64 s[14:15], 0x48000
	s_nop 0
	v_addc_co_u32_e32 v61, vcc, 0, v145, vcc
	flat_store_dwordx4 v[60:61], v[64:67] sc1
	v_cvt_pk_bf16_f32 v52, v52, v53
	v_cvt_pk_bf16_f32 v53, v54, v55
	v_cvt_pk_bf16_f32 v54, v44, v45
	v_cvt_pk_bf16_f32 v55, v46, v47
	flat_store_dwordx4 v[68:69], v[52:55] offset:256 sc1
	v_cvt_pk_bf16_f32 v44, v56, v57
	v_cvt_pk_bf16_f32 v45, v58, v59
	v_cvt_pk_bf16_f32 v46, v48, v49
	v_cvt_pk_bf16_f32 v47, v50, v51
	s_nop 1
	v_lshl_add_u64 v[52:53], v[144:145], 0, s[14:15]
	s_mov_b32 s14, 0x48000
	v_add_co_u32_e32 v48, vcc, s14, v144
	s_mov_b64 s[14:15], 0x50000
	s_nop 0
	v_addc_co_u32_e32 v49, vcc, 0, v145, vcc
	flat_store_dwordx4 v[48:49], v[44:47] sc1
	v_cvt_pk_bf16_f32 v36, v36, v37
	v_cvt_pk_bf16_f32 v37, v38, v39
	v_cvt_pk_bf16_f32 v38, v28, v29
	v_cvt_pk_bf16_f32 v39, v30, v31
	flat_store_dwordx4 v[52:53], v[36:39] offset:256 sc1
	v_cvt_pk_bf16_f32 v28, v40, v41
	v_cvt_pk_bf16_f32 v29, v42, v43
	v_cvt_pk_bf16_f32 v30, v32, v33
	v_cvt_pk_bf16_f32 v31, v34, v35
	s_nop 1
	v_lshl_add_u64 v[36:37], v[144:145], 0, s[14:15]
	s_mov_b32 s14, 0x50000
	v_add_co_u32_e32 v32, vcc, s14, v144
	s_mov_b64 s[14:15], 0x58000
	s_nop 0
	v_addc_co_u32_e32 v33, vcc, 0, v145, vcc
	flat_store_dwordx4 v[32:33], v[28:31] sc1
	v_cvt_pk_bf16_f32 v20, v20, v21
	v_cvt_pk_bf16_f32 v21, v22, v23
	v_cvt_pk_bf16_f32 v22, v12, v13
	v_cvt_pk_bf16_f32 v23, v14, v15
	flat_store_dwordx4 v[36:37], v[20:23] offset:256 sc1
	v_cvt_pk_bf16_f32 v12, v24, v25
	v_cvt_pk_bf16_f32 v13, v26, v27
	v_cvt_pk_bf16_f32 v14, v16, v17
	v_cvt_pk_bf16_f32 v15, v18, v19
	s_nop 1
	v_lshl_add_u64 v[20:21], v[144:145], 0, s[14:15]
	s_mov_b32 s14, 0x58000
	v_add_co_u32_e32 v16, vcc, s14, v144
	s_nop 1
	v_addc_co_u32_e32 v17, vcc, 0, v145, vcc
	s_and_b64 vcc, exec, s[2:3]
	s_mov_b64 s[2:3], -1
	flat_store_dwordx4 v[16:17], v[12:15] sc1
	v_cvt_pk_bf16_f32 v8, v8, v9
	v_cvt_pk_bf16_f32 v9, v10, v11
	v_cvt_pk_bf16_f32 v10, v4, v5
	v_cvt_pk_bf16_f32 v11, v6, v7
	flat_store_dwordx4 v[20:21], v[8:11] offset:256 sc1
	s_cbranch_vccnz .LBB0_657
	s_andn2_b64 vcc, exec, s[6:7]
	s_cbranch_vccnz .LBB0_656
	s_barrier
	s_branch .LBB0_656

; #define PG8_STR(x) PG8_STR2(x)
; #define PG8_STAGE(bufoff, gbase, voff) do { _Pragma("unroll") for (int _i = 0; _i < 2; ++_i) \
;         __builtin_amdgcn_global_load_lds((const unsigned*)((const char*)(gbase) + (voff)[_i]), (PG8_LAS unsigned*)(lds + (bufoff) + ldsw + _i * 8192), 16, 0, 0); } while (0)
; #define PG8_LDA(dst, b, h) do { _Pragma("unroll") for (int m = 0; m < 4; ++m) _Pragma("unroll") for (int k = 0; k < 2; ++k) dst[m][k] = *(const PG8_LAS bf16x8*)(lds + PG8_SA(b, h) + aoff + m * 2048 + k * 1024); } while (0)
; #define PG8_LDB(dst, b, h) do { _Pragma("unroll") for (int n = 0; n < 2; ++n) _Pragma("unroll") for (int k = 0; k < 2; ++k) dst[n][k] = *(const PG8_LAS bf16x8*)(lds + PG8_SB(b, h) + boff + n * 2048 + k * 1024); } while (0)
; #define PG8_MMA(ai, bj, At, Bt) do { __builtin_amdgcn_s_setprio(1); _Pragma("unroll") for (int m = 0; m < 4; ++m) _Pragma("unroll") for (int n = 0; n < 2; ++n) _Pragma("unroll") for (int k = 0; k < 2; ++k) \
;         acc[ai][bj][m][n] = __builtin_amdgcn_mfma_f32_16x16x32_bf16(Bt[n][k], At[m][k], acc[ai][bj][m][n], 0, 0, 0); __builtin_amdgcn_s_setprio(0); } while (0)
; template <class Epi, class Sched, bool ALIGN_EPI = false, bool SP2 = false>
; __device__ __forceinline__ void gemm_phase(PG8_LAS unsigned char* lds, const Gemm g, const Sched& S, const Epi& E) {
;     ...
;         for (int t = 0; t < nt; t += 2) {
;     ...
;             asm volatile(".p2align 6\n\t.rept " PG8_STR(KLOOP_ALIGN) "\n\ts_nop 0\n\t.endr");
;     ...
;             const bool last = (t == nt - 2);
;             const char* a1 = cA + (size_t)(t + 1) * kstep;
;             const char* a2 = last ? nA : cA + (size_t)(t + 2) * kstep; const char* b2 = last ? nB : cB + (size_t)(t + 2) * kstep;
;             const char* a3 = a2 + kstep; const char* b3 = b2 + kstep;
;             if (last && has_next) S.a_ready(nxt);
;             if constexpr (SP2) {
;             PG8_LDB(B0, 0, 0); PG8_LDB(B1, 0, 1); PG8_SCHED; PG8_LDA(At, 0, 0); PG8_STAGE(PG8_SA(1, 1), a1 + hstepA, voffA);
;             PG8_WAIT_V(8); PG8_WAIT_L(0); PG8_BAR; PG8_MMA(0, 0, At, B0); PG8_MMA(0, 1, At, B1); PG8_BAR; PG8_SCHED;
;             PG8_LDA(At, 0, 1); PG8_STAGE(PG8_SB(0, 0), b2, voffB); PG8_STAGE(PG8_SB(0, 1), b2 + hstepB, voffB); PG8_STAGE(PG8_SA(0, 0), a2, voffA);
;             PG8_WAIT_V(8); PG8_WAIT_L(0); PG8_BAR; PG8_MMA(1, 0, At, B0); PG8_MMA(1, 1, At, B1); PG8_BAR; PG8_SCHED;
.LBB0_815:
	s_ashr_i32 s19, s18, 31
	s_lshl_b64 s[20:21], s[18:19], 19
	s_add_u32 s20, s8, s20
	s_addc_u32 s21, s9, s21
	s_and_b64 s[22:23], s[6:7], exec
	s_cselect_b32 s19, s21, s29
	s_cselect_b32 s25, s20, s28
	s_ashr_i32 s17, s16, 31
	s_lshl_b64 s[22:23], s[16:17], 19
	s_add_u32 s22, s10, s22
	s_addc_u32 s23, s11, s23
	s_and_b64 s[30:31], s[6:7], exec
	s_cselect_b32 s17, s23, s27
	s_cselect_b32 s48, s22, s26
	s_add_u32 s49, s26, 0x100
	s_addc_u32 s50, s27, 0
	s_add_u32 s26, s28, 0x40080
	s_addc_u32 s27, s29, 0
	s_mov_b32 s51, -2
	s_add_u32 s28, s26, 0xfffc0080
	s_addc_u32 s29, s27, -1
	s_add_i32 s52, 0, 0x10000
	s_cmp_eq_u32 s51, 12
	s_cselect_b32 s31, s19, s29
	s_cselect_b32 s30, s25, s28
	v_add_u32_e32 v2, s52, v153
	s_cselect_b32 s29, s17, s50
	s_cselect_b32 s28, s48, s49
	s_add_i32 s54, 0, 0x14000
	ds_read_b128 v[148:151], v2
	ds_read_b128 v[156:159], v2 offset:1024
	ds_read_b128 v[160:163], v2 offset:2048
	ds_read_b128 v[164:167], v2 offset:3072
	v_add_u32_e32 v2, s54, v153
	ds_read_b128 v[168:171], v2
	ds_read_b128 v[172:175], v2 offset:1024
	ds_read_b128 v[176:179], v2 offset:2048
	ds_read_b128 v[180:183], v2 offset:3072
	v_lshl_add_u64 v[196:197], s[26:27], 0, v[144:145]
	s_add_i32 m0, s35, 0xc000
	ds_read_b128 v[184:187], v154
	ds_read_b128 v[188:191], v154 offset:1024
	ds_read_b128 v[192:195], v154 offset:2048
	ds_read_b128 v[210:213], v154 offset:3072
	ds_read_b128 v[226:229], v154 offset:4096
	ds_read_b128 v[230:233], v154 offset:5120
	ds_read_b128 v[234:237], v154 offset:6144
	ds_read_b128 v[238:241], v154 offset:7168
	v_lshl_add_u64 v[248:249], v[244:245], 0, s[64:65]
	s_mov_b32 m0, s43
	s_nop 0
	global_load_lds_dwordx4 v[248:249], off
	v_lshl_add_u64 v[248:249], v[246:247], 0, s[64:65]
	s_mov_b32 m0, s44
	s_nop 0
	global_load_lds_dwordx4 v[248:249], off
	s_add_i32 m0, s35, 0xc000
	s_nop 0
	global_load_lds_dwordx4 v[196:197], off
	v_lshl_add_u64 v[196:197], s[26:27], 0, v[142:143]
	s_add_i32 m0, s35, 0xe000
	s_nop 0
	global_load_lds_dwordx4 v[196:197], off
	s_waitcnt vmcnt(8)
	s_waitcnt lgkmcnt(0)
	s_barrier
	s_setprio 1
	s_waitcnt lgkmcnt(0)
	v_mfma_f32_16x16x32_bf16 v[128:131], v[148:151], v[184:187], 0
	v_mfma_f32_16x16x32_bf16 v[124:127], v[160:163], v[184:187], 0
	v_mfma_f32_16x16x32_bf16 v[116:119], v[148:151], v[192:195], 0
	v_mfma_f32_16x16x32_bf16 v[108:111], v[160:163], v[192:195], 0
	v_mfma_f32_16x16x32_bf16 v[100:103], v[148:151], v[226:229], 0
	v_mfma_f32_16x16x32_bf16 v[92:95], v[160:163], v[226:229], 0
	v_mfma_f32_16x16x32_bf16 v[84:87], v[148:151], v[234:237], 0
	v_mfma_f32_16x16x32_bf16 v[76:79], v[160:163], v[234:237], 0
	v_mfma_f32_16x16x32_bf16 v[128:131], v[156:159], v[188:191], v[128:131]
	v_mfma_f32_16x16x32_bf16 v[124:127], v[164:167], v[188:191], v[124:127]
	v_mfma_f32_16x16x32_bf16 v[116:119], v[156:159], v[210:213], v[116:119]
	v_mfma_f32_16x16x32_bf16 v[108:111], v[164:167], v[210:213], v[108:111]
	v_mfma_f32_16x16x32_bf16 v[100:103], v[156:159], v[230:233], v[100:103]
	v_mfma_f32_16x16x32_bf16 v[92:95], v[164:167], v[230:233], v[92:95]
	v_mfma_f32_16x16x32_bf16 v[84:87], v[156:159], v[238:241], v[84:87]
	v_mfma_f32_16x16x32_bf16 v[76:79], v[164:167], v[238:241], v[76:79]
	s_setprio 0
	s_setprio 1
	v_mfma_f32_16x16x32_bf16 v[120:123], v[168:171], v[184:187], 0
	v_mfma_f32_16x16x32_bf16 v[112:115], v[176:179], v[184:187], 0
	v_mfma_f32_16x16x32_bf16 v[104:107], v[168:171], v[192:195], 0
	v_mfma_f32_16x16x32_bf16 v[96:99], v[176:179], v[192:195], 0
	v_mfma_f32_16x16x32_bf16 v[88:91], v[168:171], v[226:229], 0
	v_mfma_f32_16x16x32_bf16 v[80:83], v[176:179], v[226:229], 0
	v_mfma_f32_16x16x32_bf16 v[72:75], v[168:171], v[234:237], 0
	v_mfma_f32_16x16x32_bf16 v[68:71], v[176:179], v[234:237], 0
	v_mfma_f32_16x16x32_bf16 v[120:123], v[172:175], v[188:191], v[120:123]
	v_mfma_f32_16x16x32_bf16 v[112:115], v[180:183], v[188:191], v[112:115]
	v_mfma_f32_16x16x32_bf16 v[104:107], v[172:175], v[210:213], v[104:107]
	v_mfma_f32_16x16x32_bf16 v[96:99], v[180:183], v[210:213], v[96:99]
	v_mfma_f32_16x16x32_bf16 v[88:91], v[172:175], v[230:233], v[88:91]
	v_mfma_f32_16x16x32_bf16 v[80:83], v[180:183], v[230:233], v[80:83]
	v_mfma_f32_16x16x32_bf16 v[72:75], v[172:175], v[238:241], v[72:75]
	v_mfma_f32_16x16x32_bf16 v[68:71], v[180:183], v[238:241], v[68:71]
	s_setprio 0
	s_barrier
	s_add_i32 s52, s52, s33
	v_lshl_add_u64 v[196:197], s[28:29], 0, v[136:137]
	s_mov_b32 m0, s52
	ds_read_b128 v[184:187], v154 offset:16384
	ds_read_b128 v[188:191], v154 offset:17408
	ds_read_b128 v[192:195], v154 offset:18432
	ds_read_b128 v[210:213], v154 offset:19456
	ds_read_b128 v[226:229], v154 offset:20480
	ds_read_b128 v[230:233], v154 offset:21504
	ds_read_b128 v[234:237], v154 offset:22528
	ds_read_b128 v[238:241], v154 offset:23552
	global_load_lds_dwordx4 v[196:197], off
	s_add_i32 m0, s52, 0x2000
	s_add_u32 s52, s28, 0x40000
	v_lshl_add_u64 v[242:243], s[28:29], 0, v[132:133]
	s_addc_u32 s53, s29, 0
	s_add_i32 s54, s54, s33
	global_load_lds_dwordx4 v[242:243], off
	v_lshl_add_u64 v[244:245], s[52:53], 0, v[136:137]
	s_mov_b32 m0, s54
	v_lshl_add_u64 v[246:247], s[30:31], 0, v[134:135]
	global_load_lds_dwordx4 v[244:245], off
	v_lshl_add_u64 v[244:245], s[52:53], 0, v[132:133]
	s_add_i32 m0, s54, 0x2000
	s_nop 0
	global_load_lds_dwordx4 v[244:245], off
	v_lshl_add_u64 v[244:245], s[30:31], 0, v[138:139]
	s_waitcnt vmcnt(6)
	s_waitcnt lgkmcnt(0)
	s_barrier
; #define PG8_STAGE(bufoff, gbase, voff) do { _Pragma("unroll") for (int _i = 0; _i < 2; ++_i) \
;         __builtin_amdgcn_global_load_lds((const unsigned*)((const char*)(gbase) + (voff)[_i]), (PG8_LAS unsigned*)(lds + (bufoff) + ldsw + _i * 8192), 16, 0, 0); } while (0)
; #define PG8_LDA(dst, b, h) do { _Pragma("unroll") for (int m = 0; m < 4; ++m) _Pragma("unroll") for (int k = 0; k < 2; ++k) dst[m][k] = *(const PG8_LAS bf16x8*)(lds + PG8_SA(b, h) + aoff + m * 2048 + k * 1024); } while (0)
; #define PG8_LDB(dst, b, h) do { _Pragma("unroll") for (int n = 0; n < 2; ++n) _Pragma("unroll") for (int k = 0; k < 2; ++k) dst[n][k] = *(const PG8_LAS bf16x8*)(lds + PG8_SB(b, h) + boff + n * 2048 + k * 1024); } while (0)
; #define PG8_MMA(ai, bj, At, Bt) do { __builtin_amdgcn_s_setprio(1); _Pragma("unroll") for (int m = 0; m < 4; ++m) _Pragma("unroll") for (int n = 0; n < 2; ++n) _Pragma("unroll") for (int k = 0; k < 2; ++k) \
;         acc[ai][bj][m][n] = __builtin_amdgcn_mfma_f32_16x16x32_bf16(Bt[n][k], At[m][k], acc[ai][bj][m][n], 0, 0, 0); __builtin_amdgcn_s_setprio(0); } while (0)
; #define PG8_WAIT_V(n) asm volatile("s_waitcnt vmcnt(" #n ")" ::: "memory")
; #define PG8_WAIT_L(n) asm volatile("s_waitcnt lgkmcnt(" #n ")" ::: "memory")
; #define PG8_BAR __builtin_amdgcn_s_barrier()
; #define PG8_SCHED __builtin_amdgcn_sched_barrier(0)
; template <class Epi, class Sched, bool ALIGN_EPI = false, bool SP2 = false>
; __device__ __forceinline__ void gemm_phase(PG8_LAS unsigned char* lds, const Gemm g, const Sched& S, const Epi& E) {
;     ...
;             PG8_WAIT_V(8); PG8_WAIT_L(0); PG8_BAR; PG8_MMA(0, 0, At, B0); PG8_MMA(0, 1, At, B1); PG8_BAR; PG8_SCHED;
;             PG8_LDA(At, 0, 1); PG8_STAGE(PG8_SB(0, 0), b2, voffB); PG8_STAGE(PG8_SB(0, 1), b2 + hstepB, voffB); PG8_STAGE(PG8_SA(0, 0), a2, voffA);
;             PG8_WAIT_V(8); PG8_WAIT_L(0); PG8_BAR; PG8_MMA(1, 0, At, B0); PG8_MMA(1, 1, At, B1); PG8_BAR; PG8_SCHED;
;             PG8_LDB(B0, 1, 0); PG8_LDB(B1, 1, 1); PG8_SCHED; PG8_LDA(At, 1, 0); PG8_STAGE(PG8_SA(0, 1), a2 + hstepA, voffA);
;             PG8_WAIT_V(8); PG8_WAIT_L(0); PG8_BAR; PG8_MMA(0, 0, At, B0); PG8_MMA(0, 1, At, B1); PG8_BAR; PG8_SCHED;
	s_setprio 1
	s_waitcnt lgkmcnt(0)
	v_mfma_f32_16x16x32_bf16 v[64:67], v[148:151], v[184:187], 0
	v_mfma_f32_16x16x32_bf16 v[60:63], v[160:163], v[184:187], 0
	v_mfma_f32_16x16x32_bf16 v[52:55], v[148:151], v[192:195], 0
	v_mfma_f32_16x16x32_bf16 v[44:47], v[160:163], v[192:195], 0
	v_mfma_f32_16x16x32_bf16 v[36:39], v[148:151], v[226:229], 0
	v_mfma_f32_16x16x32_bf16 v[28:31], v[160:163], v[226:229], 0
	v_mfma_f32_16x16x32_bf16 v[20:23], v[148:151], v[234:237], 0
	v_mfma_f32_16x16x32_bf16 v[12:15], v[160:163], v[234:237], 0
	v_mfma_f32_16x16x32_bf16 v[64:67], v[156:159], v[188:191], v[64:67]
	v_mfma_f32_16x16x32_bf16 v[60:63], v[164:167], v[188:191], v[60:63]
	v_mfma_f32_16x16x32_bf16 v[52:55], v[156:159], v[210:213], v[52:55]
	v_mfma_f32_16x16x32_bf16 v[44:47], v[164:167], v[210:213], v[44:47]
	v_mfma_f32_16x16x32_bf16 v[36:39], v[156:159], v[230:233], v[36:39]
	v_mfma_f32_16x16x32_bf16 v[28:31], v[164:167], v[230:233], v[28:31]
	v_mfma_f32_16x16x32_bf16 v[20:23], v[156:159], v[238:241], v[20:23]
	v_mfma_f32_16x16x32_bf16 v[12:15], v[164:167], v[238:241], v[12:15]
	s_setprio 0
	s_setprio 1
	v_mfma_f32_16x16x32_bf16 v[56:59], v[168:171], v[184:187], 0
	v_mfma_f32_16x16x32_bf16 v[48:51], v[176:179], v[184:187], 0
	v_mfma_f32_16x16x32_bf16 v[40:43], v[168:171], v[192:195], 0
	v_mfma_f32_16x16x32_bf16 v[32:35], v[176:179], v[192:195], 0
	v_mfma_f32_16x16x32_bf16 v[24:27], v[168:171], v[226:229], 0
	v_mfma_f32_16x16x32_bf16 v[16:19], v[176:179], v[226:229], 0
	v_mfma_f32_16x16x32_bf16 v[8:11], v[168:171], v[234:237], 0
	v_mfma_f32_16x16x32_bf16 v[4:7], v[176:179], v[234:237], 0
	v_mfma_f32_16x16x32_bf16 v[56:59], v[172:175], v[188:191], v[56:59]
	v_mfma_f32_16x16x32_bf16 v[48:51], v[180:183], v[188:191], v[48:51]
	v_mfma_f32_16x16x32_bf16 v[40:43], v[172:175], v[210:213], v[40:43]
	v_mfma_f32_16x16x32_bf16 v[32:35], v[180:183], v[210:213], v[32:35]
	v_mfma_f32_16x16x32_bf16 v[24:27], v[172:175], v[230:233], v[24:27]
	v_mfma_f32_16x16x32_bf16 v[16:19], v[180:183], v[230:233], v[16:19]
	v_mfma_f32_16x16x32_bf16 v[8:11], v[172:175], v[238:241], v[8:11]
	v_mfma_f32_16x16x32_bf16 v[4:7], v[180:183], v[238:241], v[4:7]
	s_setprio 0
	s_barrier
	s_add_i32 s52, 0, 0x18000
	v_add_u32_e32 v2, s52, v153
	s_add_i32 s53, 0, 0x1c000
	ds_read_b128 v[148:151], v2
	ds_read_b128 v[156:159], v2 offset:1024
	ds_read_b128 v[160:163], v2 offset:2048
	ds_read_b128 v[164:167], v2 offset:3072
	v_add_u32_e32 v2, s53, v153
	ds_read_b128 v[168:171], v2
	ds_read_b128 v[172:175], v2 offset:1024
	ds_read_b128 v[176:179], v2 offset:2048
	ds_read_b128 v[180:183], v2 offset:3072
	s_add_u32 s30, s30, 0x40000
	s_addc_u32 s31, s31, 0
	s_mov_b32 m0, s39
	v_lshl_add_u64 v[248:249], s[30:31], 0, v[138:139]
	ds_read_b128 v[184:187], v154 offset:32768
	ds_read_b128 v[188:191], v154 offset:33792
	ds_read_b128 v[192:195], v154 offset:34816
	ds_read_b128 v[210:213], v154 offset:35840
	ds_read_b128 v[226:229], v154 offset:36864
	ds_read_b128 v[230:233], v154 offset:37888
	ds_read_b128 v[234:237], v154 offset:38912
	ds_read_b128 v[238:241], v154 offset:39936
	s_mov_b32 m0, s35
	s_nop 0
	global_load_lds_dwordx4 v[244:245], off
	s_mov_b32 m0, s37
	s_nop 0
	global_load_lds_dwordx4 v[246:247], off
	s_mov_b32 m0, s39
	s_nop 0
	global_load_lds_dwordx4 v[248:249], off
	v_lshl_add_u64 v[248:249], s[30:31], 0, v[134:135]
	s_mov_b32 m0, s40
	s_nop 0
	global_load_lds_dwordx4 v[248:249], off
	s_waitcnt vmcnt(8)
	s_waitcnt lgkmcnt(0)
	s_barrier
	s_setprio 1
	s_waitcnt lgkmcnt(0)
	v_mfma_f32_16x16x32_bf16 v[128:131], v[148:151], v[184:187], v[128:131]
	v_mfma_f32_16x16x32_bf16 v[124:127], v[160:163], v[184:187], v[124:127]
	v_mfma_f32_16x16x32_bf16 v[116:119], v[148:151], v[192:195], v[116:119]
	v_mfma_f32_16x16x32_bf16 v[108:111], v[160:163], v[192:195], v[108:111]
	v_mfma_f32_16x16x32_bf16 v[100:103], v[148:151], v[226:229], v[100:103]
	v_mfma_f32_16x16x32_bf16 v[92:95], v[160:163], v[226:229], v[92:95]
	v_mfma_f32_16x16x32_bf16 v[84:87], v[148:151], v[234:237], v[84:87]
	v_mfma_f32_16x16x32_bf16 v[76:79], v[160:163], v[234:237], v[76:79]
	v_mfma_f32_16x16x32_bf16 v[128:131], v[156:159], v[188:191], v[128:131]
	v_mfma_f32_16x16x32_bf16 v[124:127], v[164:167], v[188:191], v[124:127]
	v_mfma_f32_16x16x32_bf16 v[116:119], v[156:159], v[210:213], v[116:119]
	v_mfma_f32_16x16x32_bf16 v[108:111], v[164:167], v[210:213], v[108:111]
	v_mfma_f32_16x16x32_bf16 v[100:103], v[156:159], v[230:233], v[100:103]
	v_mfma_f32_16x16x32_bf16 v[92:95], v[164:167], v[230:233], v[92:95]
	v_mfma_f32_16x16x32_bf16 v[84:87], v[156:159], v[238:241], v[84:87]
	v_mfma_f32_16x16x32_bf16 v[76:79], v[164:167], v[238:241], v[76:79]
	s_setprio 0
	s_setprio 1
	v_mfma_f32_16x16x32_bf16 v[120:123], v[168:171], v[184:187], v[120:123]
	v_mfma_f32_16x16x32_bf16 v[112:115], v[176:179], v[184:187], v[112:115]
	v_mfma_f32_16x16x32_bf16 v[104:107], v[168:171], v[192:195], v[104:107]
	v_mfma_f32_16x16x32_bf16 v[96:99], v[176:179], v[192:195], v[96:99]
	v_mfma_f32_16x16x32_bf16 v[88:91], v[168:171], v[226:229], v[88:91]
	v_mfma_f32_16x16x32_bf16 v[80:83], v[176:179], v[226:229], v[80:83]
	v_mfma_f32_16x16x32_bf16 v[72:75], v[168:171], v[234:237], v[72:75]
	v_mfma_f32_16x16x32_bf16 v[68:71], v[176:179], v[234:237], v[68:71]
	v_mfma_f32_16x16x32_bf16 v[120:123], v[172:175], v[188:191], v[120:123]
	v_mfma_f32_16x16x32_bf16 v[112:115], v[180:183], v[188:191], v[112:115]
	v_mfma_f32_16x16x32_bf16 v[104:107], v[172:175], v[210:213], v[104:107]
	v_mfma_f32_16x16x32_bf16 v[96:99], v[180:183], v[210:213], v[96:99]
	v_mfma_f32_16x16x32_bf16 v[88:91], v[172:175], v[230:233], v[88:91]
	v_mfma_f32_16x16x32_bf16 v[80:83], v[180:183], v[230:233], v[80:83]
	v_mfma_f32_16x16x32_bf16 v[72:75], v[172:175], v[238:241], v[72:75]
	v_mfma_f32_16x16x32_bf16 v[68:71], v[180:183], v[238:241], v[68:71]
	s_setprio 0
	s_barrier
; #define PG8_STAGE(bufoff, gbase, voff) do { _Pragma("unroll") for (int _i = 0; _i < 2; ++_i) \
;         __builtin_amdgcn_global_load_lds((const unsigned*)((const char*)(gbase) + (voff)[_i]), (PG8_LAS unsigned*)(lds + (bufoff) + ldsw + _i * 8192), 16, 0, 0); } while (0)
; #define PG8_LDA(dst, b, h) do { _Pragma("unroll") for (int m = 0; m < 4; ++m) _Pragma("unroll") for (int k = 0; k < 2; ++k) dst[m][k] = *(const PG8_LAS bf16x8*)(lds + PG8_SA(b, h) + aoff + m * 2048 + k * 1024); } while (0)
; #define PG8_MMA(ai, bj, At, Bt) do { __builtin_amdgcn_s_setprio(1); _Pragma("unroll") for (int m = 0; m < 4; ++m) _Pragma("unroll") for (int n = 0; n < 2; ++n) _Pragma("unroll") for (int k = 0; k < 2; ++k) \
;         acc[ai][bj][m][n] = __builtin_amdgcn_mfma_f32_16x16x32_bf16(Bt[n][k], At[m][k], acc[ai][bj][m][n], 0, 0, 0); __builtin_amdgcn_s_setprio(0); } while (0)
; #define PG8_WAIT_V(n) asm volatile("s_waitcnt vmcnt(" #n ")" ::: "memory")
; #define PG8_WAIT_L(n) asm volatile("s_waitcnt lgkmcnt(" #n ")" ::: "memory")
; #define PG8_BAR __builtin_amdgcn_s_barrier()
; #define PG8_SCHED __builtin_amdgcn_sched_barrier(0)
; template <class Epi, class Sched, bool ALIGN_EPI = false, bool SP2 = false>
; __device__ __forceinline__ void gemm_phase(PG8_LAS unsigned char* lds, const Gemm g, const Sched& S, const Epi& E) {
;     ...
;         for (int t = 0; t < nt; t += 2) {
;     ...
;             PG8_WAIT_V(8); PG8_WAIT_L(0); PG8_BAR; PG8_MMA(0, 0, At, B0); PG8_MMA(0, 1, At, B1); PG8_BAR; PG8_SCHED;
;             PG8_LDA(At, 1, 1); PG8_STAGE(PG8_SB(1, 0), b3, voffB); PG8_STAGE(PG8_SB(1, 1), b3 + hstepB, voffB); PG8_STAGE(PG8_SA(1, 0), a3, voffA);
;             PG8_WAIT_V(8); PG8_WAIT_L(0); PG8_BAR; PG8_MMA(1, 0, At, B0); PG8_MMA(1, 1, At, B1); PG8_BAR; PG8_SCHED;
	s_add_i32 s30, s52, s33
	v_lshl_add_u64 v[196:197], v[196:197], 0, s[64:65]
	s_mov_b32 m0, s30
	ds_read_b128 v[184:187], v154 offset:49152
	ds_read_b128 v[188:191], v154 offset:50176
	ds_read_b128 v[192:195], v154 offset:51200
	ds_read_b128 v[210:213], v154 offset:52224
	ds_read_b128 v[226:229], v154 offset:53248
	ds_read_b128 v[230:233], v154 offset:54272
	ds_read_b128 v[234:237], v154 offset:55296
	ds_read_b128 v[238:241], v154 offset:56320
	global_load_lds_dwordx4 v[196:197], off
	s_add_i32 m0, s30, 0x2000
	s_add_u32 s28, s28, 0x40080
	v_lshl_add_u64 v[196:197], v[242:243], 0, s[64:65]
	s_addc_u32 s29, s29, 0
	s_add_i32 s30, s53, s33
	global_load_lds_dwordx4 v[196:197], off
	v_lshl_add_u64 v[196:197], s[28:29], 0, v[136:137]
	s_mov_b32 m0, s30
	s_nop 0
	global_load_lds_dwordx4 v[196:197], off
	v_lshl_add_u64 v[196:197], s[28:29], 0, v[132:133]
	s_add_i32 m0, s30, 0x2000
	s_nop 0
	global_load_lds_dwordx4 v[196:197], off
	s_waitcnt vmcnt(6)
	s_waitcnt lgkmcnt(0)
	s_barrier
	s_setprio 1
	s_waitcnt lgkmcnt(0)
	v_mfma_f32_16x16x32_bf16 v[64:67], v[148:151], v[184:187], v[64:67]
	v_mfma_f32_16x16x32_bf16 v[60:63], v[160:163], v[184:187], v[60:63]
	v_mfma_f32_16x16x32_bf16 v[52:55], v[148:151], v[192:195], v[52:55]
	v_mfma_f32_16x16x32_bf16 v[44:47], v[160:163], v[192:195], v[44:47]
	v_mfma_f32_16x16x32_bf16 v[36:39], v[148:151], v[226:229], v[36:39]
	v_mfma_f32_16x16x32_bf16 v[28:31], v[160:163], v[226:229], v[28:31]
	v_mfma_f32_16x16x32_bf16 v[20:23], v[148:151], v[234:237], v[20:23]
	v_mfma_f32_16x16x32_bf16 v[12:15], v[160:163], v[234:237], v[12:15]
	v_mfma_f32_16x16x32_bf16 v[64:67], v[156:159], v[188:191], v[64:67]
	v_mfma_f32_16x16x32_bf16 v[60:63], v[164:167], v[188:191], v[60:63]
	v_mfma_f32_16x16x32_bf16 v[52:55], v[156:159], v[210:213], v[52:55]
	v_mfma_f32_16x16x32_bf16 v[44:47], v[164:167], v[210:213], v[44:47]
	v_mfma_f32_16x16x32_bf16 v[36:39], v[156:159], v[230:233], v[36:39]
	v_mfma_f32_16x16x32_bf16 v[28:31], v[164:167], v[230:233], v[28:31]
	v_mfma_f32_16x16x32_bf16 v[20:23], v[156:159], v[238:241], v[20:23]
	v_mfma_f32_16x16x32_bf16 v[12:15], v[164:167], v[238:241], v[12:15]
	s_setprio 0
	s_setprio 1
	v_mfma_f32_16x16x32_bf16 v[56:59], v[168:171], v[184:187], v[56:59]
	v_mfma_f32_16x16x32_bf16 v[48:51], v[176:179], v[184:187], v[48:51]
	v_mfma_f32_16x16x32_bf16 v[40:43], v[168:171], v[192:195], v[40:43]
	v_mfma_f32_16x16x32_bf16 v[32:35], v[176:179], v[192:195], v[32:35]
	v_mfma_f32_16x16x32_bf16 v[24:27], v[168:171], v[226:229], v[24:27]
	v_mfma_f32_16x16x32_bf16 v[16:19], v[176:179], v[226:229], v[16:19]
	v_mfma_f32_16x16x32_bf16 v[8:11], v[168:171], v[234:237], v[8:11]
	v_mfma_f32_16x16x32_bf16 v[4:7], v[176:179], v[234:237], v[4:7]
	v_mfma_f32_16x16x32_bf16 v[56:59], v[172:175], v[188:191], v[56:59]
	v_mfma_f32_16x16x32_bf16 v[48:51], v[180:183], v[188:191], v[48:51]
	v_mfma_f32_16x16x32_bf16 v[40:43], v[172:175], v[210:213], v[40:43]
	v_mfma_f32_16x16x32_bf16 v[32:35], v[180:183], v[210:213], v[32:35]
	v_mfma_f32_16x16x32_bf16 v[24:27], v[172:175], v[230:233], v[24:27]
	v_mfma_f32_16x16x32_bf16 v[16:19], v[180:183], v[230:233], v[16:19]
	v_mfma_f32_16x16x32_bf16 v[8:11], v[172:175], v[238:241], v[8:11]
	v_mfma_f32_16x16x32_bf16 v[4:7], v[180:183], v[238:241], v[4:7]
	s_setprio 0
	s_barrier
	s_add_i32 s51, s51, 2
	s_add_u32 s49, s49, 0x100
	s_addc_u32 s50, s50, 0
	s_add_u32 s26, s26, 0x100
	s_addc_u32 s27, s27, 0
	s_cmp_gt_u32 s51, 13
	s_cbranch_scc1 .Lpeel_exit_2

; #define PG8_BAR __builtin_amdgcn_s_barrier()
; template <class Epi, class Sched, bool ALIGN_EPI = false, bool SP2 = false>
; __device__ __forceinline__ void gemm_phase(PG8_LAS unsigned char* lds, const Gemm g, const Sched& S, const Epi& E) {
;     ...
;         if constexpr (ALIGN_EPI) { if (wr == 0) PG8_BAR; }
;         if constexpr (!Epi::AFTER_DRAIN) { E(acc, cur, wr, wc, fr, fq); S.done(cur); }
;     __device__ __forceinline__ void operator()(const f32x4 (&acc)[2][2][4][2], const Unit& u, int wr, int wc, int fr, int fq) const {
;         const int row0 = u.pm * BM + wr * 64 + fr, ct0 = wc * 32 + 8 * fq;
;         if (u.pn < 12) {
;             const int t = u.pn >> 2; const float sc = (t == 0) ? qscale : 1.0f;
;             bf16_t* base = QKV + (size_t)t * tstride + (u.pn & 3) * BM + ct0;
.Lpeel_exit_2:
	s_and_b64 vcc, exec, s[14:15]
	s_cbranch_vccnz .LBB0_821
	v_lshl_add_u32 v150, s24, 8, v152
	s_cmp_gt_i32 s47, 11
	s_mov_b64 s[24:25], -1
	s_cbranch_scc1 .LBB0_822

; #define PG8_STR(x) PG8_STR2(x)
; #define PG8_STAGE(bufoff, gbase, voff) do { _Pragma("unroll") for (int _i = 0; _i < 2; ++_i) \
;         __builtin_amdgcn_global_load_lds((const unsigned*)((const char*)(gbase) + (voff)[_i]), (PG8_LAS unsigned*)(lds + (bufoff) + ldsw + _i * 8192), 16, 0, 0); } while (0)
; #define PG8_LDA(dst, b, h) do { _Pragma("unroll") for (int m = 0; m < 4; ++m) _Pragma("unroll") for (int k = 0; k < 2; ++k) dst[m][k] = *(const PG8_LAS bf16x8*)(lds + PG8_SA(b, h) + aoff + m * 2048 + k * 1024); } while (0)
; #define PG8_LDB(dst, b, h) do { _Pragma("unroll") for (int n = 0; n < 2; ++n) _Pragma("unroll") for (int k = 0; k < 2; ++k) dst[n][k] = *(const PG8_LAS bf16x8*)(lds + PG8_SB(b, h) + boff + n * 2048 + k * 1024); } while (0)
; #define PG8_MMA(ai, bj, At, Bt) do { __builtin_amdgcn_s_setprio(1); _Pragma("unroll") for (int m = 0; m < 4; ++m) _Pragma("unroll") for (int n = 0; n < 2; ++n) _Pragma("unroll") for (int k = 0; k < 2; ++k) \
;         acc[ai][bj][m][n] = __builtin_amdgcn_mfma_f32_16x16x32_bf16(Bt[n][k], At[m][k], acc[ai][bj][m][n], 0, 0, 0); __builtin_amdgcn_s_setprio(0); } while (0)
; template <class Epi, class Sched, bool ALIGN_EPI = false, bool SP2 = false>
; __device__ __forceinline__ void gemm_phase(PG8_LAS unsigned char* lds, const Gemm g, const Sched& S, const Epi& E) {
;     ...
;         for (int t = 0; t < nt; t += 2) {
;     ...
;             asm volatile(".p2align 6\n\t.rept " PG8_STR(KLOOP_ALIGN) "\n\ts_nop 0\n\t.endr");
;     ...
;             const bool last = (t == nt - 2);
;             const char* a1 = cA + (size_t)(t + 1) * kstep;
;             const char* a2 = last ? nA : cA + (size_t)(t + 2) * kstep; const char* b2 = last ? nB : cB + (size_t)(t + 2) * kstep;
;             const char* a3 = a2 + kstep; const char* b3 = b2 + kstep;
;             if (last && has_next) S.a_ready(nxt);
;             if constexpr (SP2) {
;             PG8_LDB(B0, 0, 0); PG8_LDB(B1, 0, 1); PG8_SCHED; PG8_LDA(At, 0, 0); PG8_STAGE(PG8_SA(1, 1), a1 + hstepA, voffA);
;             PG8_WAIT_V(8); PG8_WAIT_L(0); PG8_BAR; PG8_MMA(0, 0, At, B0); PG8_MMA(0, 1, At, B1); PG8_BAR; PG8_SCHED;
;             PG8_LDA(At, 0, 1); PG8_STAGE(PG8_SB(0, 0), b2, voffB); PG8_STAGE(PG8_SB(0, 1), b2 + hstepB, voffB); PG8_STAGE(PG8_SA(0, 0), a2, voffA);
;             PG8_WAIT_V(8); PG8_WAIT_L(0); PG8_BAR; PG8_MMA(1, 0, At, B0); PG8_MMA(1, 1, At, B1); PG8_BAR; PG8_SCHED;
.LBB0_1092:
	s_ashr_i32 s15, s14, 31
	s_lshl_b64 s[18:19], s[14:15], 19
	s_add_u32 s18, s29, s18
	s_addc_u32 s19, s30, s19
	s_and_b64 s[20:21], s[4:5], exec
	s_cselect_b32 s15, s19, s25
	s_cselect_b32 s44, s18, s24
	s_ashr_i32 s13, s12, 31
	s_lshl_b64 s[20:21], s[12:13], 19
	s_add_u32 s20, s31, s20
	s_addc_u32 s21, s33, s21
	s_and_b64 s[26:27], s[4:5], exec
	s_cselect_b32 s13, s21, s23
	s_cselect_b32 s45, s20, s22
	s_add_u32 s46, s22, 0x100
	s_addc_u32 s47, s23, 0
	s_add_u32 s22, s24, 0x40080
	s_addc_u32 s23, s25, 0
	s_mov_b32 s48, -2
	s_add_u32 s24, s22, 0xfffc0080
	s_addc_u32 s25, s23, -1
	s_add_i32 s49, 0, 0x10000
	s_cmp_eq_u32 s48, 12
	s_cselect_b32 s27, s15, s25
	s_cselect_b32 s26, s44, s24
	v_add_u32_e32 v144, s49, v146
	s_cselect_b32 s25, s13, s47
	s_cselect_b32 s24, s45, s46
	s_add_i32 s52, 0, 0x14000
	ds_read_b128 v[150:153], v144
	ds_read_b128 v[154:157], v144 offset:1024
	ds_read_b128 v[158:161], v144 offset:2048
	ds_read_b128 v[162:165], v144 offset:3072
	v_add_u32_e32 v144, s52, v146
	ds_read_b128 v[166:169], v144
	ds_read_b128 v[170:173], v144 offset:1024
	ds_read_b128 v[174:177], v144 offset:2048
	ds_read_b128 v[178:181], v144 offset:3072
	v_lshl_add_u64 v[144:145], s[22:23], 0, v[142:143]
	s_add_i32 m0, s17, 0xc000
	ds_read_b128 v[182:185], v148
	ds_read_b128 v[186:189], v148 offset:1024
	ds_read_b128 v[190:193], v148 offset:2048
	ds_read_b128 v[194:197], v148 offset:3072
	ds_read_b128 v[210:213], v148 offset:4096
	ds_read_b128 v[226:229], v148 offset:5120
	ds_read_b128 v[230:233], v148 offset:6144
	ds_read_b128 v[234:237], v148 offset:7168
	v_lshl_add_u64 v[244:245], v[240:241], 0, s[64:65]
	s_mov_b32 m0, s39
	s_nop 0
	global_load_lds_dwordx4 v[244:245], off
	v_lshl_add_u64 v[244:245], v[242:243], 0, s[64:65]
	s_mov_b32 m0, s40
	s_nop 0
	global_load_lds_dwordx4 v[244:245], off
	s_add_i32 m0, s17, 0xc000
	s_nop 0
	global_load_lds_dwordx4 v[144:145], off
	v_lshl_add_u64 v[144:145], s[22:23], 0, v[140:141]
	s_add_i32 m0, s17, 0xe000
	s_nop 0
	global_load_lds_dwordx4 v[144:145], off
	s_waitcnt vmcnt(8)
	s_waitcnt lgkmcnt(0)
	s_barrier
	s_setprio 1
	s_waitcnt lgkmcnt(0)
	v_mfma_f32_16x16x32_bf16 v[128:131], v[150:153], v[182:185], 0
	v_mfma_f32_16x16x32_bf16 v[124:127], v[158:161], v[182:185], 0
	v_mfma_f32_16x16x32_bf16 v[120:123], v[150:153], v[190:193], 0
	v_mfma_f32_16x16x32_bf16 v[112:115], v[158:161], v[190:193], 0
	v_mfma_f32_16x16x32_bf16 v[104:107], v[150:153], v[210:213], 0
	v_mfma_f32_16x16x32_bf16 v[96:99], v[158:161], v[210:213], 0
	v_mfma_f32_16x16x32_bf16 v[88:91], v[150:153], v[230:233], 0
	v_mfma_f32_16x16x32_bf16 v[80:83], v[158:161], v[230:233], 0
	v_mfma_f32_16x16x32_bf16 v[128:131], v[154:157], v[186:189], v[128:131]
	v_mfma_f32_16x16x32_bf16 v[124:127], v[162:165], v[186:189], v[124:127]
	v_mfma_f32_16x16x32_bf16 v[120:123], v[154:157], v[194:197], v[120:123]
	v_mfma_f32_16x16x32_bf16 v[112:115], v[162:165], v[194:197], v[112:115]
	v_mfma_f32_16x16x32_bf16 v[104:107], v[154:157], v[226:229], v[104:107]
	v_mfma_f32_16x16x32_bf16 v[96:99], v[162:165], v[226:229], v[96:99]
	v_mfma_f32_16x16x32_bf16 v[88:91], v[154:157], v[234:237], v[88:91]
	v_mfma_f32_16x16x32_bf16 v[80:83], v[162:165], v[234:237], v[80:83]
	s_setprio 0
	s_setprio 1
	v_mfma_f32_16x16x32_bf16 v[116:119], v[166:169], v[182:185], 0
	v_mfma_f32_16x16x32_bf16 v[108:111], v[174:177], v[182:185], 0
	v_mfma_f32_16x16x32_bf16 v[100:103], v[166:169], v[190:193], 0
	v_mfma_f32_16x16x32_bf16 v[92:95], v[174:177], v[190:193], 0
	v_mfma_f32_16x16x32_bf16 v[84:87], v[166:169], v[210:213], 0
	v_mfma_f32_16x16x32_bf16 v[76:79], v[174:177], v[210:213], 0
	v_mfma_f32_16x16x32_bf16 v[72:75], v[166:169], v[230:233], 0
	v_mfma_f32_16x16x32_bf16 v[68:71], v[174:177], v[230:233], 0
	v_mfma_f32_16x16x32_bf16 v[116:119], v[170:173], v[186:189], v[116:119]
	v_mfma_f32_16x16x32_bf16 v[108:111], v[178:181], v[186:189], v[108:111]
	v_mfma_f32_16x16x32_bf16 v[100:103], v[170:173], v[194:197], v[100:103]
	v_mfma_f32_16x16x32_bf16 v[92:95], v[178:181], v[194:197], v[92:95]
	v_mfma_f32_16x16x32_bf16 v[84:87], v[170:173], v[226:229], v[84:87]
	v_mfma_f32_16x16x32_bf16 v[76:79], v[178:181], v[226:229], v[76:79]
	v_mfma_f32_16x16x32_bf16 v[72:75], v[170:173], v[234:237], v[72:75]
	v_mfma_f32_16x16x32_bf16 v[68:71], v[178:181], v[234:237], v[68:71]
	s_setprio 0
	s_barrier
	s_add_i32 s49, s49, s34
	v_lshl_add_u64 v[144:145], s[24:25], 0, v[134:135]
	s_mov_b32 m0, s49
	ds_read_b128 v[182:185], v148 offset:16384
	ds_read_b128 v[186:189], v148 offset:17408
	ds_read_b128 v[190:193], v148 offset:18432
	ds_read_b128 v[194:197], v148 offset:19456
	ds_read_b128 v[210:213], v148 offset:20480
	ds_read_b128 v[226:229], v148 offset:21504
	ds_read_b128 v[230:233], v148 offset:22528
	ds_read_b128 v[234:237], v148 offset:23552
	global_load_lds_dwordx4 v[144:145], off
	s_add_i32 m0, s49, 0x2000
	s_add_u32 s50, s24, 0x40000
	v_lshl_add_u64 v[238:239], s[24:25], 0, v[138:139]
	s_addc_u32 s51, s25, 0
	s_add_i32 s49, s52, s34
	global_load_lds_dwordx4 v[238:239], off
	v_lshl_add_u64 v[240:241], s[50:51], 0, v[134:135]
	s_mov_b32 m0, s49
	v_lshl_add_u64 v[242:243], s[26:27], 0, v[136:137]
	global_load_lds_dwordx4 v[240:241], off
	v_lshl_add_u64 v[240:241], s[50:51], 0, v[138:139]
	s_add_i32 m0, s49, 0x2000
	s_nop 0
	global_load_lds_dwordx4 v[240:241], off
	v_lshl_add_u64 v[240:241], s[26:27], 0, v[132:133]
	s_waitcnt vmcnt(6)
	s_waitcnt lgkmcnt(0)
	s_barrier
; #define PG8_STAGE(bufoff, gbase, voff) do { _Pragma("unroll") for (int _i = 0; _i < 2; ++_i) \
;         __builtin_amdgcn_global_load_lds((const unsigned*)((const char*)(gbase) + (voff)[_i]), (PG8_LAS unsigned*)(lds + (bufoff) + ldsw + _i * 8192), 16, 0, 0); } while (0)
; #define PG8_LDA(dst, b, h) do { _Pragma("unroll") for (int m = 0; m < 4; ++m) _Pragma("unroll") for (int k = 0; k < 2; ++k) dst[m][k] = *(const PG8_LAS bf16x8*)(lds + PG8_SA(b, h) + aoff + m * 2048 + k * 1024); } while (0)
; #define PG8_LDB(dst, b, h) do { _Pragma("unroll") for (int n = 0; n < 2; ++n) _Pragma("unroll") for (int k = 0; k < 2; ++k) dst[n][k] = *(const PG8_LAS bf16x8*)(lds + PG8_SB(b, h) + boff + n * 2048 + k * 1024); } while (0)
; #define PG8_MMA(ai, bj, At, Bt) do { __builtin_amdgcn_s_setprio(1); _Pragma("unroll") for (int m = 0; m < 4; ++m) _Pragma("unroll") for (int n = 0; n < 2; ++n) _Pragma("unroll") for (int k = 0; k < 2; ++k) \
;         acc[ai][bj][m][n] = __builtin_amdgcn_mfma_f32_16x16x32_bf16(Bt[n][k], At[m][k], acc[ai][bj][m][n], 0, 0, 0); __builtin_amdgcn_s_setprio(0); } while (0)
; #define PG8_WAIT_V(n) asm volatile("s_waitcnt vmcnt(" #n ")" ::: "memory")
; #define PG8_WAIT_L(n) asm volatile("s_waitcnt lgkmcnt(" #n ")" ::: "memory")
; #define PG8_BAR __builtin_amdgcn_s_barrier()
; #define PG8_SCHED __builtin_amdgcn_sched_barrier(0)
; template <class Epi, class Sched, bool ALIGN_EPI = false, bool SP2 = false>
; __device__ __forceinline__ void gemm_phase(PG8_LAS unsigned char* lds, const Gemm g, const Sched& S, const Epi& E) {
;     ...
;             PG8_WAIT_V(8); PG8_WAIT_L(0); PG8_BAR; PG8_MMA(0, 0, At, B0); PG8_MMA(0, 1, At, B1); PG8_BAR; PG8_SCHED;
;             PG8_LDA(At, 0, 1); PG8_STAGE(PG8_SB(0, 0), b2, voffB); PG8_STAGE(PG8_SB(0, 1), b2 + hstepB, voffB); PG8_STAGE(PG8_SA(0, 0), a2, voffA);
;             PG8_WAIT_V(8); PG8_WAIT_L(0); PG8_BAR; PG8_MMA(1, 0, At, B0); PG8_MMA(1, 1, At, B1); PG8_BAR; PG8_SCHED;
;             PG8_LDB(B0, 1, 0); PG8_LDB(B1, 1, 1); PG8_SCHED; PG8_LDA(At, 1, 0); PG8_STAGE(PG8_SA(0, 1), a2 + hstepA, voffA);
;             PG8_WAIT_V(8); PG8_WAIT_L(0); PG8_BAR; PG8_MMA(0, 0, At, B0); PG8_MMA(0, 1, At, B1); PG8_BAR; PG8_SCHED;
	s_setprio 1
	s_waitcnt lgkmcnt(0)
	v_mfma_f32_16x16x32_bf16 v[64:67], v[150:153], v[182:185], 0
	v_mfma_f32_16x16x32_bf16 v[60:63], v[158:161], v[182:185], 0
	v_mfma_f32_16x16x32_bf16 v[56:59], v[150:153], v[190:193], 0
	v_mfma_f32_16x16x32_bf16 v[48:51], v[158:161], v[190:193], 0
	v_mfma_f32_16x16x32_bf16 v[40:43], v[150:153], v[210:213], 0
	v_mfma_f32_16x16x32_bf16 v[32:35], v[158:161], v[210:213], 0
	v_mfma_f32_16x16x32_bf16 v[24:27], v[150:153], v[230:233], 0
	v_mfma_f32_16x16x32_bf16 v[16:19], v[158:161], v[230:233], 0
	v_mfma_f32_16x16x32_bf16 v[64:67], v[154:157], v[186:189], v[64:67]
	v_mfma_f32_16x16x32_bf16 v[60:63], v[162:165], v[186:189], v[60:63]
	v_mfma_f32_16x16x32_bf16 v[56:59], v[154:157], v[194:197], v[56:59]
	v_mfma_f32_16x16x32_bf16 v[48:51], v[162:165], v[194:197], v[48:51]
	v_mfma_f32_16x16x32_bf16 v[40:43], v[154:157], v[226:229], v[40:43]
	v_mfma_f32_16x16x32_bf16 v[32:35], v[162:165], v[226:229], v[32:35]
	v_mfma_f32_16x16x32_bf16 v[24:27], v[154:157], v[234:237], v[24:27]
	v_mfma_f32_16x16x32_bf16 v[16:19], v[162:165], v[234:237], v[16:19]
	s_setprio 0
	s_setprio 1
	v_mfma_f32_16x16x32_bf16 v[52:55], v[166:169], v[182:185], 0
	v_mfma_f32_16x16x32_bf16 v[44:47], v[174:177], v[182:185], 0
	v_mfma_f32_16x16x32_bf16 v[36:39], v[166:169], v[190:193], 0
	v_mfma_f32_16x16x32_bf16 v[28:31], v[174:177], v[190:193], 0
	v_mfma_f32_16x16x32_bf16 v[20:23], v[166:169], v[210:213], 0
	v_mfma_f32_16x16x32_bf16 v[12:15], v[174:177], v[210:213], 0
	v_mfma_f32_16x16x32_bf16 v[8:11], v[166:169], v[230:233], 0
	v_mfma_f32_16x16x32_bf16 v[4:7], v[174:177], v[230:233], 0
	v_mfma_f32_16x16x32_bf16 v[52:55], v[170:173], v[186:189], v[52:55]
	v_mfma_f32_16x16x32_bf16 v[44:47], v[178:181], v[186:189], v[44:47]
	v_mfma_f32_16x16x32_bf16 v[36:39], v[170:173], v[194:197], v[36:39]
	v_mfma_f32_16x16x32_bf16 v[28:31], v[178:181], v[194:197], v[28:31]
	v_mfma_f32_16x16x32_bf16 v[20:23], v[170:173], v[226:229], v[20:23]
	v_mfma_f32_16x16x32_bf16 v[12:15], v[178:181], v[226:229], v[12:15]
	v_mfma_f32_16x16x32_bf16 v[8:11], v[170:173], v[234:237], v[8:11]
	v_mfma_f32_16x16x32_bf16 v[4:7], v[178:181], v[234:237], v[4:7]
	s_setprio 0
	s_barrier
	s_add_i32 s49, 0, 0x18000
	v_add_u32_e32 v149, s49, v146
	s_add_i32 s50, 0, 0x1c000
	ds_read_b128 v[150:153], v149
	ds_read_b128 v[154:157], v149 offset:1024
	ds_read_b128 v[158:161], v149 offset:2048
	ds_read_b128 v[162:165], v149 offset:3072
	v_add_u32_e32 v149, s50, v146
	ds_read_b128 v[166:169], v149
	ds_read_b128 v[170:173], v149 offset:1024
	ds_read_b128 v[174:177], v149 offset:2048
	ds_read_b128 v[178:181], v149 offset:3072
	s_add_u32 s26, s26, 0x40000
	s_addc_u32 s27, s27, 0
	s_mov_b32 m0, s37
	v_lshl_add_u64 v[244:245], s[26:27], 0, v[132:133]
	ds_read_b128 v[182:185], v148 offset:32768
	ds_read_b128 v[186:189], v148 offset:33792
	ds_read_b128 v[190:193], v148 offset:34816
	ds_read_b128 v[194:197], v148 offset:35840
	ds_read_b128 v[210:213], v148 offset:36864
	ds_read_b128 v[226:229], v148 offset:37888
	ds_read_b128 v[230:233], v148 offset:38912
	ds_read_b128 v[234:237], v148 offset:39936
	s_mov_b32 m0, s17
	s_nop 0
	global_load_lds_dwordx4 v[240:241], off
	s_mov_b32 m0, s35
	s_nop 0
	global_load_lds_dwordx4 v[242:243], off
	s_mov_b32 m0, s37
	s_nop 0
	global_load_lds_dwordx4 v[244:245], off
	v_lshl_add_u64 v[244:245], s[26:27], 0, v[136:137]
	s_mov_b32 m0, s38
	s_nop 0
	global_load_lds_dwordx4 v[244:245], off
	s_waitcnt vmcnt(8)
	s_waitcnt lgkmcnt(0)
	s_barrier
	s_setprio 1
	s_waitcnt lgkmcnt(0)
	v_mfma_f32_16x16x32_bf16 v[128:131], v[150:153], v[182:185], v[128:131]
	v_mfma_f32_16x16x32_bf16 v[124:127], v[158:161], v[182:185], v[124:127]
	v_mfma_f32_16x16x32_bf16 v[120:123], v[150:153], v[190:193], v[120:123]
	v_mfma_f32_16x16x32_bf16 v[112:115], v[158:161], v[190:193], v[112:115]
	v_mfma_f32_16x16x32_bf16 v[104:107], v[150:153], v[210:213], v[104:107]
	v_mfma_f32_16x16x32_bf16 v[96:99], v[158:161], v[210:213], v[96:99]
	v_mfma_f32_16x16x32_bf16 v[88:91], v[150:153], v[230:233], v[88:91]
	v_mfma_f32_16x16x32_bf16 v[80:83], v[158:161], v[230:233], v[80:83]
	v_mfma_f32_16x16x32_bf16 v[128:131], v[154:157], v[186:189], v[128:131]
	v_mfma_f32_16x16x32_bf16 v[124:127], v[162:165], v[186:189], v[124:127]
	v_mfma_f32_16x16x32_bf16 v[120:123], v[154:157], v[194:197], v[120:123]
	v_mfma_f32_16x16x32_bf16 v[112:115], v[162:165], v[194:197], v[112:115]
	v_mfma_f32_16x16x32_bf16 v[104:107], v[154:157], v[226:229], v[104:107]
	v_mfma_f32_16x16x32_bf16 v[96:99], v[162:165], v[226:229], v[96:99]
	v_mfma_f32_16x16x32_bf16 v[88:91], v[154:157], v[234:237], v[88:91]
	v_mfma_f32_16x16x32_bf16 v[80:83], v[162:165], v[234:237], v[80:83]
	s_setprio 0
	s_setprio 1
	v_mfma_f32_16x16x32_bf16 v[116:119], v[166:169], v[182:185], v[116:119]
	v_mfma_f32_16x16x32_bf16 v[108:111], v[174:177], v[182:185], v[108:111]
	v_mfma_f32_16x16x32_bf16 v[100:103], v[166:169], v[190:193], v[100:103]
	v_mfma_f32_16x16x32_bf16 v[92:95], v[174:177], v[190:193], v[92:95]
	v_mfma_f32_16x16x32_bf16 v[84:87], v[166:169], v[210:213], v[84:87]
	v_mfma_f32_16x16x32_bf16 v[76:79], v[174:177], v[210:213], v[76:79]
	v_mfma_f32_16x16x32_bf16 v[72:75], v[166:169], v[230:233], v[72:75]
	v_mfma_f32_16x16x32_bf16 v[68:71], v[174:177], v[230:233], v[68:71]
	v_mfma_f32_16x16x32_bf16 v[116:119], v[170:173], v[186:189], v[116:119]
	v_mfma_f32_16x16x32_bf16 v[108:111], v[178:181], v[186:189], v[108:111]
	v_mfma_f32_16x16x32_bf16 v[100:103], v[170:173], v[194:197], v[100:103]
	v_mfma_f32_16x16x32_bf16 v[92:95], v[178:181], v[194:197], v[92:95]
	v_mfma_f32_16x16x32_bf16 v[84:87], v[170:173], v[226:229], v[84:87]
	v_mfma_f32_16x16x32_bf16 v[76:79], v[178:181], v[226:229], v[76:79]
	v_mfma_f32_16x16x32_bf16 v[72:75], v[170:173], v[234:237], v[72:75]
	v_mfma_f32_16x16x32_bf16 v[68:71], v[178:181], v[234:237], v[68:71]
	s_setprio 0
	s_barrier
; #define PG8_STAGE(bufoff, gbase, voff) do { _Pragma("unroll") for (int _i = 0; _i < 2; ++_i) \
;         __builtin_amdgcn_global_load_lds((const unsigned*)((const char*)(gbase) + (voff)[_i]), (PG8_LAS unsigned*)(lds + (bufoff) + ldsw + _i * 8192), 16, 0, 0); } while (0)
; #define PG8_LDA(dst, b, h) do { _Pragma("unroll") for (int m = 0; m < 4; ++m) _Pragma("unroll") for (int k = 0; k < 2; ++k) dst[m][k] = *(const PG8_LAS bf16x8*)(lds + PG8_SA(b, h) + aoff + m * 2048 + k * 1024); } while (0)
; #define PG8_LDB(dst, b, h) do { _Pragma("unroll") for (int n = 0; n < 2; ++n) _Pragma("unroll") for (int k = 0; k < 2; ++k) dst[n][k] = *(const PG8_LAS bf16x8*)(lds + PG8_SB(b, h) + boff + n * 2048 + k * 1024); } while (0)
; #define PG8_MMA(ai, bj, At, Bt) do { __builtin_amdgcn_s_setprio(1); _Pragma("unroll") for (int m = 0; m < 4; ++m) _Pragma("unroll") for (int n = 0; n < 2; ++n) _Pragma("unroll") for (int k = 0; k < 2; ++k) \
;         acc[ai][bj][m][n] = __builtin_amdgcn_mfma_f32_16x16x32_bf16(Bt[n][k], At[m][k], acc[ai][bj][m][n], 0, 0, 0); __builtin_amdgcn_s_setprio(0); } while (0)
; #define PG8_BAR __builtin_amdgcn_s_barrier()
; template <class Epi, class Sched, bool ALIGN_EPI = false, bool SP2 = false>
; __device__ __forceinline__ void gemm_phase(PG8_LAS unsigned char* lds, const Gemm g, const Sched& S, const Epi& E) {
;     ...
;             const bool last = (t == nt - 2);
;             const char* a1 = cA + (size_t)(t + 1) * kstep;
;             const char* a2 = last ? nA : cA + (size_t)(t + 2) * kstep; const char* b2 = last ? nB : cB + (size_t)(t + 2) * kstep;
;             const char* a3 = a2 + kstep; const char* b3 = b2 + kstep;
;             if (last && has_next) S.a_ready(nxt);
;             if constexpr (SP2) {
;             PG8_LDB(B0, 0, 0); PG8_LDB(B1, 0, 1); PG8_SCHED; PG8_LDA(At, 0, 0); PG8_STAGE(PG8_SA(1, 1), a1 + hstepA, voffA);
;             PG8_WAIT_V(8); PG8_WAIT_L(0); PG8_BAR; PG8_MMA(0, 0, At, B0); PG8_MMA(0, 1, At, B1); PG8_BAR; PG8_SCHED;
;     ...
;             PG8_WAIT_V(8); PG8_WAIT_L(0); PG8_BAR; PG8_MMA(0, 0, At, B0); PG8_MMA(0, 1, At, B1); PG8_BAR; PG8_SCHED;
;             PG8_LDA(At, 1, 1); PG8_STAGE(PG8_SB(1, 0), b3, voffB); PG8_STAGE(PG8_SB(1, 1), b3 + hstepB, voffB); PG8_STAGE(PG8_SA(1, 0), a3, voffA);
;             PG8_WAIT_V(8); PG8_WAIT_L(0); PG8_BAR; PG8_MMA(1, 0, At, B0); PG8_MMA(1, 1, At, B1); PG8_BAR; PG8_SCHED;
	s_add_i32 s26, s49, s34
	v_lshl_add_u64 v[144:145], v[144:145], 0, s[64:65]
	s_mov_b32 m0, s26
	ds_read_b128 v[182:185], v148 offset:49152
	ds_read_b128 v[186:189], v148 offset:50176
	ds_read_b128 v[190:193], v148 offset:51200
	ds_read_b128 v[194:197], v148 offset:52224
	ds_read_b128 v[210:213], v148 offset:53248
	ds_read_b128 v[226:229], v148 offset:54272
	ds_read_b128 v[230:233], v148 offset:55296
	ds_read_b128 v[234:237], v148 offset:56320
	global_load_lds_dwordx4 v[144:145], off
	s_add_i32 m0, s26, 0x2000
	s_add_u32 s24, s24, 0x40080
	v_lshl_add_u64 v[144:145], v[238:239], 0, s[64:65]
	s_addc_u32 s25, s25, 0
	s_add_i32 s26, s50, s34
	global_load_lds_dwordx4 v[144:145], off
	v_lshl_add_u64 v[144:145], s[24:25], 0, v[134:135]
	s_mov_b32 m0, s26
	s_nop 0
	global_load_lds_dwordx4 v[144:145], off
	v_lshl_add_u64 v[144:145], s[24:25], 0, v[138:139]
	s_add_i32 m0, s26, 0x2000
	s_nop 0
	global_load_lds_dwordx4 v[144:145], off
	s_waitcnt vmcnt(6)
	s_waitcnt lgkmcnt(0)
	s_barrier
	s_setprio 1
	s_waitcnt lgkmcnt(0)
	v_mfma_f32_16x16x32_bf16 v[64:67], v[150:153], v[182:185], v[64:67]
	v_mfma_f32_16x16x32_bf16 v[60:63], v[158:161], v[182:185], v[60:63]
	v_mfma_f32_16x16x32_bf16 v[56:59], v[150:153], v[190:193], v[56:59]
	v_mfma_f32_16x16x32_bf16 v[48:51], v[158:161], v[190:193], v[48:51]
	v_mfma_f32_16x16x32_bf16 v[40:43], v[150:153], v[210:213], v[40:43]
	v_mfma_f32_16x16x32_bf16 v[32:35], v[158:161], v[210:213], v[32:35]
	v_mfma_f32_16x16x32_bf16 v[24:27], v[150:153], v[230:233], v[24:27]
	v_mfma_f32_16x16x32_bf16 v[16:19], v[158:161], v[230:233], v[16:19]
	v_mfma_f32_16x16x32_bf16 v[64:67], v[154:157], v[186:189], v[64:67]
	v_mfma_f32_16x16x32_bf16 v[60:63], v[162:165], v[186:189], v[60:63]
	v_mfma_f32_16x16x32_bf16 v[56:59], v[154:157], v[194:197], v[56:59]
	v_mfma_f32_16x16x32_bf16 v[48:51], v[162:165], v[194:197], v[48:51]
	v_mfma_f32_16x16x32_bf16 v[40:43], v[154:157], v[226:229], v[40:43]
	v_mfma_f32_16x16x32_bf16 v[32:35], v[162:165], v[226:229], v[32:35]
	v_mfma_f32_16x16x32_bf16 v[24:27], v[154:157], v[234:237], v[24:27]
	v_mfma_f32_16x16x32_bf16 v[16:19], v[162:165], v[234:237], v[16:19]
	s_setprio 0
	s_setprio 1
	v_mfma_f32_16x16x32_bf16 v[52:55], v[166:169], v[182:185], v[52:55]
	v_mfma_f32_16x16x32_bf16 v[44:47], v[174:177], v[182:185], v[44:47]
	v_mfma_f32_16x16x32_bf16 v[36:39], v[166:169], v[190:193], v[36:39]
	v_mfma_f32_16x16x32_bf16 v[28:31], v[174:177], v[190:193], v[28:31]
	v_mfma_f32_16x16x32_bf16 v[20:23], v[166:169], v[210:213], v[20:23]
	v_mfma_f32_16x16x32_bf16 v[12:15], v[174:177], v[210:213], v[12:15]
	v_mfma_f32_16x16x32_bf16 v[8:11], v[166:169], v[230:233], v[8:11]
	v_mfma_f32_16x16x32_bf16 v[4:7], v[174:177], v[230:233], v[4:7]
	v_mfma_f32_16x16x32_bf16 v[52:55], v[170:173], v[186:189], v[52:55]
	v_mfma_f32_16x16x32_bf16 v[44:47], v[178:181], v[186:189], v[44:47]
	v_mfma_f32_16x16x32_bf16 v[36:39], v[170:173], v[194:197], v[36:39]
	v_mfma_f32_16x16x32_bf16 v[28:31], v[178:181], v[194:197], v[28:31]
	v_mfma_f32_16x16x32_bf16 v[20:23], v[170:173], v[226:229], v[20:23]
	v_mfma_f32_16x16x32_bf16 v[12:15], v[178:181], v[226:229], v[12:15]
	v_mfma_f32_16x16x32_bf16 v[8:11], v[170:173], v[234:237], v[8:11]
	v_mfma_f32_16x16x32_bf16 v[4:7], v[178:181], v[234:237], v[4:7]
	s_setprio 0
	s_barrier
	s_add_i32 s48, s48, 2
	s_add_u32 s46, s46, 0x100
	s_addc_u32 s47, s47, 0
	s_add_u32 s22, s22, 0x100
	s_addc_u32 s23, s23, 0
	s_cmp_gt_u32 s48, 13
	s_cbranch_scc1 .Lpeel_exit_3
.LBB0_1093:
	s_add_u32 s24, s22, 0xfffc0080
	s_addc_u32 s25, s23, -1
	s_add_i32 s49, 0, 0x10000
	s_cmp_eq_u32 s48, 12
	s_cselect_b32 s27, s15, s25
	s_cselect_b32 s26, s44, s24
	v_add_u32_e32 v144, s49, v146
	s_cselect_b32 s25, s13, s47
	s_cselect_b32 s24, s45, s46
	s_add_i32 s52, 0, 0x14000
	ds_read_b128 v[150:153], v144
	ds_read_b128 v[154:157], v144 offset:1024
	ds_read_b128 v[158:161], v144 offset:2048
	ds_read_b128 v[162:165], v144 offset:3072
	v_add_u32_e32 v144, s52, v146
	ds_read_b128 v[166:169], v144
	ds_read_b128 v[170:173], v144 offset:1024
	ds_read_b128 v[174:177], v144 offset:2048
	ds_read_b128 v[178:181], v144 offset:3072
	v_lshl_add_u64 v[144:145], s[22:23], 0, v[142:143]
	s_add_i32 m0, s17, 0xc000
	ds_read_b128 v[182:185], v148
	ds_read_b128 v[186:189], v148 offset:1024
	ds_read_b128 v[190:193], v148 offset:2048
	ds_read_b128 v[194:197], v148 offset:3072
	ds_read_b128 v[210:213], v148 offset:4096
	ds_read_b128 v[226:229], v148 offset:5120
	ds_read_b128 v[230:233], v148 offset:6144
	ds_read_b128 v[234:237], v148 offset:7168
	v_lshl_add_u64 v[244:245], v[240:241], 0, s[64:65]
	s_mov_b32 m0, s39
	s_nop 0
	global_load_lds_dwordx4 v[244:245], off
	v_lshl_add_u64 v[244:245], v[242:243], 0, s[64:65]
	s_mov_b32 m0, s40
	s_nop 0
	global_load_lds_dwordx4 v[244:245], off
	s_add_i32 m0, s17, 0xc000
	s_nop 0
	global_load_lds_dwordx4 v[144:145], off
	v_lshl_add_u64 v[144:145], s[22:23], 0, v[140:141]
	s_add_i32 m0, s17, 0xe000
	s_nop 0
	global_load_lds_dwordx4 v[144:145], off
	s_waitcnt vmcnt(8)
	s_waitcnt lgkmcnt(0)
	s_barrier
; #define PG8_STAGE(bufoff, gbase, voff) do { _Pragma("unroll") for (int _i = 0; _i < 2; ++_i) \
;         __builtin_amdgcn_global_load_lds((const unsigned*)((const char*)(gbase) + (voff)[_i]), (PG8_LAS unsigned*)(lds + (bufoff) + ldsw + _i * 8192), 16, 0, 0); } while (0)
; #define PG8_LDA(dst, b, h) do { _Pragma("unroll") for (int m = 0; m < 4; ++m) _Pragma("unroll") for (int k = 0; k < 2; ++k) dst[m][k] = *(const PG8_LAS bf16x8*)(lds + PG8_SA(b, h) + aoff + m * 2048 + k * 1024); } while (0)
; #define PG8_LDB(dst, b, h) do { _Pragma("unroll") for (int n = 0; n < 2; ++n) _Pragma("unroll") for (int k = 0; k < 2; ++k) dst[n][k] = *(const PG8_LAS bf16x8*)(lds + PG8_SB(b, h) + boff + n * 2048 + k * 1024); } while (0)
; #define PG8_MMA(ai, bj, At, Bt) do { __builtin_amdgcn_s_setprio(1); _Pragma("unroll") for (int m = 0; m < 4; ++m) _Pragma("unroll") for (int n = 0; n < 2; ++n) _Pragma("unroll") for (int k = 0; k < 2; ++k) \
;         acc[ai][bj][m][n] = __builtin_amdgcn_mfma_f32_16x16x32_bf16(Bt[n][k], At[m][k], acc[ai][bj][m][n], 0, 0, 0); __builtin_amdgcn_s_setprio(0); } while (0)
; #define PG8_WAIT_V(n) asm volatile("s_waitcnt vmcnt(" #n ")" ::: "memory")
; #define PG8_WAIT_L(n) asm volatile("s_waitcnt lgkmcnt(" #n ")" ::: "memory")
; #define PG8_BAR __builtin_amdgcn_s_barrier()
; #define PG8_SCHED __builtin_amdgcn_sched_barrier(0)
; template <class Epi, class Sched, bool ALIGN_EPI = false, bool SP2 = false>
; __device__ __forceinline__ void gemm_phase(PG8_LAS unsigned char* lds, const Gemm g, const Sched& S, const Epi& E) {
;     ...
;             PG8_LDB(B0, 0, 0); PG8_LDB(B1, 0, 1); PG8_SCHED; PG8_LDA(At, 0, 0); PG8_STAGE(PG8_SA(1, 1), a1 + hstepA, voffA);
;             PG8_WAIT_V(8); PG8_WAIT_L(0); PG8_BAR; PG8_MMA(0, 0, At, B0); PG8_MMA(0, 1, At, B1); PG8_BAR; PG8_SCHED;
;             PG8_LDA(At, 0, 1); PG8_STAGE(PG8_SB(0, 0), b2, voffB); PG8_STAGE(PG8_SB(0, 1), b2 + hstepB, voffB); PG8_STAGE(PG8_SA(0, 0), a2, voffA);
;             PG8_WAIT_V(8); PG8_WAIT_L(0); PG8_BAR; PG8_MMA(1, 0, At, B0); PG8_MMA(1, 1, At, B1); PG8_BAR; PG8_SCHED;
;             PG8_LDB(B0, 1, 0); PG8_LDB(B1, 1, 1); PG8_SCHED; PG8_LDA(At, 1, 0); PG8_STAGE(PG8_SA(0, 1), a2 + hstepA, voffA);
;             PG8_WAIT_V(8); PG8_WAIT_L(0); PG8_BAR; PG8_MMA(0, 0, At, B0); PG8_MMA(0, 1, At, B1); PG8_BAR; PG8_SCHED;
	s_setprio 1
	s_waitcnt lgkmcnt(0)
	v_mfma_f32_16x16x32_bf16 v[128:131], v[150:153], v[182:185], v[128:131]
	v_mfma_f32_16x16x32_bf16 v[124:127], v[158:161], v[182:185], v[124:127]
	v_mfma_f32_16x16x32_bf16 v[120:123], v[150:153], v[190:193], v[120:123]
	v_mfma_f32_16x16x32_bf16 v[112:115], v[158:161], v[190:193], v[112:115]
	v_mfma_f32_16x16x32_bf16 v[104:107], v[150:153], v[210:213], v[104:107]
	v_mfma_f32_16x16x32_bf16 v[96:99], v[158:161], v[210:213], v[96:99]
	v_mfma_f32_16x16x32_bf16 v[88:91], v[150:153], v[230:233], v[88:91]
	v_mfma_f32_16x16x32_bf16 v[80:83], v[158:161], v[230:233], v[80:83]
	v_mfma_f32_16x16x32_bf16 v[128:131], v[154:157], v[186:189], v[128:131]
	v_mfma_f32_16x16x32_bf16 v[124:127], v[162:165], v[186:189], v[124:127]
	v_mfma_f32_16x16x32_bf16 v[120:123], v[154:157], v[194:197], v[120:123]
	v_mfma_f32_16x16x32_bf16 v[112:115], v[162:165], v[194:197], v[112:115]
	v_mfma_f32_16x16x32_bf16 v[104:107], v[154:157], v[226:229], v[104:107]
	v_mfma_f32_16x16x32_bf16 v[96:99], v[162:165], v[226:229], v[96:99]
	v_mfma_f32_16x16x32_bf16 v[88:91], v[154:157], v[234:237], v[88:91]
	v_mfma_f32_16x16x32_bf16 v[80:83], v[162:165], v[234:237], v[80:83]
	s_setprio 0
	s_setprio 1
	v_mfma_f32_16x16x32_bf16 v[116:119], v[166:169], v[182:185], v[116:119]
	v_mfma_f32_16x16x32_bf16 v[108:111], v[174:177], v[182:185], v[108:111]
	v_mfma_f32_16x16x32_bf16 v[100:103], v[166:169], v[190:193], v[100:103]
	v_mfma_f32_16x16x32_bf16 v[92:95], v[174:177], v[190:193], v[92:95]
	v_mfma_f32_16x16x32_bf16 v[84:87], v[166:169], v[210:213], v[84:87]
	v_mfma_f32_16x16x32_bf16 v[76:79], v[174:177], v[210:213], v[76:79]
	v_mfma_f32_16x16x32_bf16 v[72:75], v[166:169], v[230:233], v[72:75]
	v_mfma_f32_16x16x32_bf16 v[68:71], v[174:177], v[230:233], v[68:71]
	v_mfma_f32_16x16x32_bf16 v[116:119], v[170:173], v[186:189], v[116:119]
	v_mfma_f32_16x16x32_bf16 v[108:111], v[178:181], v[186:189], v[108:111]
	v_mfma_f32_16x16x32_bf16 v[100:103], v[170:173], v[194:197], v[100:103]
	v_mfma_f32_16x16x32_bf16 v[92:95], v[178:181], v[194:197], v[92:95]
	v_mfma_f32_16x16x32_bf16 v[84:87], v[170:173], v[226:229], v[84:87]
	v_mfma_f32_16x16x32_bf16 v[76:79], v[178:181], v[226:229], v[76:79]
	v_mfma_f32_16x16x32_bf16 v[72:75], v[170:173], v[234:237], v[72:75]
	v_mfma_f32_16x16x32_bf16 v[68:71], v[178:181], v[234:237], v[68:71]
	s_setprio 0
	s_barrier
	s_add_i32 s49, s49, s34
	v_lshl_add_u64 v[144:145], s[24:25], 0, v[134:135]
	s_mov_b32 m0, s49
	ds_read_b128 v[182:185], v148 offset:16384
	ds_read_b128 v[186:189], v148 offset:17408
	ds_read_b128 v[190:193], v148 offset:18432
	ds_read_b128 v[194:197], v148 offset:19456
	ds_read_b128 v[210:213], v148 offset:20480
	ds_read_b128 v[226:229], v148 offset:21504
	ds_read_b128 v[230:233], v148 offset:22528
	ds_read_b128 v[234:237], v148 offset:23552
	global_load_lds_dwordx4 v[144:145], off
	s_add_i32 m0, s49, 0x2000
	s_add_u32 s50, s24, 0x40000
	v_lshl_add_u64 v[238:239], s[24:25], 0, v[138:139]
	s_addc_u32 s51, s25, 0
	s_add_i32 s49, s52, s34
	global_load_lds_dwordx4 v[238:239], off
	v_lshl_add_u64 v[240:241], s[50:51], 0, v[134:135]
	s_mov_b32 m0, s49
	v_lshl_add_u64 v[242:243], s[26:27], 0, v[136:137]
	global_load_lds_dwordx4 v[240:241], off
	v_lshl_add_u64 v[240:241], s[50:51], 0, v[138:139]
	s_add_i32 m0, s49, 0x2000
	s_nop 0
	global_load_lds_dwordx4 v[240:241], off
	v_lshl_add_u64 v[240:241], s[26:27], 0, v[132:133]
	s_waitcnt vmcnt(6)
	s_waitcnt lgkmcnt(0)
	s_barrier
	s_setprio 1
	s_waitcnt lgkmcnt(0)
	v_mfma_f32_16x16x32_bf16 v[64:67], v[150:153], v[182:185], v[64:67]
	v_mfma_f32_16x16x32_bf16 v[60:63], v[158:161], v[182:185], v[60:63]
	v_mfma_f32_16x16x32_bf16 v[56:59], v[150:153], v[190:193], v[56:59]
	v_mfma_f32_16x16x32_bf16 v[48:51], v[158:161], v[190:193], v[48:51]
	v_mfma_f32_16x16x32_bf16 v[40:43], v[150:153], v[210:213], v[40:43]
	v_mfma_f32_16x16x32_bf16 v[32:35], v[158:161], v[210:213], v[32:35]
	v_mfma_f32_16x16x32_bf16 v[24:27], v[150:153], v[230:233], v[24:27]
	v_mfma_f32_16x16x32_bf16 v[16:19], v[158:161], v[230:233], v[16:19]
	v_mfma_f32_16x16x32_bf16 v[64:67], v[154:157], v[186:189], v[64:67]
	v_mfma_f32_16x16x32_bf16 v[60:63], v[162:165], v[186:189], v[60:63]
	v_mfma_f32_16x16x32_bf16 v[56:59], v[154:157], v[194:197], v[56:59]
	v_mfma_f32_16x16x32_bf16 v[48:51], v[162:165], v[194:197], v[48:51]
	v_mfma_f32_16x16x32_bf16 v[40:43], v[154:157], v[226:229], v[40:43]
	v_mfma_f32_16x16x32_bf16 v[32:35], v[162:165], v[226:229], v[32:35]
	v_mfma_f32_16x16x32_bf16 v[24:27], v[154:157], v[234:237], v[24:27]
	v_mfma_f32_16x16x32_bf16 v[16:19], v[162:165], v[234:237], v[16:19]
	s_setprio 0
	s_setprio 1
	v_mfma_f32_16x16x32_bf16 v[52:55], v[166:169], v[182:185], v[52:55]
	v_mfma_f32_16x16x32_bf16 v[44:47], v[174:177], v[182:185], v[44:47]
	v_mfma_f32_16x16x32_bf16 v[36:39], v[166:169], v[190:193], v[36:39]
	v_mfma_f32_16x16x32_bf16 v[28:31], v[174:177], v[190:193], v[28:31]
	v_mfma_f32_16x16x32_bf16 v[20:23], v[166:169], v[210:213], v[20:23]
	v_mfma_f32_16x16x32_bf16 v[12:15], v[174:177], v[210:213], v[12:15]
	v_mfma_f32_16x16x32_bf16 v[8:11], v[166:169], v[230:233], v[8:11]
	v_mfma_f32_16x16x32_bf16 v[4:7], v[174:177], v[230:233], v[4:7]
	v_mfma_f32_16x16x32_bf16 v[52:55], v[170:173], v[186:189], v[52:55]
	v_mfma_f32_16x16x32_bf16 v[44:47], v[178:181], v[186:189], v[44:47]
	v_mfma_f32_16x16x32_bf16 v[36:39], v[170:173], v[194:197], v[36:39]
	v_mfma_f32_16x16x32_bf16 v[28:31], v[178:181], v[194:197], v[28:31]
	v_mfma_f32_16x16x32_bf16 v[20:23], v[170:173], v[226:229], v[20:23]
	v_mfma_f32_16x16x32_bf16 v[12:15], v[178:181], v[226:229], v[12:15]
	v_mfma_f32_16x16x32_bf16 v[8:11], v[170:173], v[234:237], v[8:11]
	v_mfma_f32_16x16x32_bf16 v[4:7], v[178:181], v[234:237], v[4:7]
	s_setprio 0
	s_barrier
; #define PG8_STAGE(bufoff, gbase, voff) do { _Pragma("unroll") for (int _i = 0; _i < 2; ++_i) \
;         __builtin_amdgcn_global_load_lds((const unsigned*)((const char*)(gbase) + (voff)[_i]), (PG8_LAS unsigned*)(lds + (bufoff) + ldsw + _i * 8192), 16, 0, 0); } while (0)
; #define PG8_LDA(dst, b, h) do { _Pragma("unroll") for (int m = 0; m < 4; ++m) _Pragma("unroll") for (int k = 0; k < 2; ++k) dst[m][k] = *(const PG8_LAS bf16x8*)(lds + PG8_SA(b, h) + aoff + m * 2048 + k * 1024); } while (0)
; #define PG8_LDB(dst, b, h) do { _Pragma("unroll") for (int n = 0; n < 2; ++n) _Pragma("unroll") for (int k = 0; k < 2; ++k) dst[n][k] = *(const PG8_LAS bf16x8*)(lds + PG8_SB(b, h) + boff + n * 2048 + k * 1024); } while (0)
; #define PG8_MMA(ai, bj, At, Bt) do { __builtin_amdgcn_s_setprio(1); _Pragma("unroll") for (int m = 0; m < 4; ++m) _Pragma("unroll") for (int n = 0; n < 2; ++n) _Pragma("unroll") for (int k = 0; k < 2; ++k) \
;         acc[ai][bj][m][n] = __builtin_amdgcn_mfma_f32_16x16x32_bf16(Bt[n][k], At[m][k], acc[ai][bj][m][n], 0, 0, 0); __builtin_amdgcn_s_setprio(0); } while (0)
; #define PG8_WAIT_V(n) asm volatile("s_waitcnt vmcnt(" #n ")" ::: "memory")
; #define PG8_WAIT_L(n) asm volatile("s_waitcnt lgkmcnt(" #n ")" ::: "memory")
; #define PG8_BAR __builtin_amdgcn_s_barrier()
; #define PG8_SCHED __builtin_amdgcn_sched_barrier(0)
; template <class Epi, class Sched, bool ALIGN_EPI = false, bool SP2 = false>
; __device__ __forceinline__ void gemm_phase(PG8_LAS unsigned char* lds, const Gemm g, const Sched& S, const Epi& E) {
;     ...
;             PG8_LDB(B0, 1, 0); PG8_LDB(B1, 1, 1); PG8_SCHED; PG8_LDA(At, 1, 0); PG8_STAGE(PG8_SA(0, 1), a2 + hstepA, voffA);
;             PG8_WAIT_V(8); PG8_WAIT_L(0); PG8_BAR; PG8_MMA(0, 0, At, B0); PG8_MMA(0, 1, At, B1); PG8_BAR; PG8_SCHED;
;             PG8_LDA(At, 1, 1); PG8_STAGE(PG8_SB(1, 0), b3, voffB); PG8_STAGE(PG8_SB(1, 1), b3 + hstepB, voffB); PG8_STAGE(PG8_SA(1, 0), a3, voffA);
	s_add_i32 s49, 0, 0x18000
	v_add_u32_e32 v149, s49, v146
	s_add_i32 s50, 0, 0x1c000
	ds_read_b128 v[150:153], v149
	ds_read_b128 v[154:157], v149 offset:1024
	ds_read_b128 v[158:161], v149 offset:2048
	ds_read_b128 v[162:165], v149 offset:3072
	v_add_u32_e32 v149, s50, v146
	ds_read_b128 v[166:169], v149
	ds_read_b128 v[170:173], v149 offset:1024
	ds_read_b128 v[174:177], v149 offset:2048
	ds_read_b128 v[178:181], v149 offset:3072
	s_add_u32 s26, s26, 0x40000
	s_addc_u32 s27, s27, 0
	s_mov_b32 m0, s37
	v_lshl_add_u64 v[244:245], s[26:27], 0, v[132:133]
	ds_read_b128 v[182:185], v148 offset:32768
	ds_read_b128 v[186:189], v148 offset:33792
	ds_read_b128 v[190:193], v148 offset:34816
	ds_read_b128 v[194:197], v148 offset:35840
	ds_read_b128 v[210:213], v148 offset:36864
	ds_read_b128 v[226:229], v148 offset:37888
	ds_read_b128 v[230:233], v148 offset:38912
	ds_read_b128 v[234:237], v148 offset:39936
	s_mov_b32 m0, s17
	s_nop 0
	global_load_lds_dwordx4 v[240:241], off
	s_mov_b32 m0, s35
	s_nop 0
	global_load_lds_dwordx4 v[242:243], off
	s_mov_b32 m0, s37
	s_nop 0
	global_load_lds_dwordx4 v[244:245], off
	v_lshl_add_u64 v[244:245], s[26:27], 0, v[136:137]
	s_mov_b32 m0, s38
	s_nop 0
	global_load_lds_dwordx4 v[244:245], off
	s_waitcnt vmcnt(8)
	s_waitcnt lgkmcnt(0)
	s_barrier
	s_setprio 1
	s_waitcnt lgkmcnt(0)
	v_mfma_f32_16x16x32_bf16 v[128:131], v[150:153], v[182:185], v[128:131]
	v_mfma_f32_16x16x32_bf16 v[124:127], v[158:161], v[182:185], v[124:127]
	v_mfma_f32_16x16x32_bf16 v[120:123], v[150:153], v[190:193], v[120:123]
	v_mfma_f32_16x16x32_bf16 v[112:115], v[158:161], v[190:193], v[112:115]
	v_mfma_f32_16x16x32_bf16 v[104:107], v[150:153], v[210:213], v[104:107]
	v_mfma_f32_16x16x32_bf16 v[96:99], v[158:161], v[210:213], v[96:99]
	v_mfma_f32_16x16x32_bf16 v[88:91], v[150:153], v[230:233], v[88:91]
	v_mfma_f32_16x16x32_bf16 v[80:83], v[158:161], v[230:233], v[80:83]
	v_mfma_f32_16x16x32_bf16 v[128:131], v[154:157], v[186:189], v[128:131]
	v_mfma_f32_16x16x32_bf16 v[124:127], v[162:165], v[186:189], v[124:127]
	v_mfma_f32_16x16x32_bf16 v[120:123], v[154:157], v[194:197], v[120:123]
	v_mfma_f32_16x16x32_bf16 v[112:115], v[162:165], v[194:197], v[112:115]
	v_mfma_f32_16x16x32_bf16 v[104:107], v[154:157], v[226:229], v[104:107]
	v_mfma_f32_16x16x32_bf16 v[96:99], v[162:165], v[226:229], v[96:99]
	v_mfma_f32_16x16x32_bf16 v[88:91], v[154:157], v[234:237], v[88:91]
	v_mfma_f32_16x16x32_bf16 v[80:83], v[162:165], v[234:237], v[80:83]
	s_setprio 0
	s_setprio 1
	v_mfma_f32_16x16x32_bf16 v[116:119], v[166:169], v[182:185], v[116:119]
	v_mfma_f32_16x16x32_bf16 v[108:111], v[174:177], v[182:185], v[108:111]
	v_mfma_f32_16x16x32_bf16 v[100:103], v[166:169], v[190:193], v[100:103]
	v_mfma_f32_16x16x32_bf16 v[92:95], v[174:177], v[190:193], v[92:95]
	v_mfma_f32_16x16x32_bf16 v[84:87], v[166:169], v[210:213], v[84:87]
	v_mfma_f32_16x16x32_bf16 v[76:79], v[174:177], v[210:213], v[76:79]
	v_mfma_f32_16x16x32_bf16 v[72:75], v[166:169], v[230:233], v[72:75]
	v_mfma_f32_16x16x32_bf16 v[68:71], v[174:177], v[230:233], v[68:71]
	v_mfma_f32_16x16x32_bf16 v[116:119], v[170:173], v[186:189], v[116:119]
	v_mfma_f32_16x16x32_bf16 v[108:111], v[178:181], v[186:189], v[108:111]
	v_mfma_f32_16x16x32_bf16 v[100:103], v[170:173], v[194:197], v[100:103]
	v_mfma_f32_16x16x32_bf16 v[92:95], v[178:181], v[194:197], v[92:95]
	v_mfma_f32_16x16x32_bf16 v[84:87], v[170:173], v[226:229], v[84:87]
	v_mfma_f32_16x16x32_bf16 v[76:79], v[178:181], v[226:229], v[76:79]
	v_mfma_f32_16x16x32_bf16 v[72:75], v[170:173], v[234:237], v[72:75]
	v_mfma_f32_16x16x32_bf16 v[68:71], v[178:181], v[234:237], v[68:71]
	s_setprio 0
	s_barrier
	s_add_i32 s26, s49, s34
	v_lshl_add_u64 v[144:145], v[144:145], 0, s[64:65]
	s_mov_b32 m0, s26
	ds_read_b128 v[182:185], v148 offset:49152
	ds_read_b128 v[186:189], v148 offset:50176
	ds_read_b128 v[190:193], v148 offset:51200
	ds_read_b128 v[194:197], v148 offset:52224
	ds_read_b128 v[210:213], v148 offset:53248
	ds_read_b128 v[226:229], v148 offset:54272
	ds_read_b128 v[230:233], v148 offset:55296
	ds_read_b128 v[234:237], v148 offset:56320
	global_load_lds_dwordx4 v[144:145], off
	s_add_i32 m0, s26, 0x2000
	s_add_u32 s24, s24, 0x40080
	v_lshl_add_u64 v[144:145], v[238:239], 0, s[64:65]
	s_addc_u32 s25, s25, 0
	s_add_i32 s26, s50, s34
	global_load_lds_dwordx4 v[144:145], off
	v_lshl_add_u64 v[144:145], s[24:25], 0, v[134:135]
	s_mov_b32 m0, s26
	s_nop 0
	global_load_lds_dwordx4 v[144:145], off
	v_lshl_add_u64 v[144:145], s[24:25], 0, v[138:139]
	s_add_i32 m0, s26, 0x2000
	s_nop 0
	global_load_lds_dwordx4 v[144:145], off
	s_waitcnt vmcnt(6)
	s_waitcnt lgkmcnt(0)
	s_barrier
; #define PG8_STAGE(bufoff, gbase, voff) do { _Pragma("unroll") for (int _i = 0; _i < 2; ++_i) \
;         __builtin_amdgcn_global_load_lds((const unsigned*)((const char*)(gbase) + (voff)[_i]), (PG8_LAS unsigned*)(lds + (bufoff) + ldsw + _i * 8192), 16, 0, 0); } while (0)
; #define PG8_LDA(dst, b, h) do { _Pragma("unroll") for (int m = 0; m < 4; ++m) _Pragma("unroll") for (int k = 0; k < 2; ++k) dst[m][k] = *(const PG8_LAS bf16x8*)(lds + PG8_SA(b, h) + aoff + m * 2048 + k * 1024); } while (0)
; #define PG8_MMA(ai, bj, At, Bt) do { __builtin_amdgcn_s_setprio(1); _Pragma("unroll") for (int m = 0; m < 4; ++m) _Pragma("unroll") for (int n = 0; n < 2; ++n) _Pragma("unroll") for (int k = 0; k < 2; ++k) \
;         acc[ai][bj][m][n] = __builtin_amdgcn_mfma_f32_16x16x32_bf16(Bt[n][k], At[m][k], acc[ai][bj][m][n], 0, 0, 0); __builtin_amdgcn_s_setprio(0); } while (0)
; #define PG8_WAIT_V(n) asm volatile("s_waitcnt vmcnt(" #n ")" ::: "memory")
; #define PG8_WAIT_L(n) asm volatile("s_waitcnt lgkmcnt(" #n ")" ::: "memory")
; #define PG8_BAR __builtin_amdgcn_s_barrier()
; #define PG8_SCHED __builtin_amdgcn_sched_barrier(0)
; template <class Epi, class Sched, bool ALIGN_EPI = false, bool SP2 = false>
; __device__ __forceinline__ void gemm_phase(PG8_LAS unsigned char* lds, const Gemm g, const Sched& S, const Epi& E) {
;     ...
;             PG8_LDA(At, 1, 1); PG8_STAGE(PG8_SB(1, 0), b3, voffB); PG8_STAGE(PG8_SB(1, 1), b3 + hstepB, voffB); PG8_STAGE(PG8_SA(1, 0), a3, voffA);
;             PG8_WAIT_V(8); PG8_WAIT_L(0); PG8_BAR; PG8_MMA(1, 0, At, B0); PG8_MMA(1, 1, At, B1); PG8_BAR; PG8_SCHED;
;     ...
;         if constexpr (ALIGN_EPI) { if (wr == 0) PG8_BAR; }
	s_setprio 1
	s_waitcnt lgkmcnt(0)
	v_mfma_f32_16x16x32_bf16 v[64:67], v[150:153], v[182:185], v[64:67]
	v_mfma_f32_16x16x32_bf16 v[60:63], v[158:161], v[182:185], v[60:63]
	v_mfma_f32_16x16x32_bf16 v[56:59], v[150:153], v[190:193], v[56:59]
	v_mfma_f32_16x16x32_bf16 v[48:51], v[158:161], v[190:193], v[48:51]
	v_mfma_f32_16x16x32_bf16 v[40:43], v[150:153], v[210:213], v[40:43]
	v_mfma_f32_16x16x32_bf16 v[32:35], v[158:161], v[210:213], v[32:35]
	v_mfma_f32_16x16x32_bf16 v[24:27], v[150:153], v[230:233], v[24:27]
	v_mfma_f32_16x16x32_bf16 v[16:19], v[158:161], v[230:233], v[16:19]
	v_mfma_f32_16x16x32_bf16 v[64:67], v[154:157], v[186:189], v[64:67]
	v_mfma_f32_16x16x32_bf16 v[60:63], v[162:165], v[186:189], v[60:63]
	v_mfma_f32_16x16x32_bf16 v[56:59], v[154:157], v[194:197], v[56:59]
	v_mfma_f32_16x16x32_bf16 v[48:51], v[162:165], v[194:197], v[48:51]
	v_mfma_f32_16x16x32_bf16 v[40:43], v[154:157], v[226:229], v[40:43]
	v_mfma_f32_16x16x32_bf16 v[32:35], v[162:165], v[226:229], v[32:35]
	v_mfma_f32_16x16x32_bf16 v[24:27], v[154:157], v[234:237], v[24:27]
	v_mfma_f32_16x16x32_bf16 v[16:19], v[162:165], v[234:237], v[16:19]
	s_setprio 0
	s_setprio 1
	v_mfma_f32_16x16x32_bf16 v[52:55], v[166:169], v[182:185], v[52:55]
	v_mfma_f32_16x16x32_bf16 v[44:47], v[174:177], v[182:185], v[44:47]
	v_mfma_f32_16x16x32_bf16 v[36:39], v[166:169], v[190:193], v[36:39]
	v_mfma_f32_16x16x32_bf16 v[28:31], v[174:177], v[190:193], v[28:31]
	v_mfma_f32_16x16x32_bf16 v[20:23], v[166:169], v[210:213], v[20:23]
	v_mfma_f32_16x16x32_bf16 v[12:15], v[174:177], v[210:213], v[12:15]
	v_mfma_f32_16x16x32_bf16 v[8:11], v[166:169], v[230:233], v[8:11]
	v_mfma_f32_16x16x32_bf16 v[4:7], v[174:177], v[230:233], v[4:7]
	v_mfma_f32_16x16x32_bf16 v[52:55], v[170:173], v[186:189], v[52:55]
	v_mfma_f32_16x16x32_bf16 v[44:47], v[178:181], v[186:189], v[44:47]
	v_mfma_f32_16x16x32_bf16 v[36:39], v[170:173], v[194:197], v[36:39]
	v_mfma_f32_16x16x32_bf16 v[28:31], v[178:181], v[194:197], v[28:31]
	v_mfma_f32_16x16x32_bf16 v[20:23], v[170:173], v[226:229], v[20:23]
	v_mfma_f32_16x16x32_bf16 v[12:15], v[178:181], v[226:229], v[12:15]
	v_mfma_f32_16x16x32_bf16 v[8:11], v[170:173], v[234:237], v[8:11]
	v_mfma_f32_16x16x32_bf16 v[4:7], v[178:181], v[234:237], v[4:7]
	s_setprio 0
	s_barrier
	s_add_i32 s48, s48, 2
	s_add_u32 s46, s46, 0x100
	s_addc_u32 s47, s47, 0
	s_add_u32 s22, s22, 0x100
	s_addc_u32 s23, s23, 0
	s_cmp_gt_u32 s48, 13
	s_cbranch_scc0 .LBB0_1093
.Lpeel_exit_3:
	s_and_b64 vcc, exec, s[10:11]
	s_cbranch_vccz .LBB0_1096
	s_barrier
; #define PG8_BAR __builtin_amdgcn_s_barrier()
; __device__ __forceinline__ u32x4 pack8(const f32x4 a, const f32x4 b) { u32x4 w; w.x = cvt_pk_bf16(a[0], a[1]); w.y = cvt_pk_bf16(a[2], a[3]); w.z = cvt_pk_bf16(b[0], b[1]); w.w = cvt_pk_bf16(b[2], b[3]); return w; }
; template <class Epi, class Sched, bool ALIGN_EPI = false, bool SP2 = false>
; __device__ __forceinline__ void gemm_phase(PG8_LAS unsigned char* lds, const Gemm g, const Sched& S, const Epi& E) {
;     ...
;         if (!has_next) break;
; #pragma unroll
;         for (int a = 0; a < 2; ++a)
; #pragma unroll
;             for (int b = 0; b < 2; ++b)
; #pragma unroll
;                 for (int m = 0; m < 4; ++m)
; #pragma unroll
;                     for (int n = 0; n < 2; ++n) acc[a][b][m][n] = (f32x4){0.f, 0.f, 0.f, 0.f};
;         cur = nxt; cA = nA; cB = nB; ++ui;
;         if constexpr (ALIGN_EPI) { if (wr == 1) PG8_BAR; }
;     __device__ __forceinline__ void operator()(const f32x4 (&acc)[2][2][4][2], const Unit& u, int wr, int wc, int fr, int fq) const {
;         const int row0 = u.pm * BM + wr * 64 + fr, col0 = u.pn * BM + wc * 32 + 8 * fq;
; #pragma unroll
;         for (int ai = 0; ai < 2; ++ai)
; #pragma unroll
;             for (int m = 0; m < 4; ++m) {
;                 bf16_t* rowp = O + (size_t)(row0 + ai * HALF + m * 16) * ldc + col0;
; #pragma unroll
;                 for (int bj = 0; bj < 2; ++bj) *(u32x4*)(rowp + bj * HALF) = pack8(acc[ai][bj][m][0], acc[ai][bj][m][1]);
;             }
;     }
.LBB0_1096:
	v_lshl_add_u32 v150, s16, 8, v2
	v_lshl_or_b32 v144, s43, 8, v147
	v_ashrrev_i32_e32 v151, 31, v150
	v_ashrrev_i32_e32 v145, 31, v144
	v_lshlrev_b64 v[152:153], 11, v[150:151]
	v_lshl_add_u64 v[152:153], s[8:9], 0, v[152:153]
	v_lshlrev_b64 v[154:155], 1, v[144:145]
	v_lshl_add_u64 v[144:145], v[152:153], 0, v[154:155]
	v_cvt_pk_bf16_f32 v128, v128, v129
	v_cvt_pk_bf16_f32 v129, v130, v131
	v_cvt_pk_bf16_f32 v130, v124, v125
	v_cvt_pk_bf16_f32 v131, v126, v127
	flat_store_dwordx4 v[144:145], v[128:131] sc1
	v_cvt_pk_bf16_f32 v116, v116, v117
	v_cvt_pk_bf16_f32 v117, v118, v119
	v_cvt_pk_bf16_f32 v118, v108, v109
	v_or_b32_e32 v108, 16, v150
	v_ashrrev_i32_e32 v109, 31, v108
	v_lshlrev_b64 v[108:109], 11, v[108:109]
	v_lshl_add_u64 v[108:109], s[8:9], 0, v[108:109]
	v_cvt_pk_bf16_f32 v119, v110, v111
	flat_store_dwordx4 v[144:145], v[116:119] offset:256 sc1
	s_mov_b32 s13, 0x40000
	s_mov_b64 s[22:23], 0x40000
	v_lshl_add_u64 v[116:117], v[108:109], 0, v[154:155]
	v_cvt_pk_bf16_f32 v108, v120, v121
	v_cvt_pk_bf16_f32 v109, v122, v123
	v_cvt_pk_bf16_f32 v110, v112, v113
	v_cvt_pk_bf16_f32 v111, v114, v115
	flat_store_dwordx4 v[116:117], v[108:111] sc1
	v_cvt_pk_bf16_f32 v100, v100, v101
	v_cvt_pk_bf16_f32 v101, v102, v103
	v_cvt_pk_bf16_f32 v102, v92, v93
	v_or_b32_e32 v92, 32, v150
	v_ashrrev_i32_e32 v93, 31, v92
	v_lshlrev_b64 v[92:93], 11, v[92:93]
	v_lshl_add_u64 v[92:93], s[8:9], 0, v[92:93]
	v_cvt_pk_bf16_f32 v103, v94, v95
	flat_store_dwordx4 v[116:117], v[100:103] offset:256 sc1
	s_nop 1
	v_lshl_add_u64 v[100:101], v[92:93], 0, v[154:155]
	v_cvt_pk_bf16_f32 v92, v104, v105
	v_cvt_pk_bf16_f32 v93, v106, v107
	v_cvt_pk_bf16_f32 v94, v96, v97
	v_cvt_pk_bf16_f32 v95, v98, v99
	flat_store_dwordx4 v[100:101], v[92:95] sc1
	v_cvt_pk_bf16_f32 v84, v84, v85
	v_cvt_pk_bf16_f32 v85, v86, v87
	v_cvt_pk_bf16_f32 v86, v76, v77
	v_or_b32_e32 v76, 48, v150
	v_ashrrev_i32_e32 v77, 31, v76
	v_lshlrev_b64 v[76:77], 11, v[76:77]
	v_lshl_add_u64 v[76:77], s[8:9], 0, v[76:77]
	v_cvt_pk_bf16_f32 v87, v78, v79
	flat_store_dwordx4 v[100:101], v[84:87] offset:256 sc1
	s_nop 1
	v_lshl_add_u64 v[84:85], v[76:77], 0, v[154:155]
	v_cvt_pk_bf16_f32 v76, v88, v89
	v_cvt_pk_bf16_f32 v77, v90, v91
	v_cvt_pk_bf16_f32 v78, v80, v81
	v_cvt_pk_bf16_f32 v79, v82, v83
	flat_store_dwordx4 v[84:85], v[76:79] sc1
	v_cvt_pk_bf16_f32 v72, v72, v73
	v_cvt_pk_bf16_f32 v73, v74, v75
	v_cvt_pk_bf16_f32 v74, v68, v69
	v_cvt_pk_bf16_f32 v75, v70, v71
	flat_store_dwordx4 v[84:85], v[72:75] offset:256 sc1
	v_cvt_pk_bf16_f32 v64, v64, v65
	v_cvt_pk_bf16_f32 v65, v66, v67
	v_cvt_pk_bf16_f32 v66, v60, v61
	v_add_co_u32_e32 v60, vcc, s13, v144
	v_lshl_add_u64 v[68:69], v[144:145], 0, s[22:23]
	s_nop 0
	v_addc_co_u32_e32 v61, vcc, 0, v145, vcc
	s_mov_b32 s13, 0x48000
	v_cvt_pk_bf16_f32 v67, v62, v63
	flat_store_dwordx4 v[60:61], v[64:67] sc1
	v_cvt_pk_bf16_f32 v52, v52, v53
	v_cvt_pk_bf16_f32 v53, v54, v55
	v_cvt_pk_bf16_f32 v54, v44, v45
	v_cvt_pk_bf16_f32 v55, v46, v47
	flat_store_dwordx4 v[68:69], v[52:55] offset:256 sc1
	s_mov_b64 s[22:23], 0x48000
	v_cvt_pk_bf16_f32 v44, v56, v57
	v_cvt_pk_bf16_f32 v45, v58, v59
	v_cvt_pk_bf16_f32 v46, v48, v49
	v_add_co_u32_e32 v48, vcc, s13, v144
	v_lshl_add_u64 v[52:53], v[144:145], 0, s[22:23]
	s_nop 0
	v_addc_co_u32_e32 v49, vcc, 0, v145, vcc
	s_mov_b32 s13, 0x50000
	v_cvt_pk_bf16_f32 v47, v50, v51
	flat_store_dwordx4 v[48:49], v[44:47] sc1
	v_cvt_pk_bf16_f32 v36, v36, v37
	v_cvt_pk_bf16_f32 v37, v38, v39
	v_cvt_pk_bf16_f32 v38, v28, v29
	v_cvt_pk_bf16_f32 v39, v30, v31
	flat_store_dwordx4 v[52:53], v[36:39] offset:256 sc1
	s_mov_b64 s[22:23], 0x50000
	v_cvt_pk_bf16_f32 v28, v40, v41
	v_cvt_pk_bf16_f32 v29, v42, v43
	v_cvt_pk_bf16_f32 v30, v32, v33
	v_add_co_u32_e32 v32, vcc, s13, v144
	v_lshl_add_u64 v[36:37], v[144:145], 0, s[22:23]
	s_nop 0
	v_addc_co_u32_e32 v33, vcc, 0, v145, vcc
	s_mov_b32 s13, 0x58000
	v_cvt_pk_bf16_f32 v31, v34, v35
	flat_store_dwordx4 v[32:33], v[28:31] sc1
	v_cvt_pk_bf16_f32 v20, v20, v21
	v_cvt_pk_bf16_f32 v21, v22, v23
	v_cvt_pk_bf16_f32 v22, v12, v13
	v_cvt_pk_bf16_f32 v23, v14, v15
	flat_store_dwordx4 v[36:37], v[20:23] offset:256 sc1
	v_cvt_pk_bf16_f32 v12, v24, v25
	v_cvt_pk_bf16_f32 v13, v26, v27
	v_cvt_pk_bf16_f32 v14, v16, v17
	v_add_co_u32_e32 v16, vcc, s13, v144
	s_mov_b64 s[22:23], 0x58000
	s_nop 0
	v_addc_co_u32_e32 v17, vcc, 0, v145, vcc
	v_lshl_add_u64 v[20:21], v[144:145], 0, s[22:23]
	s_andn2_b64 vcc, exec, s[4:5]
	s_mov_b64 s[4:5], -1
	v_cvt_pk_bf16_f32 v15, v18, v19
	flat_store_dwordx4 v[16:17], v[12:15] sc1
	v_cvt_pk_bf16_f32 v8, v8, v9
	v_cvt_pk_bf16_f32 v9, v10, v11
	v_cvt_pk_bf16_f32 v10, v4, v5
	v_cvt_pk_bf16_f32 v11, v6, v7
	flat_store_dwordx4 v[20:21], v[8:11] offset:256 sc1
	s_cbranch_vccnz .LBB0_1085
	s_andn2_b64 vcc, exec, s[6:7]
	s_cbranch_vccnz .LBB0_1084
	s_barrier
	s_branch .LBB0_1084

; #define PG8_STR(x) PG8_STR2(x)
; #define PG8_STAGE(bufoff, gbase, voff) do { _Pragma("unroll") for (int _i = 0; _i < 2; ++_i) \
;         __builtin_amdgcn_global_load_lds((const unsigned*)((const char*)(gbase) + (voff)[_i]), (PG8_LAS unsigned*)(lds + (bufoff) + ldsw + _i * 8192), 16, 0, 0); } while (0)
; #define PG8_LDA(dst, b, h) do { _Pragma("unroll") for (int m = 0; m < 4; ++m) _Pragma("unroll") for (int k = 0; k < 2; ++k) dst[m][k] = *(const PG8_LAS bf16x8*)(lds + PG8_SA(b, h) + aoff + m * 2048 + k * 1024); } while (0)
; #define PG8_LDB(dst, b, h) do { _Pragma("unroll") for (int n = 0; n < 2; ++n) _Pragma("unroll") for (int k = 0; k < 2; ++k) dst[n][k] = *(const PG8_LAS bf16x8*)(lds + PG8_SB(b, h) + boff + n * 2048 + k * 1024); } while (0)
; #define PG8_MMA(ai, bj, At, Bt) do { __builtin_amdgcn_s_setprio(1); _Pragma("unroll") for (int m = 0; m < 4; ++m) _Pragma("unroll") for (int n = 0; n < 2; ++n) _Pragma("unroll") for (int k = 0; k < 2; ++k) \
;         acc[ai][bj][m][n] = __builtin_amdgcn_mfma_f32_16x16x32_bf16(Bt[n][k], At[m][k], acc[ai][bj][m][n], 0, 0, 0); __builtin_amdgcn_s_setprio(0); } while (0)
; template <class Epi, class Sched, bool ALIGN_EPI = false, bool SP2 = false>
; __device__ __forceinline__ void gemm_phase(PG8_LAS unsigned char* lds, const Gemm g, const Sched& S, const Epi& E) {
;     ...
;         for (int t = 0; t < nt; t += 2) {
;     ...
;             asm volatile(".p2align 6\n\t.rept " PG8_STR(KLOOP_ALIGN) "\n\ts_nop 0\n\t.endr");
;     ...
;             const bool last = (t == nt - 2);
;             const char* a1 = cA + (size_t)(t + 1) * kstep;
;             const char* a2 = last ? nA : cA + (size_t)(t + 2) * kstep; const char* b2 = last ? nB : cB + (size_t)(t + 2) * kstep;
;             const char* a3 = a2 + kstep; const char* b3 = b2 + kstep;
;             if (last && has_next) S.a_ready(nxt);
;             if constexpr (SP2) {
;             PG8_LDB(B0, 0, 0); PG8_LDB(B1, 0, 1); PG8_SCHED; PG8_LDA(At, 0, 0); PG8_STAGE(PG8_SA(1, 1), a1 + hstepA, voffA);
;             PG8_WAIT_V(8); PG8_WAIT_L(0); PG8_BAR; PG8_MMA(0, 0, At, B0); PG8_MMA(0, 1, At, B1); PG8_BAR; PG8_SCHED;
;             PG8_LDA(At, 0, 1); PG8_STAGE(PG8_SB(0, 0), b2, voffB); PG8_STAGE(PG8_SB(0, 1), b2 + hstepB, voffB); PG8_STAGE(PG8_SA(0, 0), a2, voffA);
;             PG8_WAIT_V(8); PG8_WAIT_L(0); PG8_BAR; PG8_MMA(1, 0, At, B0); PG8_MMA(1, 1, At, B1); PG8_BAR; PG8_SCHED;
.LBB0_1160:
	s_mov_b64 s[24:25], s[4:5]
	s_and_b64 s[4:5], s[16:17], exec
	s_mov_b64 s[22:23], s[6:7]
	s_cselect_b32 s6, s42, s42
	s_cselect_b32 s4, s43, s43
	s_ashr_i32 s7, s6, 31
	s_lshl_b64 s[6:7], s[6:7], 19
	s_add_u32 s6, s0, s6
	s_addc_u32 s7, s1, s7
	s_and_b64 s[26:27], s[16:17], exec
	s_cselect_b32 s19, s7, s23
	s_cselect_b32 s21, s6, s22
	s_ashr_i32 s5, s4, 31
	s_lshl_b64 s[4:5], s[4:5], 19
	s_add_u32 s4, s28, s4
	s_addc_u32 s5, s29, s5
	s_and_b64 s[26:27], s[16:17], exec
	s_cselect_b32 s44, s5, s25
	s_cselect_b32 s45, s4, s24
	s_add_u32 s46, s24, 0x100
	s_addc_u32 s47, s25, 0
	s_add_u32 s22, s22, 0x40080
	s_addc_u32 s23, s23, 0
	s_mov_b32 s48, -2
	s_add_u32 s24, s22, 0xfffc0080
	s_addc_u32 s25, s23, -1
	s_add_i32 s49, 0, 0x10000
	s_cmp_eq_u32 s48, 12
	s_cselect_b32 s27, s19, s25
	s_cselect_b32 s26, s21, s24
	v_add_u32_e32 v149, s49, v154
	s_cselect_b32 s25, s44, s47
	s_cselect_b32 s24, s45, s46
	s_add_i32 s52, 0, 0x14000
	ds_read_b128 v[150:153], v149
	ds_read_b128 v[156:159], v149 offset:1024
	ds_read_b128 v[160:163], v149 offset:2048
	ds_read_b128 v[164:167], v149 offset:3072
	v_add_u32_e32 v149, s52, v154
	ds_read_b128 v[168:171], v149
	ds_read_b128 v[172:175], v149 offset:1024
	ds_read_b128 v[176:179], v149 offset:2048
	ds_read_b128 v[180:183], v149 offset:3072
	v_lshl_add_u64 v[196:197], s[22:23], 0, v[146:147]
	s_add_i32 m0, s31, 0xc000
	ds_read_b128 v[184:187], v155
	ds_read_b128 v[188:191], v155 offset:1024
	ds_read_b128 v[192:195], v155 offset:2048
	ds_read_b128 v[210:213], v155 offset:3072
	ds_read_b128 v[226:229], v155 offset:4096
	ds_read_b128 v[230:233], v155 offset:5120
	ds_read_b128 v[234:237], v155 offset:6144
	ds_read_b128 v[238:241], v155 offset:7168
	v_lshl_add_u64 v[248:249], v[244:245], 0, s[64:65]
	s_mov_b32 m0, s38
	s_nop 0
	global_load_lds_dwordx4 v[248:249], off
	v_lshl_add_u64 v[248:249], v[246:247], 0, s[64:65]
	s_mov_b32 m0, s39
	s_nop 0
	global_load_lds_dwordx4 v[248:249], off
	s_add_i32 m0, s31, 0xc000
	s_nop 0
	global_load_lds_dwordx4 v[196:197], off
	v_lshl_add_u64 v[196:197], s[22:23], 0, v[144:145]
	s_add_i32 m0, s31, 0xe000
	s_nop 0
	global_load_lds_dwordx4 v[196:197], off
	s_waitcnt vmcnt(8)
	s_waitcnt lgkmcnt(0)
	s_barrier
	s_setprio 1
	s_waitcnt lgkmcnt(0)
	v_mfma_f32_16x16x32_bf16 v[128:131], v[150:153], v[184:187], 0
	v_mfma_f32_16x16x32_bf16 v[124:127], v[160:163], v[184:187], 0
	v_mfma_f32_16x16x32_bf16 v[112:115], v[150:153], v[192:195], 0
	v_mfma_f32_16x16x32_bf16 v[108:111], v[160:163], v[192:195], 0
	v_mfma_f32_16x16x32_bf16 v[96:99], v[150:153], v[226:229], 0
	v_mfma_f32_16x16x32_bf16 v[92:95], v[160:163], v[226:229], 0
	v_mfma_f32_16x16x32_bf16 v[80:83], v[150:153], v[234:237], 0
	v_mfma_f32_16x16x32_bf16 v[76:79], v[160:163], v[234:237], 0
	v_mfma_f32_16x16x32_bf16 v[128:131], v[156:159], v[188:191], v[128:131]
	v_mfma_f32_16x16x32_bf16 v[124:127], v[164:167], v[188:191], v[124:127]
	v_mfma_f32_16x16x32_bf16 v[112:115], v[156:159], v[210:213], v[112:115]
	v_mfma_f32_16x16x32_bf16 v[108:111], v[164:167], v[210:213], v[108:111]
	v_mfma_f32_16x16x32_bf16 v[96:99], v[156:159], v[230:233], v[96:99]
	v_mfma_f32_16x16x32_bf16 v[92:95], v[164:167], v[230:233], v[92:95]
	v_mfma_f32_16x16x32_bf16 v[80:83], v[156:159], v[238:241], v[80:83]
	v_mfma_f32_16x16x32_bf16 v[76:79], v[164:167], v[238:241], v[76:79]
	s_setprio 0
	s_setprio 1
	v_mfma_f32_16x16x32_bf16 v[120:123], v[168:171], v[184:187], 0
	v_mfma_f32_16x16x32_bf16 v[116:119], v[176:179], v[184:187], 0
	v_mfma_f32_16x16x32_bf16 v[104:107], v[168:171], v[192:195], 0
	v_mfma_f32_16x16x32_bf16 v[100:103], v[176:179], v[192:195], 0
	v_mfma_f32_16x16x32_bf16 v[88:91], v[168:171], v[226:229], 0
	v_mfma_f32_16x16x32_bf16 v[84:87], v[176:179], v[226:229], 0
	v_mfma_f32_16x16x32_bf16 v[72:75], v[168:171], v[234:237], 0
	v_mfma_f32_16x16x32_bf16 v[68:71], v[176:179], v[234:237], 0
	v_mfma_f32_16x16x32_bf16 v[120:123], v[172:175], v[188:191], v[120:123]
	v_mfma_f32_16x16x32_bf16 v[116:119], v[180:183], v[188:191], v[116:119]
	v_mfma_f32_16x16x32_bf16 v[104:107], v[172:175], v[210:213], v[104:107]
	v_mfma_f32_16x16x32_bf16 v[100:103], v[180:183], v[210:213], v[100:103]
	v_mfma_f32_16x16x32_bf16 v[88:91], v[172:175], v[230:233], v[88:91]
	v_mfma_f32_16x16x32_bf16 v[84:87], v[180:183], v[230:233], v[84:87]
	v_mfma_f32_16x16x32_bf16 v[72:75], v[172:175], v[238:241], v[72:75]
	v_mfma_f32_16x16x32_bf16 v[68:71], v[180:183], v[238:241], v[68:71]
	s_setprio 0
	s_barrier
	s_add_i32 s49, s49, s30
	v_lshl_add_u64 v[196:197], s[24:25], 0, v[134:135]
	s_mov_b32 m0, s49
	ds_read_b128 v[184:187], v155 offset:16384
	ds_read_b128 v[188:191], v155 offset:17408
	ds_read_b128 v[192:195], v155 offset:18432
	ds_read_b128 v[210:213], v155 offset:19456
	ds_read_b128 v[226:229], v155 offset:20480
	ds_read_b128 v[230:233], v155 offset:21504
	ds_read_b128 v[234:237], v155 offset:22528
	ds_read_b128 v[238:241], v155 offset:23552
	global_load_lds_dwordx4 v[196:197], off
	s_add_i32 m0, s49, 0x2000
	s_add_u32 s50, s24, 0x40000
	v_lshl_add_u64 v[242:243], s[24:25], 0, v[138:139]
	s_addc_u32 s51, s25, 0
	s_add_i32 s49, s52, s30
	global_load_lds_dwordx4 v[242:243], off
	v_lshl_add_u64 v[244:245], s[50:51], 0, v[134:135]
	s_mov_b32 m0, s49
	v_lshl_add_u64 v[246:247], s[26:27], 0, v[136:137]
	global_load_lds_dwordx4 v[244:245], off
	v_lshl_add_u64 v[244:245], s[50:51], 0, v[138:139]
	s_add_i32 m0, s49, 0x2000
	s_nop 0
	global_load_lds_dwordx4 v[244:245], off
	v_lshl_add_u64 v[244:245], s[26:27], 0, v[132:133]
	s_waitcnt vmcnt(6)
	s_waitcnt lgkmcnt(0)
	s_barrier
; #define PG8_STAGE(bufoff, gbase, voff) do { _Pragma("unroll") for (int _i = 0; _i < 2; ++_i) \
;         __builtin_amdgcn_global_load_lds((const unsigned*)((const char*)(gbase) + (voff)[_i]), (PG8_LAS unsigned*)(lds + (bufoff) + ldsw + _i * 8192), 16, 0, 0); } while (0)
; #define PG8_LDA(dst, b, h) do { _Pragma("unroll") for (int m = 0; m < 4; ++m) _Pragma("unroll") for (int k = 0; k < 2; ++k) dst[m][k] = *(const PG8_LAS bf16x8*)(lds + PG8_SA(b, h) + aoff + m * 2048 + k * 1024); } while (0)
; #define PG8_LDB(dst, b, h) do { _Pragma("unroll") for (int n = 0; n < 2; ++n) _Pragma("unroll") for (int k = 0; k < 2; ++k) dst[n][k] = *(const PG8_LAS bf16x8*)(lds + PG8_SB(b, h) + boff + n * 2048 + k * 1024); } while (0)
; #define PG8_MMA(ai, bj, At, Bt) do { __builtin_amdgcn_s_setprio(1); _Pragma("unroll") for (int m = 0; m < 4; ++m) _Pragma("unroll") for (int n = 0; n < 2; ++n) _Pragma("unroll") for (int k = 0; k < 2; ++k) \
;         acc[ai][bj][m][n] = __builtin_amdgcn_mfma_f32_16x16x32_bf16(Bt[n][k], At[m][k], acc[ai][bj][m][n], 0, 0, 0); __builtin_amdgcn_s_setprio(0); } while (0)
; #define PG8_WAIT_V(n) asm volatile("s_waitcnt vmcnt(" #n ")" ::: "memory")
; #define PG8_WAIT_L(n) asm volatile("s_waitcnt lgkmcnt(" #n ")" ::: "memory")
; #define PG8_BAR __builtin_amdgcn_s_barrier()
; #define PG8_SCHED __builtin_amdgcn_sched_barrier(0)
; template <class Epi, class Sched, bool ALIGN_EPI = false, bool SP2 = false>
; __device__ __forceinline__ void gemm_phase(PG8_LAS unsigned char* lds, const Gemm g, const Sched& S, const Epi& E) {
;     ...
;             PG8_LDA(At, 0, 1); PG8_STAGE(PG8_SB(0, 0), b2, voffB); PG8_STAGE(PG8_SB(0, 1), b2 + hstepB, voffB); PG8_STAGE(PG8_SA(0, 0), a2, voffA);
;             PG8_WAIT_V(8); PG8_WAIT_L(0); PG8_BAR; PG8_MMA(1, 0, At, B0); PG8_MMA(1, 1, At, B1); PG8_BAR; PG8_SCHED;
;             PG8_LDB(B0, 1, 0); PG8_LDB(B1, 1, 1); PG8_SCHED; PG8_LDA(At, 1, 0); PG8_STAGE(PG8_SA(0, 1), a2 + hstepA, voffA);
;             PG8_WAIT_V(8); PG8_WAIT_L(0); PG8_BAR; PG8_MMA(0, 0, At, B0); PG8_MMA(0, 1, At, B1); PG8_BAR; PG8_SCHED;
	s_setprio 1
	s_waitcnt lgkmcnt(0)
	v_mfma_f32_16x16x32_bf16 v[64:67], v[150:153], v[184:187], 0
	v_mfma_f32_16x16x32_bf16 v[60:63], v[160:163], v[184:187], 0
	v_mfma_f32_16x16x32_bf16 v[52:55], v[150:153], v[192:195], 0
	v_mfma_f32_16x16x32_bf16 v[44:47], v[160:163], v[192:195], 0
	v_mfma_f32_16x16x32_bf16 v[36:39], v[150:153], v[226:229], 0
	v_mfma_f32_16x16x32_bf16 v[28:31], v[160:163], v[226:229], 0
	v_mfma_f32_16x16x32_bf16 v[20:23], v[150:153], v[234:237], 0
	v_mfma_f32_16x16x32_bf16 v[12:15], v[160:163], v[234:237], 0
	v_mfma_f32_16x16x32_bf16 v[64:67], v[156:159], v[188:191], v[64:67]
	v_mfma_f32_16x16x32_bf16 v[60:63], v[164:167], v[188:191], v[60:63]
	v_mfma_f32_16x16x32_bf16 v[52:55], v[156:159], v[210:213], v[52:55]
	v_mfma_f32_16x16x32_bf16 v[44:47], v[164:167], v[210:213], v[44:47]
	v_mfma_f32_16x16x32_bf16 v[36:39], v[156:159], v[230:233], v[36:39]
	v_mfma_f32_16x16x32_bf16 v[28:31], v[164:167], v[230:233], v[28:31]
	v_mfma_f32_16x16x32_bf16 v[20:23], v[156:159], v[238:241], v[20:23]
	v_mfma_f32_16x16x32_bf16 v[12:15], v[164:167], v[238:241], v[12:15]
	s_setprio 0
	s_setprio 1
	v_mfma_f32_16x16x32_bf16 v[56:59], v[168:171], v[184:187], 0
	v_mfma_f32_16x16x32_bf16 v[48:51], v[176:179], v[184:187], 0
	v_mfma_f32_16x16x32_bf16 v[40:43], v[168:171], v[192:195], 0
	v_mfma_f32_16x16x32_bf16 v[32:35], v[176:179], v[192:195], 0
	v_mfma_f32_16x16x32_bf16 v[24:27], v[168:171], v[226:229], 0
	v_mfma_f32_16x16x32_bf16 v[16:19], v[176:179], v[226:229], 0
	v_mfma_f32_16x16x32_bf16 v[8:11], v[168:171], v[234:237], 0
	v_mfma_f32_16x16x32_bf16 v[4:7], v[176:179], v[234:237], 0
	v_mfma_f32_16x16x32_bf16 v[56:59], v[172:175], v[188:191], v[56:59]
	v_mfma_f32_16x16x32_bf16 v[48:51], v[180:183], v[188:191], v[48:51]
	v_mfma_f32_16x16x32_bf16 v[40:43], v[172:175], v[210:213], v[40:43]
	v_mfma_f32_16x16x32_bf16 v[32:35], v[180:183], v[210:213], v[32:35]
	v_mfma_f32_16x16x32_bf16 v[24:27], v[172:175], v[230:233], v[24:27]
	v_mfma_f32_16x16x32_bf16 v[16:19], v[180:183], v[230:233], v[16:19]
	v_mfma_f32_16x16x32_bf16 v[8:11], v[172:175], v[238:241], v[8:11]
	v_mfma_f32_16x16x32_bf16 v[4:7], v[180:183], v[238:241], v[4:7]
	s_setprio 0
	s_barrier
	s_add_i32 s49, 0, 0x18000
	v_add_u32_e32 v149, s49, v154
	s_add_i32 s50, 0, 0x1c000
	ds_read_b128 v[150:153], v149
	ds_read_b128 v[156:159], v149 offset:1024
	ds_read_b128 v[160:163], v149 offset:2048
	ds_read_b128 v[164:167], v149 offset:3072
	v_add_u32_e32 v149, s50, v154
	ds_read_b128 v[168:171], v149
	ds_read_b128 v[172:175], v149 offset:1024
	ds_read_b128 v[176:179], v149 offset:2048
	ds_read_b128 v[180:183], v149 offset:3072
	s_add_u32 s26, s26, 0x40000
	s_addc_u32 s27, s27, 0
	s_mov_b32 m0, s34
	v_lshl_add_u64 v[248:249], s[26:27], 0, v[132:133]
	ds_read_b128 v[184:187], v155 offset:32768
	ds_read_b128 v[188:191], v155 offset:33792
	ds_read_b128 v[192:195], v155 offset:34816
	ds_read_b128 v[210:213], v155 offset:35840
	ds_read_b128 v[226:229], v155 offset:36864
	ds_read_b128 v[230:233], v155 offset:37888
	ds_read_b128 v[234:237], v155 offset:38912
	ds_read_b128 v[238:241], v155 offset:39936
	s_mov_b32 m0, s31
	s_nop 0
	global_load_lds_dwordx4 v[244:245], off
	s_mov_b32 m0, s33
	s_nop 0
	global_load_lds_dwordx4 v[246:247], off
	s_mov_b32 m0, s34
	s_nop 0
	global_load_lds_dwordx4 v[248:249], off
	v_lshl_add_u64 v[248:249], s[26:27], 0, v[136:137]
	s_mov_b32 m0, s35
	s_nop 0
	global_load_lds_dwordx4 v[248:249], off
	s_waitcnt vmcnt(8)
	s_waitcnt lgkmcnt(0)
	s_barrier
; #define PG8_STAGE(bufoff, gbase, voff) do { _Pragma("unroll") for (int _i = 0; _i < 2; ++_i) \
;         __builtin_amdgcn_global_load_lds((const unsigned*)((const char*)(gbase) + (voff)[_i]), (PG8_LAS unsigned*)(lds + (bufoff) + ldsw + _i * 8192), 16, 0, 0); } while (0)
; #define PG8_LDA(dst, b, h) do { _Pragma("unroll") for (int m = 0; m < 4; ++m) _Pragma("unroll") for (int k = 0; k < 2; ++k) dst[m][k] = *(const PG8_LAS bf16x8*)(lds + PG8_SA(b, h) + aoff + m * 2048 + k * 1024); } while (0)
; #define PG8_LDB(dst, b, h) do { _Pragma("unroll") for (int n = 0; n < 2; ++n) _Pragma("unroll") for (int k = 0; k < 2; ++k) dst[n][k] = *(const PG8_LAS bf16x8*)(lds + PG8_SB(b, h) + boff + n * 2048 + k * 1024); } while (0)
; #define PG8_MMA(ai, bj, At, Bt) do { __builtin_amdgcn_s_setprio(1); _Pragma("unroll") for (int m = 0; m < 4; ++m) _Pragma("unroll") for (int n = 0; n < 2; ++n) _Pragma("unroll") for (int k = 0; k < 2; ++k) \
;         acc[ai][bj][m][n] = __builtin_amdgcn_mfma_f32_16x16x32_bf16(Bt[n][k], At[m][k], acc[ai][bj][m][n], 0, 0, 0); __builtin_amdgcn_s_setprio(0); } while (0)
; #define PG8_WAIT_V(n) asm volatile("s_waitcnt vmcnt(" #n ")" ::: "memory")
; #define PG8_WAIT_L(n) asm volatile("s_waitcnt lgkmcnt(" #n ")" ::: "memory")
; #define PG8_BAR __builtin_amdgcn_s_barrier()
; #define PG8_SCHED __builtin_amdgcn_sched_barrier(0)
; template <class Epi, class Sched, bool ALIGN_EPI = false, bool SP2 = false>
; __device__ __forceinline__ void gemm_phase(PG8_LAS unsigned char* lds, const Gemm g, const Sched& S, const Epi& E) {
;     ...
;             PG8_LDB(B0, 1, 0); PG8_LDB(B1, 1, 1); PG8_SCHED; PG8_LDA(At, 1, 0); PG8_STAGE(PG8_SA(0, 1), a2 + hstepA, voffA);
;             PG8_WAIT_V(8); PG8_WAIT_L(0); PG8_BAR; PG8_MMA(0, 0, At, B0); PG8_MMA(0, 1, At, B1); PG8_BAR; PG8_SCHED;
;             PG8_LDA(At, 1, 1); PG8_STAGE(PG8_SB(1, 0), b3, voffB); PG8_STAGE(PG8_SB(1, 1), b3 + hstepB, voffB); PG8_STAGE(PG8_SA(1, 0), a3, voffA);
;             PG8_WAIT_V(8); PG8_WAIT_L(0); PG8_BAR; PG8_MMA(1, 0, At, B0); PG8_MMA(1, 1, At, B1); PG8_BAR; PG8_SCHED;
	s_setprio 1
	s_waitcnt lgkmcnt(0)
	v_mfma_f32_16x16x32_bf16 v[128:131], v[150:153], v[184:187], v[128:131]
	v_mfma_f32_16x16x32_bf16 v[124:127], v[160:163], v[184:187], v[124:127]
	v_mfma_f32_16x16x32_bf16 v[112:115], v[150:153], v[192:195], v[112:115]
	v_mfma_f32_16x16x32_bf16 v[108:111], v[160:163], v[192:195], v[108:111]
	v_mfma_f32_16x16x32_bf16 v[96:99], v[150:153], v[226:229], v[96:99]
	v_mfma_f32_16x16x32_bf16 v[92:95], v[160:163], v[226:229], v[92:95]
	v_mfma_f32_16x16x32_bf16 v[80:83], v[150:153], v[234:237], v[80:83]
	v_mfma_f32_16x16x32_bf16 v[76:79], v[160:163], v[234:237], v[76:79]
	v_mfma_f32_16x16x32_bf16 v[128:131], v[156:159], v[188:191], v[128:131]
	v_mfma_f32_16x16x32_bf16 v[124:127], v[164:167], v[188:191], v[124:127]
	v_mfma_f32_16x16x32_bf16 v[112:115], v[156:159], v[210:213], v[112:115]
	v_mfma_f32_16x16x32_bf16 v[108:111], v[164:167], v[210:213], v[108:111]
	v_mfma_f32_16x16x32_bf16 v[96:99], v[156:159], v[230:233], v[96:99]
	v_mfma_f32_16x16x32_bf16 v[92:95], v[164:167], v[230:233], v[92:95]
	v_mfma_f32_16x16x32_bf16 v[80:83], v[156:159], v[238:241], v[80:83]
	v_mfma_f32_16x16x32_bf16 v[76:79], v[164:167], v[238:241], v[76:79]
	s_setprio 0
	s_setprio 1
	v_mfma_f32_16x16x32_bf16 v[120:123], v[168:171], v[184:187], v[120:123]
	v_mfma_f32_16x16x32_bf16 v[116:119], v[176:179], v[184:187], v[116:119]
	v_mfma_f32_16x16x32_bf16 v[104:107], v[168:171], v[192:195], v[104:107]
	v_mfma_f32_16x16x32_bf16 v[100:103], v[176:179], v[192:195], v[100:103]
	v_mfma_f32_16x16x32_bf16 v[88:91], v[168:171], v[226:229], v[88:91]
	v_mfma_f32_16x16x32_bf16 v[84:87], v[176:179], v[226:229], v[84:87]
	v_mfma_f32_16x16x32_bf16 v[72:75], v[168:171], v[234:237], v[72:75]
	v_mfma_f32_16x16x32_bf16 v[68:71], v[176:179], v[234:237], v[68:71]
	v_mfma_f32_16x16x32_bf16 v[120:123], v[172:175], v[188:191], v[120:123]
	v_mfma_f32_16x16x32_bf16 v[116:119], v[180:183], v[188:191], v[116:119]
	v_mfma_f32_16x16x32_bf16 v[104:107], v[172:175], v[210:213], v[104:107]
	v_mfma_f32_16x16x32_bf16 v[100:103], v[180:183], v[210:213], v[100:103]
	v_mfma_f32_16x16x32_bf16 v[88:91], v[172:175], v[230:233], v[88:91]
	v_mfma_f32_16x16x32_bf16 v[84:87], v[180:183], v[230:233], v[84:87]
	v_mfma_f32_16x16x32_bf16 v[72:75], v[172:175], v[238:241], v[72:75]
	v_mfma_f32_16x16x32_bf16 v[68:71], v[180:183], v[238:241], v[68:71]
	s_setprio 0
	s_barrier
	s_add_i32 s26, s49, s30
	v_lshl_add_u64 v[196:197], v[196:197], 0, s[64:65]
	s_mov_b32 m0, s26
	ds_read_b128 v[184:187], v155 offset:49152
	ds_read_b128 v[188:191], v155 offset:50176
	ds_read_b128 v[192:195], v155 offset:51200
	ds_read_b128 v[210:213], v155 offset:52224
	ds_read_b128 v[226:229], v155 offset:53248
	ds_read_b128 v[230:233], v155 offset:54272
	ds_read_b128 v[234:237], v155 offset:55296
	ds_read_b128 v[238:241], v155 offset:56320
	global_load_lds_dwordx4 v[196:197], off
	s_add_i32 m0, s26, 0x2000
	s_add_u32 s24, s24, 0x40080
	v_lshl_add_u64 v[196:197], v[242:243], 0, s[64:65]
	s_addc_u32 s25, s25, 0
	s_add_i32 s26, s50, s30
	global_load_lds_dwordx4 v[196:197], off
	v_lshl_add_u64 v[196:197], s[24:25], 0, v[134:135]
	s_mov_b32 m0, s26
	s_nop 0
	global_load_lds_dwordx4 v[196:197], off
	v_lshl_add_u64 v[196:197], s[24:25], 0, v[138:139]
	s_add_i32 m0, s26, 0x2000
	s_nop 0
	global_load_lds_dwordx4 v[196:197], off
	s_waitcnt vmcnt(6)
	s_waitcnt lgkmcnt(0)
	s_barrier
	s_setprio 1
	s_waitcnt lgkmcnt(0)
	v_mfma_f32_16x16x32_bf16 v[64:67], v[150:153], v[184:187], v[64:67]
	v_mfma_f32_16x16x32_bf16 v[60:63], v[160:163], v[184:187], v[60:63]
	v_mfma_f32_16x16x32_bf16 v[52:55], v[150:153], v[192:195], v[52:55]
	v_mfma_f32_16x16x32_bf16 v[44:47], v[160:163], v[192:195], v[44:47]
	v_mfma_f32_16x16x32_bf16 v[36:39], v[150:153], v[226:229], v[36:39]
	v_mfma_f32_16x16x32_bf16 v[28:31], v[160:163], v[226:229], v[28:31]
	v_mfma_f32_16x16x32_bf16 v[20:23], v[150:153], v[234:237], v[20:23]
	v_mfma_f32_16x16x32_bf16 v[12:15], v[160:163], v[234:237], v[12:15]
	v_mfma_f32_16x16x32_bf16 v[64:67], v[156:159], v[188:191], v[64:67]
	v_mfma_f32_16x16x32_bf16 v[60:63], v[164:167], v[188:191], v[60:63]
	v_mfma_f32_16x16x32_bf16 v[52:55], v[156:159], v[210:213], v[52:55]
	v_mfma_f32_16x16x32_bf16 v[44:47], v[164:167], v[210:213], v[44:47]
	v_mfma_f32_16x16x32_bf16 v[36:39], v[156:159], v[230:233], v[36:39]
	v_mfma_f32_16x16x32_bf16 v[28:31], v[164:167], v[230:233], v[28:31]
	v_mfma_f32_16x16x32_bf16 v[20:23], v[156:159], v[238:241], v[20:23]
	v_mfma_f32_16x16x32_bf16 v[12:15], v[164:167], v[238:241], v[12:15]
	s_setprio 0
	s_setprio 1
	v_mfma_f32_16x16x32_bf16 v[56:59], v[168:171], v[184:187], v[56:59]
	v_mfma_f32_16x16x32_bf16 v[48:51], v[176:179], v[184:187], v[48:51]
	v_mfma_f32_16x16x32_bf16 v[40:43], v[168:171], v[192:195], v[40:43]
	v_mfma_f32_16x16x32_bf16 v[32:35], v[176:179], v[192:195], v[32:35]
	v_mfma_f32_16x16x32_bf16 v[24:27], v[168:171], v[226:229], v[24:27]
	v_mfma_f32_16x16x32_bf16 v[16:19], v[176:179], v[226:229], v[16:19]
	v_mfma_f32_16x16x32_bf16 v[8:11], v[168:171], v[234:237], v[8:11]
	v_mfma_f32_16x16x32_bf16 v[4:7], v[176:179], v[234:237], v[4:7]
	v_mfma_f32_16x16x32_bf16 v[56:59], v[172:175], v[188:191], v[56:59]
	v_mfma_f32_16x16x32_bf16 v[48:51], v[180:183], v[188:191], v[48:51]
	v_mfma_f32_16x16x32_bf16 v[40:43], v[172:175], v[210:213], v[40:43]
	v_mfma_f32_16x16x32_bf16 v[32:35], v[180:183], v[210:213], v[32:35]
	v_mfma_f32_16x16x32_bf16 v[24:27], v[172:175], v[230:233], v[24:27]
	v_mfma_f32_16x16x32_bf16 v[16:19], v[180:183], v[230:233], v[16:19]
	v_mfma_f32_16x16x32_bf16 v[8:11], v[172:175], v[238:241], v[8:11]
	v_mfma_f32_16x16x32_bf16 v[4:7], v[180:183], v[238:241], v[4:7]
	s_setprio 0
	s_barrier
	s_add_i32 s48, s48, 2
	s_add_u32 s46, s46, 0x100
	s_addc_u32 s47, s47, 0
	s_add_u32 s22, s22, 0x100
	s_addc_u32 s23, s23, 0
	s_cmp_gt_u32 s48, 13
	s_cbranch_scc1 .Lpeel_exit_4

; #define PG8_BAR __builtin_amdgcn_s_barrier()
; template <class Epi, class Sched, bool ALIGN_EPI = false, bool SP2 = false>
; __device__ __forceinline__ void gemm_phase(PG8_LAS unsigned char* lds, const Gemm g, const Sched& S, const Epi& E) {
;     ...
;         if constexpr (ALIGN_EPI) { if (wr == 0) PG8_BAR; }
;         if constexpr (!Epi::AFTER_DRAIN) { E(acc, cur, wr, wc, fr, fq); S.done(cur); }
.Lpeel_exit_4:
	s_and_b64 vcc, exec, s[12:13]
	s_cbranch_vccz .LBB0_1164
	s_barrier

; #define PG8_STR(x) PG8_STR2(x)
; #define PG8_STAGE(bufoff, gbase, voff) do { _Pragma("unroll") for (int _i = 0; _i < 2; ++_i) \
;         __builtin_amdgcn_global_load_lds((const unsigned*)((const char*)(gbase) + (voff)[_i]), (PG8_LAS unsigned*)(lds + (bufoff) + ldsw + _i * 8192), 16, 0, 0); } while (0)
; #define PG8_LDA(dst, b, h) do { _Pragma("unroll") for (int m = 0; m < 4; ++m) _Pragma("unroll") for (int k = 0; k < 2; ++k) dst[m][k] = *(const PG8_LAS bf16x8*)(lds + PG8_SA(b, h) + aoff + m * 2048 + k * 1024); } while (0)
; #define PG8_LDB(dst, b, h) do { _Pragma("unroll") for (int n = 0; n < 2; ++n) _Pragma("unroll") for (int k = 0; k < 2; ++k) dst[n][k] = *(const PG8_LAS bf16x8*)(lds + PG8_SB(b, h) + boff + n * 2048 + k * 1024); } while (0)
; #define PG8_MMA(ai, bj, At, Bt) do { __builtin_amdgcn_s_setprio(1); _Pragma("unroll") for (int m = 0; m < 4; ++m) _Pragma("unroll") for (int n = 0; n < 2; ++n) _Pragma("unroll") for (int k = 0; k < 2; ++k) \
;         acc[ai][bj][m][n] = __builtin_amdgcn_mfma_f32_16x16x32_bf16(Bt[n][k], At[m][k], acc[ai][bj][m][n], 0, 0, 0); __builtin_amdgcn_s_setprio(0); } while (0)
; template <class Epi, class Sched, bool ALIGN_EPI = false, bool SP2 = false>
; __device__ __forceinline__ void gemm_phase(PG8_LAS unsigned char* lds, const Gemm g, const Sched& S, const Epi& E) {
;     ...
;         for (int t = 0; t < nt; t += 2) {
;     ...
;             asm volatile(".p2align 6\n\t.rept " PG8_STR(KLOOP_ALIGN) "\n\ts_nop 0\n\t.endr");
;     ...
;             const bool last = (t == nt - 2);
;             const char* a1 = cA + (size_t)(t + 1) * kstep;
;             const char* a2 = last ? nA : cA + (size_t)(t + 2) * kstep; const char* b2 = last ? nB : cB + (size_t)(t + 2) * kstep;
;             const char* a3 = a2 + kstep; const char* b3 = b2 + kstep;
;             if (last && has_next) S.a_ready(nxt);
;             if constexpr (SP2) {
;             PG8_LDB(B0, 0, 0); PG8_LDB(B1, 0, 1); PG8_SCHED; PG8_LDA(At, 0, 0); PG8_STAGE(PG8_SA(1, 1), a1 + hstepA, voffA);
;             PG8_WAIT_V(8); PG8_WAIT_L(0); PG8_BAR; PG8_MMA(0, 0, At, B0); PG8_MMA(0, 1, At, B1); PG8_BAR; PG8_SCHED;
;             PG8_LDA(At, 0, 1); PG8_STAGE(PG8_SB(0, 0), b2, voffB); PG8_STAGE(PG8_SB(0, 1), b2 + hstepB, voffB); PG8_STAGE(PG8_SA(0, 0), a2, voffA);
;             PG8_WAIT_V(8); PG8_WAIT_L(0); PG8_BAR; PG8_MMA(1, 0, At, B0); PG8_MMA(1, 1, At, B1); PG8_BAR; PG8_SCHED;
.LBB0_1692:
	s_ashr_i32 s13, s12, 31
	s_lshl_b64 s[16:17], s[12:13], 19
	s_add_u32 s16, s27, s16
	s_addc_u32 s17, s28, s17
	s_and_b64 s[18:19], s[2:3], exec
	s_cselect_b32 s13, s17, s23
	s_cselect_b32 s41, s16, s22
	s_ashr_i32 s11, s10, 31
	s_lshl_b64 s[18:19], s[10:11], 19
	s_add_u32 s18, s29, s18
	s_addc_u32 s19, s30, s19
	s_and_b64 s[24:25], s[2:3], exec
	s_cselect_b32 s11, s19, s21
	s_cselect_b32 s42, s18, s20
	s_add_u32 s43, s20, 0x100
	s_addc_u32 s44, s21, 0
	s_add_u32 s20, s22, 0x40080
	s_addc_u32 s21, s23, 0
	s_mov_b32 s45, -2
	s_add_u32 s22, s20, 0xfffc0080
	s_addc_u32 s23, s21, -1
	s_add_i32 s46, 0, 0x10000
	s_cmp_eq_u32 s45, 12
	s_cselect_b32 s25, s13, s23
	s_cselect_b32 s24, s41, s22
	v_add_u32_e32 v144, s46, v146
	s_cselect_b32 s23, s11, s44
	s_cselect_b32 s22, s42, s43
	s_add_i32 s48, 0, 0x14000
	ds_read_b128 v[150:153], v144
	ds_read_b128 v[154:157], v144 offset:1024
	ds_read_b128 v[158:161], v144 offset:2048
	ds_read_b128 v[162:165], v144 offset:3072
	v_add_u32_e32 v144, s48, v146
	ds_read_b128 v[166:169], v144
	ds_read_b128 v[170:173], v144 offset:1024
	ds_read_b128 v[174:177], v144 offset:2048
	ds_read_b128 v[178:181], v144 offset:3072
	v_lshl_add_u64 v[144:145], s[20:21], 0, v[142:143]
	s_add_i32 m0, s15, 0xc000
	ds_read_b128 v[182:185], v148
	ds_read_b128 v[186:189], v148 offset:1024
	ds_read_b128 v[190:193], v148 offset:2048
	ds_read_b128 v[194:197], v148 offset:3072
	ds_read_b128 v[210:213], v148 offset:4096
	ds_read_b128 v[226:229], v148 offset:5120
	ds_read_b128 v[230:233], v148 offset:6144
	ds_read_b128 v[234:237], v148 offset:7168
	v_lshl_add_u64 v[244:245], v[240:241], 0, s[64:65]
	s_mov_b32 m0, s36
	s_nop 0
	global_load_lds_dwordx4 v[244:245], off
	v_lshl_add_u64 v[244:245], v[242:243], 0, s[64:65]
	s_mov_b32 m0, s37
	s_nop 0
	global_load_lds_dwordx4 v[244:245], off
	s_add_i32 m0, s15, 0xc000
	s_nop 0
	global_load_lds_dwordx4 v[144:145], off
	v_lshl_add_u64 v[144:145], s[20:21], 0, v[140:141]
	s_add_i32 m0, s15, 0xe000
	s_nop 0
	global_load_lds_dwordx4 v[144:145], off
	s_waitcnt vmcnt(8)
	s_waitcnt lgkmcnt(0)
	s_barrier
	s_setprio 1
	s_waitcnt lgkmcnt(0)
	v_mfma_f32_16x16x32_bf16 v[128:131], v[150:153], v[182:185], 0
	v_mfma_f32_16x16x32_bf16 v[124:127], v[158:161], v[182:185], 0
	v_mfma_f32_16x16x32_bf16 v[120:123], v[150:153], v[190:193], 0
	v_mfma_f32_16x16x32_bf16 v[112:115], v[158:161], v[190:193], 0
	v_mfma_f32_16x16x32_bf16 v[104:107], v[150:153], v[210:213], 0
	v_mfma_f32_16x16x32_bf16 v[96:99], v[158:161], v[210:213], 0
	v_mfma_f32_16x16x32_bf16 v[88:91], v[150:153], v[230:233], 0
	v_mfma_f32_16x16x32_bf16 v[80:83], v[158:161], v[230:233], 0
	v_mfma_f32_16x16x32_bf16 v[128:131], v[154:157], v[186:189], v[128:131]
	v_mfma_f32_16x16x32_bf16 v[124:127], v[162:165], v[186:189], v[124:127]
	v_mfma_f32_16x16x32_bf16 v[120:123], v[154:157], v[194:197], v[120:123]
	v_mfma_f32_16x16x32_bf16 v[112:115], v[162:165], v[194:197], v[112:115]
	v_mfma_f32_16x16x32_bf16 v[104:107], v[154:157], v[226:229], v[104:107]
	v_mfma_f32_16x16x32_bf16 v[96:99], v[162:165], v[226:229], v[96:99]
	v_mfma_f32_16x16x32_bf16 v[88:91], v[154:157], v[234:237], v[88:91]
	v_mfma_f32_16x16x32_bf16 v[80:83], v[162:165], v[234:237], v[80:83]
	s_setprio 0
	s_setprio 1
	v_mfma_f32_16x16x32_bf16 v[116:119], v[166:169], v[182:185], 0
	v_mfma_f32_16x16x32_bf16 v[108:111], v[174:177], v[182:185], 0
	v_mfma_f32_16x16x32_bf16 v[100:103], v[166:169], v[190:193], 0
	v_mfma_f32_16x16x32_bf16 v[92:95], v[174:177], v[190:193], 0
	v_mfma_f32_16x16x32_bf16 v[84:87], v[166:169], v[210:213], 0
	v_mfma_f32_16x16x32_bf16 v[76:79], v[174:177], v[210:213], 0
	v_mfma_f32_16x16x32_bf16 v[72:75], v[166:169], v[230:233], 0
	v_mfma_f32_16x16x32_bf16 v[68:71], v[174:177], v[230:233], 0
	v_mfma_f32_16x16x32_bf16 v[116:119], v[170:173], v[186:189], v[116:119]
	v_mfma_f32_16x16x32_bf16 v[108:111], v[178:181], v[186:189], v[108:111]
	v_mfma_f32_16x16x32_bf16 v[100:103], v[170:173], v[194:197], v[100:103]
	v_mfma_f32_16x16x32_bf16 v[92:95], v[178:181], v[194:197], v[92:95]
	v_mfma_f32_16x16x32_bf16 v[84:87], v[170:173], v[226:229], v[84:87]
	v_mfma_f32_16x16x32_bf16 v[76:79], v[178:181], v[226:229], v[76:79]
	v_mfma_f32_16x16x32_bf16 v[72:75], v[170:173], v[234:237], v[72:75]
	v_mfma_f32_16x16x32_bf16 v[68:71], v[178:181], v[234:237], v[68:71]
	s_setprio 0
	s_barrier
	s_add_i32 s46, s46, s31
	v_lshl_add_u64 v[144:145], s[22:23], 0, v[134:135]
	s_mov_b32 m0, s46
	ds_read_b128 v[182:185], v148 offset:16384
	ds_read_b128 v[186:189], v148 offset:17408
	ds_read_b128 v[190:193], v148 offset:18432
	ds_read_b128 v[194:197], v148 offset:19456
	ds_read_b128 v[210:213], v148 offset:20480
	ds_read_b128 v[226:229], v148 offset:21504
	ds_read_b128 v[230:233], v148 offset:22528
	ds_read_b128 v[234:237], v148 offset:23552
	global_load_lds_dwordx4 v[144:145], off
	s_add_i32 m0, s46, 0x2000
	s_add_u32 s46, s22, 0x40000
	v_lshl_add_u64 v[238:239], s[22:23], 0, v[138:139]
	s_addc_u32 s47, s23, 0
	s_add_i32 s48, s48, s31
	global_load_lds_dwordx4 v[238:239], off
	v_lshl_add_u64 v[240:241], s[46:47], 0, v[134:135]
	s_mov_b32 m0, s48
	v_lshl_add_u64 v[242:243], s[24:25], 0, v[136:137]
	global_load_lds_dwordx4 v[240:241], off
	v_lshl_add_u64 v[240:241], s[46:47], 0, v[138:139]
	s_add_i32 m0, s48, 0x2000
	s_nop 0
	global_load_lds_dwordx4 v[240:241], off
	v_lshl_add_u64 v[240:241], s[24:25], 0, v[132:133]
	s_waitcnt vmcnt(6)
	s_waitcnt lgkmcnt(0)
	s_barrier
; #define PG8_STAGE(bufoff, gbase, voff) do { _Pragma("unroll") for (int _i = 0; _i < 2; ++_i) \
;         __builtin_amdgcn_global_load_lds((const unsigned*)((const char*)(gbase) + (voff)[_i]), (PG8_LAS unsigned*)(lds + (bufoff) + ldsw + _i * 8192), 16, 0, 0); } while (0)
; #define PG8_LDA(dst, b, h) do { _Pragma("unroll") for (int m = 0; m < 4; ++m) _Pragma("unroll") for (int k = 0; k < 2; ++k) dst[m][k] = *(const PG8_LAS bf16x8*)(lds + PG8_SA(b, h) + aoff + m * 2048 + k * 1024); } while (0)
; #define PG8_LDB(dst, b, h) do { _Pragma("unroll") for (int n = 0; n < 2; ++n) _Pragma("unroll") for (int k = 0; k < 2; ++k) dst[n][k] = *(const PG8_LAS bf16x8*)(lds + PG8_SB(b, h) + boff + n * 2048 + k * 1024); } while (0)
; #define PG8_MMA(ai, bj, At, Bt) do { __builtin_amdgcn_s_setprio(1); _Pragma("unroll") for (int m = 0; m < 4; ++m) _Pragma("unroll") for (int n = 0; n < 2; ++n) _Pragma("unroll") for (int k = 0; k < 2; ++k) \
;         acc[ai][bj][m][n] = __builtin_amdgcn_mfma_f32_16x16x32_bf16(Bt[n][k], At[m][k], acc[ai][bj][m][n], 0, 0, 0); __builtin_amdgcn_s_setprio(0); } while (0)
; #define PG8_WAIT_V(n) asm volatile("s_waitcnt vmcnt(" #n ")" ::: "memory")
; #define PG8_WAIT_L(n) asm volatile("s_waitcnt lgkmcnt(" #n ")" ::: "memory")
; #define PG8_BAR __builtin_amdgcn_s_barrier()
; #define PG8_SCHED __builtin_amdgcn_sched_barrier(0)
; template <class Epi, class Sched, bool ALIGN_EPI = false, bool SP2 = false>
; __device__ __forceinline__ void gemm_phase(PG8_LAS unsigned char* lds, const Gemm g, const Sched& S, const Epi& E) {
;     ...
;             PG8_LDA(At, 0, 1); PG8_STAGE(PG8_SB(0, 0), b2, voffB); PG8_STAGE(PG8_SB(0, 1), b2 + hstepB, voffB); PG8_STAGE(PG8_SA(0, 0), a2, voffA);
;             PG8_WAIT_V(8); PG8_WAIT_L(0); PG8_BAR; PG8_MMA(1, 0, At, B0); PG8_MMA(1, 1, At, B1); PG8_BAR; PG8_SCHED;
;             PG8_LDB(B0, 1, 0); PG8_LDB(B1, 1, 1); PG8_SCHED; PG8_LDA(At, 1, 0); PG8_STAGE(PG8_SA(0, 1), a2 + hstepA, voffA);
;             PG8_WAIT_V(8); PG8_WAIT_L(0); PG8_BAR; PG8_MMA(0, 0, At, B0); PG8_MMA(0, 1, At, B1); PG8_BAR; PG8_SCHED;
	s_setprio 1
	s_waitcnt lgkmcnt(0)
	v_mfma_f32_16x16x32_bf16 v[64:67], v[150:153], v[182:185], 0
	v_mfma_f32_16x16x32_bf16 v[60:63], v[158:161], v[182:185], 0
	v_mfma_f32_16x16x32_bf16 v[56:59], v[150:153], v[190:193], 0
	v_mfma_f32_16x16x32_bf16 v[48:51], v[158:161], v[190:193], 0
	v_mfma_f32_16x16x32_bf16 v[40:43], v[150:153], v[210:213], 0
	v_mfma_f32_16x16x32_bf16 v[32:35], v[158:161], v[210:213], 0
	v_mfma_f32_16x16x32_bf16 v[24:27], v[150:153], v[230:233], 0
	v_mfma_f32_16x16x32_bf16 v[16:19], v[158:161], v[230:233], 0
	v_mfma_f32_16x16x32_bf16 v[64:67], v[154:157], v[186:189], v[64:67]
	v_mfma_f32_16x16x32_bf16 v[60:63], v[162:165], v[186:189], v[60:63]
	v_mfma_f32_16x16x32_bf16 v[56:59], v[154:157], v[194:197], v[56:59]
	v_mfma_f32_16x16x32_bf16 v[48:51], v[162:165], v[194:197], v[48:51]
	v_mfma_f32_16x16x32_bf16 v[40:43], v[154:157], v[226:229], v[40:43]
	v_mfma_f32_16x16x32_bf16 v[32:35], v[162:165], v[226:229], v[32:35]
	v_mfma_f32_16x16x32_bf16 v[24:27], v[154:157], v[234:237], v[24:27]
	v_mfma_f32_16x16x32_bf16 v[16:19], v[162:165], v[234:237], v[16:19]
	s_setprio 0
	s_setprio 1
	v_mfma_f32_16x16x32_bf16 v[52:55], v[166:169], v[182:185], 0
	v_mfma_f32_16x16x32_bf16 v[44:47], v[174:177], v[182:185], 0
	v_mfma_f32_16x16x32_bf16 v[36:39], v[166:169], v[190:193], 0
	v_mfma_f32_16x16x32_bf16 v[28:31], v[174:177], v[190:193], 0
	v_mfma_f32_16x16x32_bf16 v[20:23], v[166:169], v[210:213], 0
	v_mfma_f32_16x16x32_bf16 v[12:15], v[174:177], v[210:213], 0
	v_mfma_f32_16x16x32_bf16 v[8:11], v[166:169], v[230:233], 0
	v_mfma_f32_16x16x32_bf16 v[4:7], v[174:177], v[230:233], 0
	v_mfma_f32_16x16x32_bf16 v[52:55], v[170:173], v[186:189], v[52:55]
	v_mfma_f32_16x16x32_bf16 v[44:47], v[178:181], v[186:189], v[44:47]
	v_mfma_f32_16x16x32_bf16 v[36:39], v[170:173], v[194:197], v[36:39]
	v_mfma_f32_16x16x32_bf16 v[28:31], v[178:181], v[194:197], v[28:31]
	v_mfma_f32_16x16x32_bf16 v[20:23], v[170:173], v[226:229], v[20:23]
	v_mfma_f32_16x16x32_bf16 v[12:15], v[178:181], v[226:229], v[12:15]
	v_mfma_f32_16x16x32_bf16 v[8:11], v[170:173], v[234:237], v[8:11]
	v_mfma_f32_16x16x32_bf16 v[4:7], v[178:181], v[234:237], v[4:7]
	s_setprio 0
	s_barrier
	s_add_i32 s46, 0, 0x18000
	v_add_u32_e32 v149, s46, v146
	s_add_i32 s47, 0, 0x1c000
	ds_read_b128 v[150:153], v149
	ds_read_b128 v[154:157], v149 offset:1024
	ds_read_b128 v[158:161], v149 offset:2048
	ds_read_b128 v[162:165], v149 offset:3072
	v_add_u32_e32 v149, s47, v146
	ds_read_b128 v[166:169], v149
	ds_read_b128 v[170:173], v149 offset:1024
	ds_read_b128 v[174:177], v149 offset:2048
	ds_read_b128 v[178:181], v149 offset:3072
	s_add_u32 s24, s24, 0x40000
	s_addc_u32 s25, s25, 0
	s_mov_b32 m0, s34
	v_lshl_add_u64 v[244:245], s[24:25], 0, v[132:133]
	ds_read_b128 v[182:185], v148 offset:32768
	ds_read_b128 v[186:189], v148 offset:33792
	ds_read_b128 v[190:193], v148 offset:34816
	ds_read_b128 v[194:197], v148 offset:35840
	ds_read_b128 v[210:213], v148 offset:36864
	ds_read_b128 v[226:229], v148 offset:37888
	ds_read_b128 v[230:233], v148 offset:38912
	ds_read_b128 v[234:237], v148 offset:39936
	s_mov_b32 m0, s15
	s_nop 0
	global_load_lds_dwordx4 v[240:241], off
	s_mov_b32 m0, s33
	s_nop 0
	global_load_lds_dwordx4 v[242:243], off
	s_mov_b32 m0, s34
	s_nop 0
	global_load_lds_dwordx4 v[244:245], off
	v_lshl_add_u64 v[244:245], s[24:25], 0, v[136:137]
	s_mov_b32 m0, s35
	s_nop 0
	global_load_lds_dwordx4 v[244:245], off
	s_waitcnt vmcnt(8)
	s_waitcnt lgkmcnt(0)
	s_barrier
; #define PG8_STAGE(bufoff, gbase, voff) do { _Pragma("unroll") for (int _i = 0; _i < 2; ++_i) \
;         __builtin_amdgcn_global_load_lds((const unsigned*)((const char*)(gbase) + (voff)[_i]), (PG8_LAS unsigned*)(lds + (bufoff) + ldsw + _i * 8192), 16, 0, 0); } while (0)
; #define PG8_LDA(dst, b, h) do { _Pragma("unroll") for (int m = 0; m < 4; ++m) _Pragma("unroll") for (int k = 0; k < 2; ++k) dst[m][k] = *(const PG8_LAS bf16x8*)(lds + PG8_SA(b, h) + aoff + m * 2048 + k * 1024); } while (0)
; #define PG8_LDB(dst, b, h) do { _Pragma("unroll") for (int n = 0; n < 2; ++n) _Pragma("unroll") for (int k = 0; k < 2; ++k) dst[n][k] = *(const PG8_LAS bf16x8*)(lds + PG8_SB(b, h) + boff + n * 2048 + k * 1024); } while (0)
; #define PG8_MMA(ai, bj, At, Bt) do { __builtin_amdgcn_s_setprio(1); _Pragma("unroll") for (int m = 0; m < 4; ++m) _Pragma("unroll") for (int n = 0; n < 2; ++n) _Pragma("unroll") for (int k = 0; k < 2; ++k) \
;         acc[ai][bj][m][n] = __builtin_amdgcn_mfma_f32_16x16x32_bf16(Bt[n][k], At[m][k], acc[ai][bj][m][n], 0, 0, 0); __builtin_amdgcn_s_setprio(0); } while (0)
; #define PG8_WAIT_V(n) asm volatile("s_waitcnt vmcnt(" #n ")" ::: "memory")
; #define PG8_WAIT_L(n) asm volatile("s_waitcnt lgkmcnt(" #n ")" ::: "memory")
; #define PG8_BAR __builtin_amdgcn_s_barrier()
; #define PG8_SCHED __builtin_amdgcn_sched_barrier(0)
; template <class Epi, class Sched, bool ALIGN_EPI = false, bool SP2 = false>
; __device__ __forceinline__ void gemm_phase(PG8_LAS unsigned char* lds, const Gemm g, const Sched& S, const Epi& E) {
;     ...
;             PG8_LDB(B0, 1, 0); PG8_LDB(B1, 1, 1); PG8_SCHED; PG8_LDA(At, 1, 0); PG8_STAGE(PG8_SA(0, 1), a2 + hstepA, voffA);
;             PG8_WAIT_V(8); PG8_WAIT_L(0); PG8_BAR; PG8_MMA(0, 0, At, B0); PG8_MMA(0, 1, At, B1); PG8_BAR; PG8_SCHED;
;             PG8_LDA(At, 1, 1); PG8_STAGE(PG8_SB(1, 0), b3, voffB); PG8_STAGE(PG8_SB(1, 1), b3 + hstepB, voffB); PG8_STAGE(PG8_SA(1, 0), a3, voffA);
;             PG8_WAIT_V(8); PG8_WAIT_L(0); PG8_BAR; PG8_MMA(1, 0, At, B0); PG8_MMA(1, 1, At, B1); PG8_BAR; PG8_SCHED;
	s_setprio 1
	s_waitcnt lgkmcnt(0)
	v_mfma_f32_16x16x32_bf16 v[128:131], v[150:153], v[182:185], v[128:131]
	v_mfma_f32_16x16x32_bf16 v[124:127], v[158:161], v[182:185], v[124:127]
	v_mfma_f32_16x16x32_bf16 v[120:123], v[150:153], v[190:193], v[120:123]
	v_mfma_f32_16x16x32_bf16 v[112:115], v[158:161], v[190:193], v[112:115]
	v_mfma_f32_16x16x32_bf16 v[104:107], v[150:153], v[210:213], v[104:107]
	v_mfma_f32_16x16x32_bf16 v[96:99], v[158:161], v[210:213], v[96:99]
	v_mfma_f32_16x16x32_bf16 v[88:91], v[150:153], v[230:233], v[88:91]
	v_mfma_f32_16x16x32_bf16 v[80:83], v[158:161], v[230:233], v[80:83]
	v_mfma_f32_16x16x32_bf16 v[128:131], v[154:157], v[186:189], v[128:131]
	v_mfma_f32_16x16x32_bf16 v[124:127], v[162:165], v[186:189], v[124:127]
	v_mfma_f32_16x16x32_bf16 v[120:123], v[154:157], v[194:197], v[120:123]
	v_mfma_f32_16x16x32_bf16 v[112:115], v[162:165], v[194:197], v[112:115]
	v_mfma_f32_16x16x32_bf16 v[104:107], v[154:157], v[226:229], v[104:107]
	v_mfma_f32_16x16x32_bf16 v[96:99], v[162:165], v[226:229], v[96:99]
	v_mfma_f32_16x16x32_bf16 v[88:91], v[154:157], v[234:237], v[88:91]
	v_mfma_f32_16x16x32_bf16 v[80:83], v[162:165], v[234:237], v[80:83]
	s_setprio 0
	s_setprio 1
	v_mfma_f32_16x16x32_bf16 v[116:119], v[166:169], v[182:185], v[116:119]
	v_mfma_f32_16x16x32_bf16 v[108:111], v[174:177], v[182:185], v[108:111]
	v_mfma_f32_16x16x32_bf16 v[100:103], v[166:169], v[190:193], v[100:103]
	v_mfma_f32_16x16x32_bf16 v[92:95], v[174:177], v[190:193], v[92:95]
	v_mfma_f32_16x16x32_bf16 v[84:87], v[166:169], v[210:213], v[84:87]
	v_mfma_f32_16x16x32_bf16 v[76:79], v[174:177], v[210:213], v[76:79]
	v_mfma_f32_16x16x32_bf16 v[72:75], v[166:169], v[230:233], v[72:75]
	v_mfma_f32_16x16x32_bf16 v[68:71], v[174:177], v[230:233], v[68:71]
	v_mfma_f32_16x16x32_bf16 v[116:119], v[170:173], v[186:189], v[116:119]
	v_mfma_f32_16x16x32_bf16 v[108:111], v[178:181], v[186:189], v[108:111]
	v_mfma_f32_16x16x32_bf16 v[100:103], v[170:173], v[194:197], v[100:103]
	v_mfma_f32_16x16x32_bf16 v[92:95], v[178:181], v[194:197], v[92:95]
	v_mfma_f32_16x16x32_bf16 v[84:87], v[170:173], v[226:229], v[84:87]
	v_mfma_f32_16x16x32_bf16 v[76:79], v[178:181], v[226:229], v[76:79]
	v_mfma_f32_16x16x32_bf16 v[72:75], v[170:173], v[234:237], v[72:75]
	v_mfma_f32_16x16x32_bf16 v[68:71], v[178:181], v[234:237], v[68:71]
	s_setprio 0
	s_barrier
	s_add_i32 s24, s46, s31
	v_lshl_add_u64 v[144:145], v[144:145], 0, s[64:65]
	s_mov_b32 m0, s24
	ds_read_b128 v[182:185], v148 offset:49152
	ds_read_b128 v[186:189], v148 offset:50176
	ds_read_b128 v[190:193], v148 offset:51200
	ds_read_b128 v[194:197], v148 offset:52224
	ds_read_b128 v[210:213], v148 offset:53248
	ds_read_b128 v[226:229], v148 offset:54272
	ds_read_b128 v[230:233], v148 offset:55296
	ds_read_b128 v[234:237], v148 offset:56320
	global_load_lds_dwordx4 v[144:145], off
	s_add_i32 m0, s24, 0x2000
	s_add_u32 s22, s22, 0x40080
	v_lshl_add_u64 v[144:145], v[238:239], 0, s[64:65]
	s_addc_u32 s23, s23, 0
	s_add_i32 s24, s47, s31
	global_load_lds_dwordx4 v[144:145], off
	v_lshl_add_u64 v[144:145], s[22:23], 0, v[134:135]
	s_mov_b32 m0, s24
	s_nop 0
	global_load_lds_dwordx4 v[144:145], off
	v_lshl_add_u64 v[144:145], s[22:23], 0, v[138:139]
	s_add_i32 m0, s24, 0x2000
	s_nop 0
	global_load_lds_dwordx4 v[144:145], off
	s_waitcnt vmcnt(6)
	s_waitcnt lgkmcnt(0)
	s_barrier
	s_setprio 1
	s_waitcnt lgkmcnt(0)
	v_mfma_f32_16x16x32_bf16 v[64:67], v[150:153], v[182:185], v[64:67]
	v_mfma_f32_16x16x32_bf16 v[60:63], v[158:161], v[182:185], v[60:63]
	v_mfma_f32_16x16x32_bf16 v[56:59], v[150:153], v[190:193], v[56:59]
	v_mfma_f32_16x16x32_bf16 v[48:51], v[158:161], v[190:193], v[48:51]
	v_mfma_f32_16x16x32_bf16 v[40:43], v[150:153], v[210:213], v[40:43]
	v_mfma_f32_16x16x32_bf16 v[32:35], v[158:161], v[210:213], v[32:35]
	v_mfma_f32_16x16x32_bf16 v[24:27], v[150:153], v[230:233], v[24:27]
	v_mfma_f32_16x16x32_bf16 v[16:19], v[158:161], v[230:233], v[16:19]
	v_mfma_f32_16x16x32_bf16 v[64:67], v[154:157], v[186:189], v[64:67]
	v_mfma_f32_16x16x32_bf16 v[60:63], v[162:165], v[186:189], v[60:63]
	v_mfma_f32_16x16x32_bf16 v[56:59], v[154:157], v[194:197], v[56:59]
	v_mfma_f32_16x16x32_bf16 v[48:51], v[162:165], v[194:197], v[48:51]
	v_mfma_f32_16x16x32_bf16 v[40:43], v[154:157], v[226:229], v[40:43]
	v_mfma_f32_16x16x32_bf16 v[32:35], v[162:165], v[226:229], v[32:35]
	v_mfma_f32_16x16x32_bf16 v[24:27], v[154:157], v[234:237], v[24:27]
	v_mfma_f32_16x16x32_bf16 v[16:19], v[162:165], v[234:237], v[16:19]
	s_setprio 0
	s_setprio 1
	v_mfma_f32_16x16x32_bf16 v[52:55], v[166:169], v[182:185], v[52:55]
	v_mfma_f32_16x16x32_bf16 v[44:47], v[174:177], v[182:185], v[44:47]
	v_mfma_f32_16x16x32_bf16 v[36:39], v[166:169], v[190:193], v[36:39]
	v_mfma_f32_16x16x32_bf16 v[28:31], v[174:177], v[190:193], v[28:31]
	v_mfma_f32_16x16x32_bf16 v[20:23], v[166:169], v[210:213], v[20:23]
	v_mfma_f32_16x16x32_bf16 v[12:15], v[174:177], v[210:213], v[12:15]
	v_mfma_f32_16x16x32_bf16 v[8:11], v[166:169], v[230:233], v[8:11]
	v_mfma_f32_16x16x32_bf16 v[4:7], v[174:177], v[230:233], v[4:7]
	v_mfma_f32_16x16x32_bf16 v[52:55], v[170:173], v[186:189], v[52:55]
	v_mfma_f32_16x16x32_bf16 v[44:47], v[178:181], v[186:189], v[44:47]
	v_mfma_f32_16x16x32_bf16 v[36:39], v[170:173], v[194:197], v[36:39]
	v_mfma_f32_16x16x32_bf16 v[28:31], v[178:181], v[194:197], v[28:31]
	v_mfma_f32_16x16x32_bf16 v[20:23], v[170:173], v[226:229], v[20:23]
	v_mfma_f32_16x16x32_bf16 v[12:15], v[178:181], v[226:229], v[12:15]
	v_mfma_f32_16x16x32_bf16 v[8:11], v[170:173], v[234:237], v[8:11]
	v_mfma_f32_16x16x32_bf16 v[4:7], v[178:181], v[234:237], v[4:7]
	s_setprio 0
	s_barrier
	s_add_i32 s45, s45, 2
	s_add_u32 s43, s43, 0x100
	s_addc_u32 s44, s44, 0
	s_add_u32 s20, s20, 0x100
	s_addc_u32 s21, s21, 0
	s_cmp_gt_u32 s45, 13
	s_cbranch_scc1 .Lpeel_exit_7

; #define PG8_BAR __builtin_amdgcn_s_barrier()
; template <class Epi, class Sched, bool ALIGN_EPI = false, bool SP2 = false>
; __device__ __forceinline__ void gemm_phase(PG8_LAS unsigned char* lds, const Gemm g, const Sched& S, const Epi& E) {
;     ...
;         if constexpr (ALIGN_EPI) { if (wr == 0) PG8_BAR; }
;         if constexpr (!Epi::AFTER_DRAIN) { E(acc, cur, wr, wc, fr, fq); S.done(cur); }
.Lpeel_exit_7:
	s_and_b64 vcc, exec, s[8:9]
	s_cbranch_vccz .LBB0_1696
	s_barrier
